# baseline (speedup 1.0000x reference)
.LBB7_26:
	s_lshl_b32 s34, s70, 8
	s_add_i32 s34, s34, s48
	v_or_b32_e32 v250, s34, v165
	v_ashrrev_i32_e32 v251, 31, v250
	v_lshl_add_u64 v[250:251], v[250:251], 3, s[12:13]
	s_lshl_b32 s35, s67, 8
	s_or_b32 s35, s35, s51
	v_or_b32_e32 v252, s35, v164
	v_ashrrev_i32_e32 v253, 31, v252
	v_lshl_add_u64 v[252:253], v[252:253], 2, s[14:15]
	global_load_dword v226, v[250:251], off offset:4
	global_load_dword v227, v[250:251], off offset:132
	global_load_dword v228, v[250:251], off offset:260
	global_load_dword v229, v[250:251], off offset:388
	global_load_dword v230, v[250:251], off offset:1028
	global_load_dword v231, v[250:251], off offset:1156
	global_load_dword v232, v[250:251], off offset:1284
	global_load_dword v233, v[250:251], off offset:1412
	global_load_dwordx4 v[234:237], v[252:253], off
	global_load_dwordx4 v[238:241], v[252:253], off offset:16
	global_load_dwordx4 v[242:245], v[252:253], off offset:128
	global_load_dwordx4 v[246:249], v[252:253], off offset:144
	s_add_u32 s28, s28, 0x30080
	s_addc_u32 s29, s29, 0
	s_add_u32 s71, s30, 0x100
	v_mov_b32_e32 v0, 0
	s_addc_u32 s72, s31, 0
	s_mov_b32 s73, -2
	v_mov_b32_e32 v1, v0
	v_mov_b32_e32 v2, v0
	v_mov_b32_e32 v3, v0
	v_mov_b32_e32 v4, v0
	v_mov_b32_e32 v5, v0
	v_mov_b32_e32 v6, v0
	v_mov_b32_e32 v7, v0
	v_mov_b32_e32 v12, v0
	v_mov_b32_e32 v13, v0
	v_mov_b32_e32 v14, v0
	v_mov_b32_e32 v15, v0
	v_mov_b32_e32 v20, v0
	v_mov_b32_e32 v21, v0
	v_mov_b32_e32 v22, v0
	v_mov_b32_e32 v23, v0
	v_mov_b32_e32 v28, v0
	v_mov_b32_e32 v29, v0
	v_mov_b32_e32 v30, v0
	v_mov_b32_e32 v31, v0
	v_mov_b32_e32 v36, v0
	v_mov_b32_e32 v37, v0
	v_mov_b32_e32 v38, v0
	v_mov_b32_e32 v39, v0
	v_mov_b32_e32 v44, v0
	v_mov_b32_e32 v45, v0
	v_mov_b32_e32 v46, v0
	v_mov_b32_e32 v47, v0
	v_mov_b32_e32 v52, v0
	v_mov_b32_e32 v53, v0
	v_mov_b32_e32 v54, v0
	v_mov_b32_e32 v55, v0
	v_mov_b32_e32 v8, v0
	v_mov_b32_e32 v9, v0
	v_mov_b32_e32 v10, v0
	v_mov_b32_e32 v11, v0
	v_mov_b32_e32 v16, v0
	v_mov_b32_e32 v17, v0
	v_mov_b32_e32 v18, v0
	v_mov_b32_e32 v19, v0
	v_mov_b32_e32 v24, v0
	v_mov_b32_e32 v25, v0
	v_mov_b32_e32 v26, v0
	v_mov_b32_e32 v27, v0
	v_mov_b32_e32 v32, v0
	v_mov_b32_e32 v33, v0
	v_mov_b32_e32 v34, v0
	v_mov_b32_e32 v35, v0
	v_mov_b32_e32 v40, v0
	v_mov_b32_e32 v41, v0
	v_mov_b32_e32 v42, v0
	v_mov_b32_e32 v43, v0
	v_mov_b32_e32 v48, v0
	v_mov_b32_e32 v49, v0
	v_mov_b32_e32 v50, v0
	v_mov_b32_e32 v51, v0
	v_mov_b32_e32 v56, v0
	v_mov_b32_e32 v57, v0
	v_mov_b32_e32 v58, v0
	v_mov_b32_e32 v59, v0
	v_mov_b32_e32 v60, v0
	v_mov_b32_e32 v61, v0
	v_mov_b32_e32 v62, v0
	v_mov_b32_e32 v63, v0
	v_mov_b32_e32 v64, v0
	v_mov_b32_e32 v65, v0
	v_mov_b32_e32 v66, v0
	v_mov_b32_e32 v67, v0
	v_mov_b32_e32 v68, v0
	v_mov_b32_e32 v69, v0
	v_mov_b32_e32 v70, v0
	v_mov_b32_e32 v71, v0
	v_mov_b32_e32 v76, v0
	v_mov_b32_e32 v77, v0
	v_mov_b32_e32 v78, v0
	v_mov_b32_e32 v79, v0
	v_mov_b32_e32 v84, v0
	v_mov_b32_e32 v85, v0
	v_mov_b32_e32 v86, v0
	v_mov_b32_e32 v87, v0
	v_mov_b32_e32 v92, v0
	v_mov_b32_e32 v93, v0
	v_mov_b32_e32 v94, v0
	v_mov_b32_e32 v95, v0
	v_mov_b32_e32 v100, v0
	v_mov_b32_e32 v101, v0
	v_mov_b32_e32 v102, v0
	v_mov_b32_e32 v103, v0
	v_mov_b32_e32 v112, v0
	v_mov_b32_e32 v113, v0
	v_mov_b32_e32 v114, v0
	v_mov_b32_e32 v115, v0
	v_mov_b32_e32 v116, v0
	v_mov_b32_e32 v117, v0
	v_mov_b32_e32 v118, v0
	v_mov_b32_e32 v119, v0
	v_mov_b32_e32 v72, v0
	v_mov_b32_e32 v73, v0
	v_mov_b32_e32 v74, v0
	v_mov_b32_e32 v75, v0
	v_mov_b32_e32 v80, v0
	v_mov_b32_e32 v81, v0
	v_mov_b32_e32 v82, v0
	v_mov_b32_e32 v83, v0
	v_mov_b32_e32 v88, v0
	v_mov_b32_e32 v89, v0
	v_mov_b32_e32 v90, v0
	v_mov_b32_e32 v91, v0
	v_mov_b32_e32 v96, v0
	v_mov_b32_e32 v97, v0
	v_mov_b32_e32 v98, v0
	v_mov_b32_e32 v99, v0
	v_mov_b32_e32 v104, v0
	v_mov_b32_e32 v105, v0
	v_mov_b32_e32 v106, v0
	v_mov_b32_e32 v107, v0
	v_mov_b32_e32 v108, v0
	v_mov_b32_e32 v109, v0
	v_mov_b32_e32 v110, v0
	v_mov_b32_e32 v111, v0
	v_mov_b32_e32 v120, v0
	v_mov_b32_e32 v121, v0
	v_mov_b32_e32 v122, v0
	v_mov_b32_e32 v123, v0
	v_mov_b32_e32 v124, v0
	v_mov_b32_e32 v125, v0
	v_mov_b32_e32 v126, v0
	v_mov_b32_e32 v127, v0
	ds_read_b128 v[128:131], v170
	ds_read_b128 v[132:135], v170 offset:1024
	ds_read_b128 v[136:139], v170 offset:2048
	ds_read_b128 v[140:143], v170 offset:3072
.LBB7_27:
	s_add_u32 s30, s28, 0xfffd0080
	s_addc_u32 s31, s29, -1
	s_cmp_eq_u32 s73, 8
	s_cselect_b32 s35, s9, s31
	s_cselect_b32 s34, s8, s30
	s_cselect_b32 s31, s1, s72
	s_cselect_b32 s30, s0, s71
	s_add_i32 m0, s43, 0xc000
	ds_read_b128 v[158:161], v171
	ds_read_b128 v[176:179], v171 offset:1024
	ds_read_b128 v[180:183], v171 offset:2048
	ds_read_b128 v[184:187], v171 offset:3072
	ds_read_b128 v[188:191], v171 offset:4096
	ds_read_b128 v[192:195], v171 offset:5120
	ds_read_b128 v[196:199], v171 offset:6144
	ds_read_b128 v[200:203], v171 offset:7168
	global_load_lds_dwordx4 v152, s[28:29]
	s_add_i32 m0, s43, 0xe000
	s_nop 0
	global_load_lds_dwordx4 v154, s[28:29]
	s_waitcnt lgkmcnt(8)
	s_barrier
	s_waitcnt lgkmcnt(0)
	v_mfma_f32_16x16x32_f16 v[124:127], v[128:131], v[158:161], v[124:127]
	v_mfma_f32_16x16x32_f16 v[120:123], v[136:139], v[158:161], v[120:123]
	v_mfma_f32_16x16x32_f16 v[108:111], v[128:131], v[180:183], v[108:111]
	v_mfma_f32_16x16x32_f16 v[104:107], v[136:139], v[180:183], v[104:107]
	v_mfma_f32_16x16x32_f16 v[96:99], v[128:131], v[188:191], v[96:99]
	v_mfma_f32_16x16x32_f16 v[88:91], v[136:139], v[188:191], v[88:91]
	v_mfma_f32_16x16x32_f16 v[80:83], v[128:131], v[196:199], v[80:83]
	v_mfma_f32_16x16x32_f16 v[72:75], v[136:139], v[196:199], v[72:75]
	v_mfma_f32_16x16x32_f16 v[124:127], v[132:135], v[176:179], v[124:127]
	v_mfma_f32_16x16x32_f16 v[120:123], v[140:143], v[176:179], v[120:123]
	v_mfma_f32_16x16x32_f16 v[108:111], v[132:135], v[184:187], v[108:111]
	v_mfma_f32_16x16x32_f16 v[104:107], v[140:143], v[184:187], v[104:107]
	v_mfma_f32_16x16x32_f16 v[96:99], v[132:135], v[192:195], v[96:99]
	v_mfma_f32_16x16x32_f16 v[88:91], v[140:143], v[192:195], v[88:91]
	v_mfma_f32_16x16x32_f16 v[80:83], v[132:135], v[200:203], v[80:83]
	v_mfma_f32_16x16x32_f16 v[72:75], v[140:143], v[200:203], v[72:75]
	s_barrier
	s_add_i32 s74, s65, s42
	s_add_u32 s78, s30, 0x80
	s_addc_u32 s79, s31, 0
	s_mov_b32 m0, s74
	ds_read_b128 v[204:207], v172
	ds_read_b128 v[208:211], v172 offset:1024
	ds_read_b128 v[212:215], v172 offset:2048
	ds_read_b128 v[216:219], v172 offset:3072
	global_load_lds_dwordx4 v146, s[30:31]
	s_add_i32 m0, s74, 0x2000
	s_nop 0
	global_load_lds_dwordx4 v150, s[30:31]
	s_barrier
	s_waitcnt lgkmcnt(0)
	v_mfma_f32_16x16x32_f16 v[116:119], v[204:207], v[158:161], v[116:119]
	v_mfma_f32_16x16x32_f16 v[112:115], v[212:215], v[158:161], v[112:115]
	v_mfma_f32_16x16x32_f16 v[100:103], v[204:207], v[180:183], v[100:103]
	v_mfma_f32_16x16x32_f16 v[92:95], v[212:215], v[180:183], v[92:95]
	v_mfma_f32_16x16x32_f16 v[84:87], v[204:207], v[188:191], v[84:87]
	v_mfma_f32_16x16x32_f16 v[76:79], v[212:215], v[188:191], v[76:79]
	v_mfma_f32_16x16x32_f16 v[68:71], v[204:207], v[196:199], v[68:71]
	v_mfma_f32_16x16x32_f16 v[64:67], v[212:215], v[196:199], v[64:67]
	v_mfma_f32_16x16x32_f16 v[116:119], v[208:211], v[176:179], v[116:119]
	v_mfma_f32_16x16x32_f16 v[112:115], v[216:219], v[176:179], v[112:115]
	v_mfma_f32_16x16x32_f16 v[100:103], v[208:211], v[184:187], v[100:103]
	v_mfma_f32_16x16x32_f16 v[92:95], v[216:219], v[184:187], v[92:95]
	v_mfma_f32_16x16x32_f16 v[84:87], v[208:211], v[192:195], v[84:87]
	v_mfma_f32_16x16x32_f16 v[76:79], v[216:219], v[192:195], v[76:79]
	v_mfma_f32_16x16x32_f16 v[68:71], v[208:211], v[200:203], v[68:71]
	v_mfma_f32_16x16x32_f16 v[64:67], v[216:219], v[200:203], v[64:67]
	s_barrier
	s_mov_b32 m0, s43
	s_add_u32 s80, s34, 0x80
	s_addc_u32 s81, s35, 0
	ds_read_b128 v[158:161], v171 offset:16384
	ds_read_b128 v[176:179], v171 offset:17408
	ds_read_b128 v[180:183], v171 offset:18432
	ds_read_b128 v[184:187], v171 offset:19456
	ds_read_b128 v[188:191], v171 offset:20480
	ds_read_b128 v[192:195], v171 offset:21504
	ds_read_b128 v[196:199], v171 offset:22528
	ds_read_b128 v[200:203], v171 offset:23552
	global_load_lds_dwordx4 v144, s[34:35]
	s_mov_b32 m0, s44
	s_nop 0
	global_load_lds_dwordx4 v148, s[34:35]
	s_waitcnt vmcnt(10)
	s_barrier
	s_waitcnt lgkmcnt(0)
	v_mfma_f32_16x16x32_f16 v[60:63], v[128:131], v[158:161], v[60:63]
	v_mfma_f32_16x16x32_f16 v[56:59], v[136:139], v[158:161], v[56:59]
	v_mfma_f32_16x16x32_f16 v[48:51], v[128:131], v[180:183], v[48:51]
	v_mfma_f32_16x16x32_f16 v[40:43], v[136:139], v[180:183], v[40:43]
	v_mfma_f32_16x16x32_f16 v[32:35], v[128:131], v[188:191], v[32:35]
	v_mfma_f32_16x16x32_f16 v[24:27], v[136:139], v[188:191], v[24:27]
	v_mfma_f32_16x16x32_f16 v[16:19], v[128:131], v[196:199], v[16:19]
	v_mfma_f32_16x16x32_f16 v[8:11], v[136:139], v[196:199], v[8:11]
	v_mfma_f32_16x16x32_f16 v[60:63], v[132:135], v[176:179], v[60:63]
	v_mfma_f32_16x16x32_f16 v[56:59], v[140:143], v[176:179], v[56:59]
	v_mfma_f32_16x16x32_f16 v[48:51], v[132:135], v[184:187], v[48:51]
	v_mfma_f32_16x16x32_f16 v[40:43], v[140:143], v[184:187], v[40:43]
	v_mfma_f32_16x16x32_f16 v[32:35], v[132:135], v[192:195], v[32:35]
	v_mfma_f32_16x16x32_f16 v[24:27], v[140:143], v[192:195], v[24:27]
	v_mfma_f32_16x16x32_f16 v[16:19], v[132:135], v[200:203], v[16:19]
	v_mfma_f32_16x16x32_f16 v[8:11], v[140:143], v[200:203], v[8:11]
	s_barrier
	s_add_u32 s74, s30, 0xc000
	s_addc_u32 s75, s31, 0
	s_add_i32 s76, s66, s42
	s_mov_b32 m0, s76
	s_nop 0
	global_load_lds_dwordx4 v146, s[74:75]
	s_add_i32 m0, s76, 0x2000
	s_nop 0
	global_load_lds_dwordx4 v150, s[74:75]
	s_add_i32 s74, 0, 0x18000
	v_add_u32_e32 v140, s74, v166
	ds_read_b128 v[128:131], v140
	ds_read_b128 v[132:135], v140 offset:1024
	ds_read_b128 v[136:139], v140 offset:2048
	ds_read_b128 v[140:143], v140 offset:3072
	s_waitcnt vmcnt(6)
	s_barrier
	v_mfma_f32_16x16x32_f16 v[52:55], v[204:207], v[158:161], v[52:55]
	v_mfma_f32_16x16x32_f16 v[44:47], v[212:215], v[158:161], v[44:47]
	v_mfma_f32_16x16x32_f16 v[36:39], v[204:207], v[180:183], v[36:39]
	v_mfma_f32_16x16x32_f16 v[28:31], v[212:215], v[180:183], v[28:31]
	v_mfma_f32_16x16x32_f16 v[20:23], v[204:207], v[188:191], v[20:23]
	v_mfma_f32_16x16x32_f16 v[12:15], v[212:215], v[188:191], v[12:15]
	v_mfma_f32_16x16x32_f16 v[4:7], v[204:207], v[196:199], v[4:7]
	v_mfma_f32_16x16x32_f16 v[0:3], v[212:215], v[196:199], v[0:3]
	v_mfma_f32_16x16x32_f16 v[52:55], v[208:211], v[176:179], v[52:55]
	v_mfma_f32_16x16x32_f16 v[44:47], v[216:219], v[176:179], v[44:47]
	v_mfma_f32_16x16x32_f16 v[36:39], v[208:211], v[184:187], v[36:39]
	v_mfma_f32_16x16x32_f16 v[28:31], v[216:219], v[184:187], v[28:31]
	v_mfma_f32_16x16x32_f16 v[20:23], v[208:211], v[192:195], v[20:23]
	v_mfma_f32_16x16x32_f16 v[12:15], v[216:219], v[192:195], v[12:15]
	v_mfma_f32_16x16x32_f16 v[4:7], v[208:211], v[200:203], v[4:7]
	v_mfma_f32_16x16x32_f16 v[0:3], v[216:219], v[200:203], v[0:3]
	s_barrier
	s_add_u32 s34, s34, 0x30000
	s_addc_u32 s35, s35, 0
	s_mov_b32 m0, s45
	ds_read_b128 v[158:161], v171 offset:32768
	ds_read_b128 v[176:179], v171 offset:33792
	ds_read_b128 v[180:183], v171 offset:34816
	ds_read_b128 v[184:187], v171 offset:35840
	ds_read_b128 v[188:191], v171 offset:36864
	ds_read_b128 v[192:195], v171 offset:37888
	ds_read_b128 v[196:199], v171 offset:38912
	ds_read_b128 v[200:203], v171 offset:39936
	global_load_lds_dwordx4 v144, s[34:35]
	s_mov_b32 m0, s46
	s_nop 0
	global_load_lds_dwordx4 v148, s[34:35]
	s_waitcnt lgkmcnt(8)
	s_barrier
	s_waitcnt lgkmcnt(0)
	v_mfma_f32_16x16x32_f16 v[124:127], v[128:131], v[158:161], v[124:127]
	v_mfma_f32_16x16x32_f16 v[120:123], v[136:139], v[158:161], v[120:123]
	v_mfma_f32_16x16x32_f16 v[108:111], v[128:131], v[180:183], v[108:111]
	v_mfma_f32_16x16x32_f16 v[104:107], v[136:139], v[180:183], v[104:107]
	v_mfma_f32_16x16x32_f16 v[96:99], v[128:131], v[188:191], v[96:99]
	v_mfma_f32_16x16x32_f16 v[88:91], v[136:139], v[188:191], v[88:91]
	v_mfma_f32_16x16x32_f16 v[80:83], v[128:131], v[196:199], v[80:83]
	v_mfma_f32_16x16x32_f16 v[72:75], v[136:139], v[196:199], v[72:75]
	v_mfma_f32_16x16x32_f16 v[124:127], v[132:135], v[176:179], v[124:127]
	v_mfma_f32_16x16x32_f16 v[120:123], v[140:143], v[176:179], v[120:123]
	v_mfma_f32_16x16x32_f16 v[108:111], v[132:135], v[184:187], v[108:111]
	v_mfma_f32_16x16x32_f16 v[104:107], v[140:143], v[184:187], v[104:107]
	v_mfma_f32_16x16x32_f16 v[96:99], v[132:135], v[192:195], v[96:99]
	v_mfma_f32_16x16x32_f16 v[88:91], v[140:143], v[192:195], v[88:91]
	v_mfma_f32_16x16x32_f16 v[80:83], v[132:135], v[200:203], v[80:83]
	v_mfma_f32_16x16x32_f16 v[72:75], v[140:143], v[200:203], v[72:75]
	s_barrier
	s_add_i32 s34, 0, 0x1c000
	s_add_i32 s35, s74, s42
	v_add_u32_e32 v175, s34, v166
	s_mov_b32 m0, s35
	ds_read_b128 v[204:207], v175
	ds_read_b128 v[208:211], v175 offset:1024
	ds_read_b128 v[212:215], v175 offset:2048
	ds_read_b128 v[216:219], v175 offset:3072
	global_load_lds_dwordx4 v146, s[78:79]
	s_add_i32 m0, s35, 0x2000
	s_nop 0
	global_load_lds_dwordx4 v150, s[78:79]
	s_barrier
	s_waitcnt lgkmcnt(0)
	v_mfma_f32_16x16x32_f16 v[116:119], v[204:207], v[158:161], v[116:119]
	v_mfma_f32_16x16x32_f16 v[112:115], v[212:215], v[158:161], v[112:115]
	v_mfma_f32_16x16x32_f16 v[100:103], v[204:207], v[180:183], v[100:103]
	v_mfma_f32_16x16x32_f16 v[92:95], v[212:215], v[180:183], v[92:95]
	v_mfma_f32_16x16x32_f16 v[84:87], v[204:207], v[188:191], v[84:87]
	v_mfma_f32_16x16x32_f16 v[76:79], v[212:215], v[188:191], v[76:79]
	v_mfma_f32_16x16x32_f16 v[68:71], v[204:207], v[196:199], v[68:71]
	v_mfma_f32_16x16x32_f16 v[64:67], v[212:215], v[196:199], v[64:67]
	v_mfma_f32_16x16x32_f16 v[116:119], v[208:211], v[176:179], v[116:119]
	v_mfma_f32_16x16x32_f16 v[112:115], v[216:219], v[176:179], v[112:115]
	v_mfma_f32_16x16x32_f16 v[100:103], v[208:211], v[184:187], v[100:103]
	v_mfma_f32_16x16x32_f16 v[92:95], v[216:219], v[184:187], v[92:95]
	v_mfma_f32_16x16x32_f16 v[84:87], v[208:211], v[192:195], v[84:87]
	v_mfma_f32_16x16x32_f16 v[76:79], v[216:219], v[192:195], v[76:79]
	v_mfma_f32_16x16x32_f16 v[68:71], v[208:211], v[200:203], v[68:71]
	v_mfma_f32_16x16x32_f16 v[64:67], v[216:219], v[200:203], v[64:67]
	s_barrier
	s_mov_b32 m0, s49
	ds_read_b128 v[158:161], v171 offset:49152
	ds_read_b128 v[176:179], v171 offset:50176
	ds_read_b128 v[180:183], v171 offset:51200
	ds_read_b128 v[184:187], v171 offset:52224
	ds_read_b128 v[188:191], v171 offset:53248
	ds_read_b128 v[192:195], v171 offset:54272
	ds_read_b128 v[196:199], v171 offset:55296
	ds_read_b128 v[200:203], v171 offset:56320
	global_load_lds_dwordx4 v144, s[80:81]
	s_mov_b32 m0, s50
	s_nop 0
	global_load_lds_dwordx4 v148, s[80:81]
	s_waitcnt vmcnt(10)
	s_barrier
	s_waitcnt lgkmcnt(0)
	v_mfma_f32_16x16x32_f16 v[60:63], v[128:131], v[158:161], v[60:63]
	v_mfma_f32_16x16x32_f16 v[56:59], v[136:139], v[158:161], v[56:59]
	v_mfma_f32_16x16x32_f16 v[48:51], v[128:131], v[180:183], v[48:51]
	v_mfma_f32_16x16x32_f16 v[40:43], v[136:139], v[180:183], v[40:43]
	v_mfma_f32_16x16x32_f16 v[32:35], v[128:131], v[188:191], v[32:35]
	v_mfma_f32_16x16x32_f16 v[24:27], v[136:139], v[188:191], v[24:27]
	v_mfma_f32_16x16x32_f16 v[16:19], v[128:131], v[196:199], v[16:19]
	v_mfma_f32_16x16x32_f16 v[8:11], v[136:139], v[196:199], v[8:11]
	v_mfma_f32_16x16x32_f16 v[60:63], v[132:135], v[176:179], v[60:63]
	v_mfma_f32_16x16x32_f16 v[56:59], v[140:143], v[176:179], v[56:59]
	v_mfma_f32_16x16x32_f16 v[48:51], v[132:135], v[184:187], v[48:51]
	v_mfma_f32_16x16x32_f16 v[40:43], v[140:143], v[184:187], v[40:43]
	v_mfma_f32_16x16x32_f16 v[32:35], v[132:135], v[192:195], v[32:35]
	v_mfma_f32_16x16x32_f16 v[24:27], v[140:143], v[192:195], v[24:27]
	v_mfma_f32_16x16x32_f16 v[16:19], v[132:135], v[200:203], v[16:19]
	v_mfma_f32_16x16x32_f16 v[8:11], v[140:143], v[200:203], v[8:11]
	s_barrier
	s_add_u32 s30, s30, 0xc080
	s_addc_u32 s31, s31, 0
	s_add_i32 s34, s34, s42
	s_mov_b32 m0, s34
	s_nop 0
	global_load_lds_dwordx4 v146, s[30:31]
	s_add_i32 m0, s34, 0x2000
	s_nop 0
	global_load_lds_dwordx4 v150, s[30:31]
	ds_read_b128 v[128:131], v170
	ds_read_b128 v[132:135], v170 offset:1024
	ds_read_b128 v[136:139], v170 offset:2048
	ds_read_b128 v[140:143], v170 offset:3072
	s_waitcnt vmcnt(6)
	s_barrier
	v_mfma_f32_16x16x32_f16 v[52:55], v[204:207], v[158:161], v[52:55]
	v_mfma_f32_16x16x32_f16 v[44:47], v[212:215], v[158:161], v[44:47]
	v_mfma_f32_16x16x32_f16 v[36:39], v[204:207], v[180:183], v[36:39]
	v_mfma_f32_16x16x32_f16 v[28:31], v[212:215], v[180:183], v[28:31]
	v_mfma_f32_16x16x32_f16 v[20:23], v[204:207], v[188:191], v[20:23]
	v_mfma_f32_16x16x32_f16 v[12:15], v[212:215], v[188:191], v[12:15]
	v_mfma_f32_16x16x32_f16 v[4:7], v[204:207], v[196:199], v[4:7]
	v_mfma_f32_16x16x32_f16 v[0:3], v[212:215], v[196:199], v[0:3]
	v_mfma_f32_16x16x32_f16 v[52:55], v[208:211], v[176:179], v[52:55]
	v_mfma_f32_16x16x32_f16 v[44:47], v[216:219], v[176:179], v[44:47]
	v_mfma_f32_16x16x32_f16 v[36:39], v[208:211], v[184:187], v[36:39]
	v_mfma_f32_16x16x32_f16 v[28:31], v[216:219], v[184:187], v[28:31]
	v_mfma_f32_16x16x32_f16 v[20:23], v[208:211], v[192:195], v[20:23]
	v_mfma_f32_16x16x32_f16 v[12:15], v[216:219], v[192:195], v[12:15]
	v_mfma_f32_16x16x32_f16 v[4:7], v[208:211], v[200:203], v[4:7]
	v_mfma_f32_16x16x32_f16 v[0:3], v[216:219], v[200:203], v[0:3]
	s_barrier
	s_add_i32 s73, s73, 2
	s_add_u32 s28, s28, 0x100
	s_addc_u32 s29, s29, 0
	s_add_u32 s71, s71, 0x100
	s_addc_u32 s72, s72, 0
	s_cmp_gt_u32 s73, 9
	s_cbranch_scc0 .LBB7_27
	s_lshl_b32 s28, s70, 8
	s_add_i32 s28, s28, s48
	s_lshl_b32 s29, s67, 8
	s_or_b32 s29, s29, s51
	s_waitcnt vmcnt(6)
	v_pk_fma_f32 v[126:127], v[126:127], v[226:227], v[236:237] op_sel_hi:[1,0,1]
	v_pk_fma_f32 v[124:125], v[124:125], v[226:227], v[234:235] op_sel_hi:[1,0,1]
	v_pk_fma_f32 v[186:187], v[122:123], v[226:227], v[240:241] op_sel_hi:[1,0,1]
	v_pk_fma_f32 v[122:123], v[120:121], v[226:227], v[238:239] op_sel_hi:[1,0,1]
	v_cvt_pk_f16_f32 v120, v124, v125
	v_cvt_pk_f16_f32 v121, v126, v127
	v_cvt_pk_f16_f32 v122, v122, v123
	v_cvt_pk_f16_f32 v123, v186, v187
	ds_write_b128 v173, v[120:123]
	v_pk_fma_f32 v[118:119], v[118:119], v[226:227], v[244:245] op_sel_hi:[1,0,1]
	v_pk_fma_f32 v[116:117], v[116:117], v[226:227], v[242:243] op_sel_hi:[1,0,1]
	v_pk_fma_f32 v[120:121], v[114:115], v[226:227], v[248:249] op_sel_hi:[1,0,1]
	v_pk_fma_f32 v[114:115], v[112:113], v[226:227], v[246:247] op_sel_hi:[1,0,1]
	v_cvt_pk_f16_f32 v112, v116, v117
	v_cvt_pk_f16_f32 v113, v118, v119
	v_cvt_pk_f16_f32 v114, v114, v115
	v_cvt_pk_f16_f32 v115, v120, v121
	ds_write_b128 v173, v[112:115] offset:64
	v_or_b32_e32 v116, s28, v167
	ds_read_b128 v[112:115], v174
	v_mul_lo_u32 v116, v116, s10
	v_add_u32_e32 v120, s29, v116
	v_lshlrev_b32_e32 v121, 1, v120
	v_add_u32_e32 v122, v121, v168
	ds_read_b128 v[116:119], v174 offset:1152
	s_waitcnt lgkmcnt(0)
	buffer_store_dwordx4 v[112:115], v122, s[20:23], 0 offen nt
	v_pk_fma_f32 v[110:111], v[110:111], v[226:227], v[236:237] op_sel:[0,1,0]
	v_pk_fma_f32 v[108:109], v[108:109], v[226:227], v[234:235] op_sel:[0,1,0]
	v_pk_fma_f32 v[112:113], v[106:107], v[226:227], v[240:241] op_sel:[0,1,0]
	v_pk_fma_f32 v[106:107], v[104:105], v[226:227], v[238:239] op_sel:[0,1,0]
	v_cvt_pk_f16_f32 v104, v108, v109
	v_cvt_pk_f16_f32 v105, v110, v111
	v_cvt_pk_f16_f32 v106, v106, v107
	v_cvt_pk_f16_f32 v107, v112, v113
	ds_write_b128 v173, v[104:107]
	v_pk_fma_f32 v[102:103], v[102:103], v[226:227], v[244:245] op_sel:[0,1,0]
	v_pk_fma_f32 v[100:101], v[100:101], v[226:227], v[242:243] op_sel:[0,1,0]
	v_pk_fma_f32 v[104:105], v[94:95], v[226:227], v[248:249] op_sel:[0,1,0]
	v_pk_fma_f32 v[94:95], v[92:93], v[226:227], v[246:247] op_sel:[0,1,0]
	v_cvt_pk_f16_f32 v92, v100, v101
	v_cvt_pk_f16_f32 v93, v102, v103
	v_cvt_pk_f16_f32 v94, v94, v95
	v_cvt_pk_f16_f32 v95, v104, v105
	ds_write_b128 v173, v[92:95] offset:64
	ds_read_b128 v[92:95], v174
	ds_read_b128 v[100:103], v174 offset:1152
	v_add_u32_e32 v104, s55, v121
	v_add_u32_e32 v114, v121, v169
	v_add_u32_e32 v105, v104, v168
	buffer_store_dwordx4 v[116:119], v114, s[20:23], 0 offen nt
	s_waitcnt lgkmcnt(1)
	buffer_store_dwordx4 v[92:95], v105, s[20:23], 0 offen nt
	v_pk_fma_f32 v[86:87], v[86:87], v[228:229], v[244:245] op_sel_hi:[1,0,1]
	v_pk_fma_f32 v[84:85], v[84:85], v[228:229], v[242:243] op_sel_hi:[1,0,1]
	v_pk_fma_f32 v[92:93], v[98:99], v[228:229], v[236:237] op_sel_hi:[1,0,1]
	v_pk_fma_f32 v[94:95], v[96:97], v[228:229], v[234:235] op_sel_hi:[1,0,1]
	v_pk_fma_f32 v[96:97], v[90:91], v[228:229], v[240:241] op_sel_hi:[1,0,1]
	v_pk_fma_f32 v[90:91], v[88:89], v[228:229], v[238:239] op_sel_hi:[1,0,1]
	v_cvt_pk_f16_f32 v88, v94, v95
	v_cvt_pk_f16_f32 v89, v92, v93
	v_cvt_pk_f16_f32 v90, v90, v91
	v_cvt_pk_f16_f32 v91, v96, v97
	ds_write_b128 v173, v[88:91]
	v_pk_fma_f32 v[88:89], v[78:79], v[228:229], v[248:249] op_sel_hi:[1,0,1]
	v_pk_fma_f32 v[78:79], v[76:77], v[228:229], v[246:247] op_sel_hi:[1,0,1]
	v_cvt_pk_f16_f32 v76, v84, v85
	v_cvt_pk_f16_f32 v77, v86, v87
	v_cvt_pk_f16_f32 v78, v78, v79
	v_cvt_pk_f16_f32 v79, v88, v89
	ds_write_b128 v173, v[76:79] offset:64
	ds_read_b128 v[76:79], v174
	ds_read_b128 v[84:87], v174 offset:1152
	v_add_u32_e32 v88, s55, v104
	v_add_u32_e32 v105, v104, v169
	v_add_u32_e32 v89, v88, v168
	s_waitcnt lgkmcnt(4)
	buffer_store_dwordx4 v[100:103], v105, s[20:23], 0 offen nt
	s_waitcnt lgkmcnt(1)
	buffer_store_dwordx4 v[76:79], v89, s[20:23], 0 offen nt
	v_pk_fma_f32 v[70:71], v[70:71], v[228:229], v[244:245] op_sel:[0,1,0]
	v_pk_fma_f32 v[68:69], v[68:69], v[228:229], v[242:243] op_sel:[0,1,0]
	v_add_u32_e32 v76, v88, v169
	s_waitcnt lgkmcnt(0)
	buffer_store_dwordx4 v[84:87], v76, s[20:23], 0 offen nt
	v_pk_fma_f32 v[76:77], v[82:83], v[228:229], v[236:237] op_sel:[0,1,0]
	v_pk_fma_f32 v[78:79], v[80:81], v[228:229], v[234:235] op_sel:[0,1,0]
	v_pk_fma_f32 v[80:81], v[74:75], v[228:229], v[240:241] op_sel:[0,1,0]
	v_pk_fma_f32 v[74:75], v[72:73], v[228:229], v[238:239] op_sel:[0,1,0]
	v_cvt_pk_f16_f32 v72, v78, v79
	v_cvt_pk_f16_f32 v73, v76, v77
	v_cvt_pk_f16_f32 v74, v74, v75
	v_cvt_pk_f16_f32 v75, v80, v81
	ds_write_b128 v173, v[72:75]
	v_pk_fma_f32 v[72:73], v[66:67], v[228:229], v[248:249] op_sel:[0,1,0]
	v_pk_fma_f32 v[66:67], v[64:65], v[228:229], v[246:247] op_sel:[0,1,0]
	v_cvt_pk_f16_f32 v64, v68, v69
	v_cvt_pk_f16_f32 v65, v70, v71
	v_cvt_pk_f16_f32 v66, v66, v67
	v_cvt_pk_f16_f32 v67, v72, v73
	ds_write_b128 v173, v[64:67] offset:64
	ds_read_b128 v[64:67], v174
	ds_read_b128 v[68:71], v174 offset:1152
	v_add_u32_e32 v72, s56, v120
	v_lshlrev_b32_e32 v73, 1, v72
	v_add_u32_e32 v74, v73, v168
	s_waitcnt lgkmcnt(1)
	buffer_store_dwordx4 v[64:67], v74, s[20:23], 0 offen nt
	v_pk_fma_f32 v[62:63], v[62:63], v[230:231], v[236:237] op_sel_hi:[1,0,1]
	v_pk_fma_f32 v[60:61], v[60:61], v[230:231], v[234:235] op_sel_hi:[1,0,1]
	v_pk_fma_f32 v[64:65], v[58:59], v[230:231], v[240:241] op_sel_hi:[1,0,1]
	v_pk_fma_f32 v[58:59], v[56:57], v[230:231], v[238:239] op_sel_hi:[1,0,1]
	v_cvt_pk_f16_f32 v56, v60, v61
	v_cvt_pk_f16_f32 v57, v62, v63
	v_cvt_pk_f16_f32 v58, v58, v59
	v_cvt_pk_f16_f32 v59, v64, v65
	ds_write_b128 v173, v[56:59]
	v_pk_fma_f32 v[54:55], v[54:55], v[230:231], v[244:245] op_sel_hi:[1,0,1]
	v_pk_fma_f32 v[52:53], v[52:53], v[230:231], v[242:243] op_sel_hi:[1,0,1]
	v_pk_fma_f32 v[56:57], v[46:47], v[230:231], v[248:249] op_sel_hi:[1,0,1]
	v_pk_fma_f32 v[46:47], v[44:45], v[230:231], v[246:247] op_sel_hi:[1,0,1]
	v_cvt_pk_f16_f32 v44, v52, v53
	v_cvt_pk_f16_f32 v45, v54, v55
	v_cvt_pk_f16_f32 v46, v46, v47
	v_cvt_pk_f16_f32 v47, v56, v57
	ds_write_b128 v173, v[44:47] offset:64
	ds_read_b128 v[44:47], v174
	ds_read_b128 v[52:55], v174 offset:1152
	v_add_u32_e32 v56, s62, v88
	v_add_u32_e32 v66, v73, v169
	v_add_u32_e32 v57, v56, v168
	s_waitcnt lgkmcnt(4)
	buffer_store_dwordx4 v[68:71], v66, s[20:23], 0 offen nt
	s_waitcnt lgkmcnt(1)
	buffer_store_dwordx4 v[44:47], v57, s[20:23], 0 offen nt
	v_pk_fma_f32 v[38:39], v[38:39], v[230:231], v[244:245] op_sel:[0,1,0]
	v_pk_fma_f32 v[36:37], v[36:37], v[230:231], v[242:243] op_sel:[0,1,0]
	v_add_u32_e32 v44, v56, v169
	s_waitcnt lgkmcnt(0)
	buffer_store_dwordx4 v[52:55], v44, s[20:23], 0 offen nt
	v_pk_fma_f32 v[44:45], v[50:51], v[230:231], v[236:237] op_sel:[0,1,0]
	v_pk_fma_f32 v[46:47], v[48:49], v[230:231], v[234:235] op_sel:[0,1,0]
	v_pk_fma_f32 v[48:49], v[42:43], v[230:231], v[240:241] op_sel:[0,1,0]
	v_pk_fma_f32 v[42:43], v[40:41], v[230:231], v[238:239] op_sel:[0,1,0]
	v_cvt_pk_f16_f32 v40, v46, v47
	v_cvt_pk_f16_f32 v41, v44, v45
	v_cvt_pk_f16_f32 v42, v42, v43
	v_cvt_pk_f16_f32 v43, v48, v49
	ds_write_b128 v173, v[40:43]
	v_pk_fma_f32 v[40:41], v[30:31], v[230:231], v[248:249] op_sel:[0,1,0]
	v_pk_fma_f32 v[30:31], v[28:29], v[230:231], v[246:247] op_sel:[0,1,0]
	v_cvt_pk_f16_f32 v28, v36, v37
	v_cvt_pk_f16_f32 v29, v38, v39
	v_cvt_pk_f16_f32 v30, v30, v31
	v_cvt_pk_f16_f32 v31, v40, v41
	ds_write_b128 v173, v[28:31] offset:64
	ds_read_b128 v[28:31], v174
	ds_read_b128 v[36:39], v174 offset:1152
	v_add_u32_e32 v40, s63, v72
	v_lshlrev_b32_e32 v41, 1, v40
	v_add_u32_e32 v42, v41, v168
	s_waitcnt lgkmcnt(1)
	buffer_store_dwordx4 v[28:31], v42, s[20:23], 0 offen nt
	v_pk_fma_f32 v[22:23], v[22:23], v[232:233], v[244:245] op_sel_hi:[1,0,1]
	v_pk_fma_f32 v[20:21], v[20:21], v[232:233], v[242:243] op_sel_hi:[1,0,1]
	v_add_u32_e32 v28, v41, v169
	s_waitcnt lgkmcnt(0)
	buffer_store_dwordx4 v[36:39], v28, s[20:23], 0 offen nt
	v_pk_fma_f32 v[28:29], v[34:35], v[232:233], v[236:237] op_sel_hi:[1,0,1]
	v_pk_fma_f32 v[30:31], v[32:33], v[232:233], v[234:235] op_sel_hi:[1,0,1]
	v_pk_fma_f32 v[32:33], v[26:27], v[232:233], v[240:241] op_sel_hi:[1,0,1]
	v_pk_fma_f32 v[26:27], v[24:25], v[232:233], v[238:239] op_sel_hi:[1,0,1]
	v_cvt_pk_f16_f32 v24, v30, v31
	v_cvt_pk_f16_f32 v25, v28, v29
	v_cvt_pk_f16_f32 v26, v26, v27
	v_cvt_pk_f16_f32 v27, v32, v33
	ds_write_b128 v173, v[24:27]
	v_pk_fma_f32 v[24:25], v[14:15], v[232:233], v[248:249] op_sel_hi:[1,0,1]
	v_pk_fma_f32 v[14:15], v[12:13], v[232:233], v[246:247] op_sel_hi:[1,0,1]
	v_cvt_pk_f16_f32 v12, v20, v21
	v_cvt_pk_f16_f32 v13, v22, v23
	v_cvt_pk_f16_f32 v14, v14, v15
	v_cvt_pk_f16_f32 v15, v24, v25
	ds_write_b128 v173, v[12:15] offset:64
	ds_read_b128 v[12:15], v174
	ds_read_b128 v[20:23], v174 offset:1152
	v_add_u32_e32 v24, s64, v40
	v_lshlrev_b32_e32 v25, 1, v24
	v_add_u32_e32 v26, v25, v168
	s_waitcnt lgkmcnt(1)
	buffer_store_dwordx4 v[12:15], v26, s[20:23], 0 offen nt
	v_pk_fma_f32 v[6:7], v[6:7], v[232:233], v[244:245] op_sel:[0,1,0]
	v_pk_fma_f32 v[4:5], v[4:5], v[232:233], v[242:243] op_sel:[0,1,0]
	v_pk_fma_f32 v[12:13], v[18:19], v[232:233], v[236:237] op_sel:[0,1,0]
	v_pk_fma_f32 v[14:15], v[16:17], v[232:233], v[234:235] op_sel:[0,1,0]
	v_pk_fma_f32 v[16:17], v[10:11], v[232:233], v[240:241] op_sel:[0,1,0]
	v_pk_fma_f32 v[10:11], v[8:9], v[232:233], v[238:239] op_sel:[0,1,0]
	v_cvt_pk_f16_f32 v8, v14, v15
	v_cvt_pk_f16_f32 v9, v12, v13
	v_cvt_pk_f16_f32 v10, v10, v11
	v_cvt_pk_f16_f32 v11, v16, v17
	ds_write_b128 v173, v[8:11]
	v_pk_fma_f32 v[8:9], v[2:3], v[232:233], v[248:249] op_sel:[0,1,0]
	v_pk_fma_f32 v[2:3], v[0:1], v[232:233], v[246:247] op_sel:[0,1,0]
	v_cvt_pk_f16_f32 v0, v4, v5
	v_cvt_pk_f16_f32 v1, v6, v7
	v_cvt_pk_f16_f32 v2, v2, v3
	v_cvt_pk_f16_f32 v3, v8, v9
	ds_write_b128 v173, v[0:3] offset:64
	ds_read_b128 v[0:3], v174
	ds_read_b128 v[4:7], v174 offset:1152
	v_add_lshl_u32 v8, v24, s64, 1
	v_add_u32_e32 v25, v25, v169
	v_add_u32_e32 v9, v8, v168
	s_waitcnt lgkmcnt(4)
	buffer_store_dwordx4 v[20:23], v25, s[20:23], 0 offen nt
	s_waitcnt lgkmcnt(1)
	buffer_store_dwordx4 v[0:3], v9, s[20:23], 0 offen nt
	s_mov_b32 s67, s68
	s_mov_b32 s70, s69
	v_add_u32_e32 v0, v8, v169
	s_mov_b64 s[30:31], s[0:1]
	s_mov_b64 s[28:29], s[8:9]
	s_mov_b64 vcc, s[6:7]
	s_waitcnt lgkmcnt(0)
	buffer_store_dwordx4 v[4:7], v0, s[20:23], 0 offen nt
	s_cbranch_vccz .LBB7_12
	s_waitcnt vmcnt(0)
	s_cmpk_gt_u32 s36, 0xff
	s_cbranch_scc1 .LBB7_31
	s_barrier

.LBB7_32:
	s_endpgm
	s_endpgm
	s_endpgm
	s_endpgm
	s_endpgm
	s_endpgm
	s_endpgm
	s_endpgm
	s_endpgm
	s_endpgm
	s_endpgm
	s_endpgm
	s_endpgm
	s_endpgm
	s_endpgm
	s_endpgm
	s_endpgm
	s_endpgm
	s_endpgm
	s_endpgm
	s_endpgm
	s_endpgm
	s_endpgm
	s_endpgm
	s_endpgm
	s_endpgm
	s_endpgm
	.section	.rodata,"a",@progbits
	.p2align	6, 0x0

.LBB8_26:
	s_add_u32 s38, s38, 0x30080
	s_addc_u32 s39, s39, 0
	s_add_u32 s85, s40, 0x100
	v_mov_b32_e32 v0, 0
	s_addc_u32 s86, s41, 0
	s_mov_b32 s87, -2
	v_mov_b32_e32 v1, v0
	v_mov_b32_e32 v2, v0
	v_mov_b32_e32 v3, v0
	v_mov_b32_e32 v4, v0
	v_mov_b32_e32 v5, v0
	v_mov_b32_e32 v6, v0
	v_mov_b32_e32 v7, v0
	v_mov_b32_e32 v16, v0
	v_mov_b32_e32 v17, v0
	v_mov_b32_e32 v18, v0
	v_mov_b32_e32 v19, v0
	v_mov_b32_e32 v20, v0
	v_mov_b32_e32 v21, v0
	v_mov_b32_e32 v22, v0
	v_mov_b32_e32 v23, v0
	v_mov_b32_e32 v32, v0
	v_mov_b32_e32 v33, v0
	v_mov_b32_e32 v34, v0
	v_mov_b32_e32 v35, v0
	v_mov_b32_e32 v36, v0
	v_mov_b32_e32 v37, v0
	v_mov_b32_e32 v38, v0
	v_mov_b32_e32 v39, v0
	v_mov_b32_e32 v48, v0
	v_mov_b32_e32 v49, v0
	v_mov_b32_e32 v50, v0
	v_mov_b32_e32 v51, v0
	v_mov_b32_e32 v52, v0
	v_mov_b32_e32 v53, v0
	v_mov_b32_e32 v54, v0
	v_mov_b32_e32 v55, v0
	v_mov_b32_e32 v8, v0
	v_mov_b32_e32 v9, v0
	v_mov_b32_e32 v10, v0
	v_mov_b32_e32 v11, v0
	v_mov_b32_e32 v12, v0
	v_mov_b32_e32 v13, v0
	v_mov_b32_e32 v14, v0
	v_mov_b32_e32 v15, v0
	v_mov_b32_e32 v24, v0
	v_mov_b32_e32 v25, v0
	v_mov_b32_e32 v26, v0
	v_mov_b32_e32 v27, v0
	v_mov_b32_e32 v28, v0
	v_mov_b32_e32 v29, v0
	v_mov_b32_e32 v30, v0
	v_mov_b32_e32 v31, v0
	v_mov_b32_e32 v40, v0
	v_mov_b32_e32 v41, v0
	v_mov_b32_e32 v42, v0
	v_mov_b32_e32 v43, v0
	v_mov_b32_e32 v44, v0
	v_mov_b32_e32 v45, v0
	v_mov_b32_e32 v46, v0
	v_mov_b32_e32 v47, v0
	v_mov_b32_e32 v56, v0
	v_mov_b32_e32 v57, v0
	v_mov_b32_e32 v58, v0
	v_mov_b32_e32 v59, v0
	v_mov_b32_e32 v60, v0
	v_mov_b32_e32 v61, v0
	v_mov_b32_e32 v62, v0
	v_mov_b32_e32 v63, v0
	v_mov_b32_e32 v64, v0
	v_mov_b32_e32 v65, v0
	v_mov_b32_e32 v66, v0
	v_mov_b32_e32 v67, v0
	v_mov_b32_e32 v68, v0
	v_mov_b32_e32 v69, v0
	v_mov_b32_e32 v70, v0
	v_mov_b32_e32 v71, v0
	v_mov_b32_e32 v96, v0
	v_mov_b32_e32 v97, v0
	v_mov_b32_e32 v98, v0
	v_mov_b32_e32 v99, v0
	v_mov_b32_e32 v100, v0
	v_mov_b32_e32 v101, v0
	v_mov_b32_e32 v102, v0
	v_mov_b32_e32 v103, v0
	v_mov_b32_e32 v112, v0
	v_mov_b32_e32 v113, v0
	v_mov_b32_e32 v114, v0
	v_mov_b32_e32 v115, v0
	v_mov_b32_e32 v116, v0
	v_mov_b32_e32 v117, v0
	v_mov_b32_e32 v118, v0
	v_mov_b32_e32 v119, v0
	v_mov_b32_e32 v128, v0
	v_mov_b32_e32 v129, v0
	v_mov_b32_e32 v130, v0
	v_mov_b32_e32 v131, v0
	v_mov_b32_e32 v132, v0
	v_mov_b32_e32 v133, v0
	v_mov_b32_e32 v134, v0
	v_mov_b32_e32 v135, v0
	v_mov_b32_e32 v76, v0
	v_mov_b32_e32 v77, v0
	v_mov_b32_e32 v78, v0
	v_mov_b32_e32 v79, v0
	v_mov_b32_e32 v84, v0
	v_mov_b32_e32 v85, v0
	v_mov_b32_e32 v86, v0
	v_mov_b32_e32 v87, v0
	v_mov_b32_e32 v104, v0
	v_mov_b32_e32 v105, v0
	v_mov_b32_e32 v106, v0
	v_mov_b32_e32 v107, v0
	v_mov_b32_e32 v108, v0
	v_mov_b32_e32 v109, v0
	v_mov_b32_e32 v110, v0
	v_mov_b32_e32 v111, v0
	v_mov_b32_e32 v120, v0
	v_mov_b32_e32 v121, v0
	v_mov_b32_e32 v122, v0
	v_mov_b32_e32 v123, v0
	v_mov_b32_e32 v124, v0
	v_mov_b32_e32 v125, v0
	v_mov_b32_e32 v126, v0
	v_mov_b32_e32 v127, v0
	v_mov_b32_e32 v140, v0
	v_mov_b32_e32 v141, v0
	v_mov_b32_e32 v142, v0
	v_mov_b32_e32 v143, v0
	v_mov_b32_e32 v144, v0
	v_mov_b32_e32 v145, v0
	v_mov_b32_e32 v146, v0
	v_mov_b32_e32 v147, v0
	ds_read_b128 v[72:75], v231
	ds_read_b128 v[80:83], v231 offset:1024
	ds_read_b128 v[88:91], v231 offset:2048
	ds_read_b128 v[92:95], v231 offset:3072
.LBB8_27:
	s_add_u32 s40, s38, 0xfffd0080
	s_addc_u32 s41, s39, -1
	s_cmp_eq_u32 s87, 8
	s_cselect_b32 s43, s9, s41
	s_cselect_b32 s42, s8, s40
	s_cselect_b32 s41, s1, s86
	s_cselect_b32 s40, s0, s85
	s_add_i32 m0, s51, 0xc000
	ds_read_b128 v[136:139], v232
	ds_read_b128 v[148:151], v232 offset:1024
	ds_read_b128 v[152:155], v232 offset:2048
	ds_read_b128 v[156:159], v232 offset:3072
	ds_read_b128 v[160:163], v232 offset:4096
	ds_read_b128 v[164:167], v232 offset:5120
	ds_read_b128 v[168:171], v232 offset:6144
	ds_read_b128 v[172:175], v232 offset:7168
	global_load_lds_dwordx4 v184, s[38:39]
	s_add_i32 m0, s51, 0xe000
	s_nop 0
	global_load_lds_dwordx4 v186, s[38:39]
	s_waitcnt lgkmcnt(8)
	s_barrier
	s_waitcnt lgkmcnt(0)
	v_mfma_f32_16x16x32_f16 v[144:147], v[72:75], v[136:139], v[144:147]
	v_mfma_f32_16x16x32_f16 v[140:143], v[88:91], v[136:139], v[140:143]
	v_mfma_f32_16x16x32_f16 v[124:127], v[72:75], v[152:155], v[124:127]
	v_mfma_f32_16x16x32_f16 v[120:123], v[88:91], v[152:155], v[120:123]
	v_mfma_f32_16x16x32_f16 v[108:111], v[72:75], v[160:163], v[108:111]
	v_mfma_f32_16x16x32_f16 v[104:107], v[88:91], v[160:163], v[104:107]
	v_mfma_f32_16x16x32_f16 v[84:87], v[72:75], v[168:171], v[84:87]
	v_mfma_f32_16x16x32_f16 v[76:79], v[88:91], v[168:171], v[76:79]
	v_mfma_f32_16x16x32_f16 v[144:147], v[80:83], v[148:151], v[144:147]
	v_mfma_f32_16x16x32_f16 v[140:143], v[92:95], v[148:151], v[140:143]
	v_mfma_f32_16x16x32_f16 v[124:127], v[80:83], v[156:159], v[124:127]
	v_mfma_f32_16x16x32_f16 v[120:123], v[92:95], v[156:159], v[120:123]
	v_mfma_f32_16x16x32_f16 v[108:111], v[80:83], v[164:167], v[108:111]
	v_mfma_f32_16x16x32_f16 v[104:107], v[92:95], v[164:167], v[104:107]
	v_mfma_f32_16x16x32_f16 v[84:87], v[80:83], v[172:175], v[84:87]
	v_mfma_f32_16x16x32_f16 v[76:79], v[92:95], v[172:175], v[76:79]
	s_barrier
	s_add_i32 s88, s70, s50
	s_add_u32 s92, s40, 0x80
	s_addc_u32 s93, s41, 0
	s_mov_b32 m0, s88
	ds_read_b128 v[190:193], v233
	ds_read_b128 v[194:197], v233 offset:1024
	ds_read_b128 v[198:201], v233 offset:2048
	ds_read_b128 v[202:205], v233 offset:3072
	global_load_lds_dwordx4 v178, s[40:41]
	s_add_i32 m0, s88, 0x2000
	s_nop 0
	global_load_lds_dwordx4 v182, s[40:41]
	s_barrier
	s_waitcnt lgkmcnt(0)
	v_mfma_f32_16x16x32_f16 v[132:135], v[190:193], v[136:139], v[132:135]
	v_mfma_f32_16x16x32_f16 v[128:131], v[198:201], v[136:139], v[128:131]
	v_mfma_f32_16x16x32_f16 v[116:119], v[190:193], v[152:155], v[116:119]
	v_mfma_f32_16x16x32_f16 v[112:115], v[198:201], v[152:155], v[112:115]
	v_mfma_f32_16x16x32_f16 v[100:103], v[190:193], v[160:163], v[100:103]
	v_mfma_f32_16x16x32_f16 v[96:99], v[198:201], v[160:163], v[96:99]
	v_mfma_f32_16x16x32_f16 v[68:71], v[190:193], v[168:171], v[68:71]
	v_mfma_f32_16x16x32_f16 v[64:67], v[198:201], v[168:171], v[64:67]
	v_mfma_f32_16x16x32_f16 v[132:135], v[194:197], v[148:151], v[132:135]
	v_mfma_f32_16x16x32_f16 v[128:131], v[202:205], v[148:151], v[128:131]
	v_mfma_f32_16x16x32_f16 v[116:119], v[194:197], v[156:159], v[116:119]
	v_mfma_f32_16x16x32_f16 v[112:115], v[202:205], v[156:159], v[112:115]
	v_mfma_f32_16x16x32_f16 v[100:103], v[194:197], v[164:167], v[100:103]
	v_mfma_f32_16x16x32_f16 v[96:99], v[202:205], v[164:167], v[96:99]
	v_mfma_f32_16x16x32_f16 v[68:71], v[194:197], v[172:175], v[68:71]
	v_mfma_f32_16x16x32_f16 v[64:67], v[202:205], v[172:175], v[64:67]
	s_barrier
	s_mov_b32 m0, s51
	s_add_u32 s94, s42, 0x80
	s_addc_u32 s95, s43, 0
	ds_read_b128 v[136:139], v232 offset:16384
	ds_read_b128 v[148:151], v232 offset:17408
	ds_read_b128 v[152:155], v232 offset:18432
	ds_read_b128 v[156:159], v232 offset:19456
	ds_read_b128 v[160:163], v232 offset:20480
	ds_read_b128 v[164:167], v232 offset:21504
	ds_read_b128 v[168:171], v232 offset:22528
	ds_read_b128 v[172:175], v232 offset:23552
	global_load_lds_dwordx4 v176, s[42:43]
	s_mov_b32 m0, s52
	s_nop 0
	global_load_lds_dwordx4 v180, s[42:43]
	s_waitcnt vmcnt(10)
	s_barrier
	s_waitcnt lgkmcnt(0)
	v_mfma_f32_16x16x32_f16 v[60:63], v[72:75], v[136:139], v[60:63]
	v_mfma_f32_16x16x32_f16 v[56:59], v[88:91], v[136:139], v[56:59]
	v_mfma_f32_16x16x32_f16 v[44:47], v[72:75], v[152:155], v[44:47]
	v_mfma_f32_16x16x32_f16 v[40:43], v[88:91], v[152:155], v[40:43]
	v_mfma_f32_16x16x32_f16 v[28:31], v[72:75], v[160:163], v[28:31]
	v_mfma_f32_16x16x32_f16 v[24:27], v[88:91], v[160:163], v[24:27]
	v_mfma_f32_16x16x32_f16 v[12:15], v[72:75], v[168:171], v[12:15]
	v_mfma_f32_16x16x32_f16 v[8:11], v[88:91], v[168:171], v[8:11]
	v_mfma_f32_16x16x32_f16 v[60:63], v[80:83], v[148:151], v[60:63]
	v_mfma_f32_16x16x32_f16 v[56:59], v[92:95], v[148:151], v[56:59]
	v_mfma_f32_16x16x32_f16 v[44:47], v[80:83], v[156:159], v[44:47]
	v_mfma_f32_16x16x32_f16 v[40:43], v[92:95], v[156:159], v[40:43]
	v_mfma_f32_16x16x32_f16 v[28:31], v[80:83], v[164:167], v[28:31]
	v_mfma_f32_16x16x32_f16 v[24:27], v[92:95], v[164:167], v[24:27]
	v_mfma_f32_16x16x32_f16 v[12:15], v[80:83], v[172:175], v[12:15]
	v_mfma_f32_16x16x32_f16 v[8:11], v[92:95], v[172:175], v[8:11]
	s_barrier
	s_add_u32 s88, s40, 0xc000
	s_addc_u32 s89, s41, 0
	s_add_i32 s90, s71, s50
	s_mov_b32 m0, s90
	s_nop 0
	global_load_lds_dwordx4 v178, s[88:89]
	s_add_i32 m0, s90, 0x2000
	s_nop 0
	global_load_lds_dwordx4 v182, s[88:89]
	s_add_i32 s88, 0, 0x18000
	v_add_u32_e32 v92, s88, v228
	ds_read_b128 v[72:75], v92
	ds_read_b128 v[80:83], v92 offset:1024
	ds_read_b128 v[88:91], v92 offset:2048
	ds_read_b128 v[92:95], v92 offset:3072
	s_waitcnt vmcnt(6)
	s_barrier
	v_mfma_f32_16x16x32_f16 v[52:55], v[190:193], v[136:139], v[52:55]
	v_mfma_f32_16x16x32_f16 v[48:51], v[198:201], v[136:139], v[48:51]
	v_mfma_f32_16x16x32_f16 v[36:39], v[190:193], v[152:155], v[36:39]
	v_mfma_f32_16x16x32_f16 v[32:35], v[198:201], v[152:155], v[32:35]
	v_mfma_f32_16x16x32_f16 v[20:23], v[190:193], v[160:163], v[20:23]
	v_mfma_f32_16x16x32_f16 v[16:19], v[198:201], v[160:163], v[16:19]
	v_mfma_f32_16x16x32_f16 v[4:7], v[190:193], v[168:171], v[4:7]
	v_mfma_f32_16x16x32_f16 v[0:3], v[198:201], v[168:171], v[0:3]
	v_mfma_f32_16x16x32_f16 v[52:55], v[194:197], v[148:151], v[52:55]
	v_mfma_f32_16x16x32_f16 v[48:51], v[202:205], v[148:151], v[48:51]
	v_mfma_f32_16x16x32_f16 v[36:39], v[194:197], v[156:159], v[36:39]
	v_mfma_f32_16x16x32_f16 v[32:35], v[202:205], v[156:159], v[32:35]
	v_mfma_f32_16x16x32_f16 v[20:23], v[194:197], v[164:167], v[20:23]
	v_mfma_f32_16x16x32_f16 v[16:19], v[202:205], v[164:167], v[16:19]
	v_mfma_f32_16x16x32_f16 v[4:7], v[194:197], v[172:175], v[4:7]
	v_mfma_f32_16x16x32_f16 v[0:3], v[202:205], v[172:175], v[0:3]
	s_barrier
	s_add_u32 s42, s42, 0x30000
	s_addc_u32 s43, s43, 0
	s_mov_b32 m0, s53
	ds_read_b128 v[136:139], v232 offset:32768
	ds_read_b128 v[148:151], v232 offset:33792
	ds_read_b128 v[152:155], v232 offset:34816
	ds_read_b128 v[156:159], v232 offset:35840
	ds_read_b128 v[160:163], v232 offset:36864
	ds_read_b128 v[164:167], v232 offset:37888
	ds_read_b128 v[168:171], v232 offset:38912
	ds_read_b128 v[172:175], v232 offset:39936
	global_load_lds_dwordx4 v176, s[42:43]
	s_mov_b32 m0, s54
	s_nop 0
	global_load_lds_dwordx4 v180, s[42:43]
	s_waitcnt lgkmcnt(8)
	s_barrier
	s_waitcnt lgkmcnt(0)
	v_mfma_f32_16x16x32_f16 v[144:147], v[72:75], v[136:139], v[144:147]
	v_mfma_f32_16x16x32_f16 v[140:143], v[88:91], v[136:139], v[140:143]
	v_mfma_f32_16x16x32_f16 v[124:127], v[72:75], v[152:155], v[124:127]
	v_mfma_f32_16x16x32_f16 v[120:123], v[88:91], v[152:155], v[120:123]
	v_mfma_f32_16x16x32_f16 v[108:111], v[72:75], v[160:163], v[108:111]
	v_mfma_f32_16x16x32_f16 v[104:107], v[88:91], v[160:163], v[104:107]
	v_mfma_f32_16x16x32_f16 v[84:87], v[72:75], v[168:171], v[84:87]
	v_mfma_f32_16x16x32_f16 v[76:79], v[88:91], v[168:171], v[76:79]
	v_mfma_f32_16x16x32_f16 v[144:147], v[80:83], v[148:151], v[144:147]
	v_mfma_f32_16x16x32_f16 v[140:143], v[92:95], v[148:151], v[140:143]
	v_mfma_f32_16x16x32_f16 v[124:127], v[80:83], v[156:159], v[124:127]
	v_mfma_f32_16x16x32_f16 v[120:123], v[92:95], v[156:159], v[120:123]
	v_mfma_f32_16x16x32_f16 v[108:111], v[80:83], v[164:167], v[108:111]
	v_mfma_f32_16x16x32_f16 v[104:107], v[92:95], v[164:167], v[104:107]
	v_mfma_f32_16x16x32_f16 v[84:87], v[80:83], v[172:175], v[84:87]
	v_mfma_f32_16x16x32_f16 v[76:79], v[92:95], v[172:175], v[76:79]
	s_barrier
	s_add_i32 s42, 0, 0x1c000
	s_add_i32 s43, s88, s50
	v_add_u32_e32 v202, s42, v228
	s_mov_b32 m0, s43
	ds_read_b128 v[190:193], v202
	ds_read_b128 v[194:197], v202 offset:1024
	ds_read_b128 v[198:201], v202 offset:2048
	ds_read_b128 v[202:205], v202 offset:3072
	global_load_lds_dwordx4 v178, s[92:93]
	s_add_i32 m0, s43, 0x2000
	s_nop 0
	global_load_lds_dwordx4 v182, s[92:93]
	s_barrier
	s_waitcnt lgkmcnt(0)
	v_mfma_f32_16x16x32_f16 v[132:135], v[190:193], v[136:139], v[132:135]
	v_mfma_f32_16x16x32_f16 v[128:131], v[198:201], v[136:139], v[128:131]
	v_mfma_f32_16x16x32_f16 v[116:119], v[190:193], v[152:155], v[116:119]
	v_mfma_f32_16x16x32_f16 v[112:115], v[198:201], v[152:155], v[112:115]
	v_mfma_f32_16x16x32_f16 v[100:103], v[190:193], v[160:163], v[100:103]
	v_mfma_f32_16x16x32_f16 v[96:99], v[198:201], v[160:163], v[96:99]
	v_mfma_f32_16x16x32_f16 v[68:71], v[190:193], v[168:171], v[68:71]
	v_mfma_f32_16x16x32_f16 v[64:67], v[198:201], v[168:171], v[64:67]
	v_mfma_f32_16x16x32_f16 v[132:135], v[194:197], v[148:151], v[132:135]
	v_mfma_f32_16x16x32_f16 v[128:131], v[202:205], v[148:151], v[128:131]
	v_mfma_f32_16x16x32_f16 v[116:119], v[194:197], v[156:159], v[116:119]
	v_mfma_f32_16x16x32_f16 v[112:115], v[202:205], v[156:159], v[112:115]
	v_mfma_f32_16x16x32_f16 v[100:103], v[194:197], v[164:167], v[100:103]
	v_mfma_f32_16x16x32_f16 v[96:99], v[202:205], v[164:167], v[96:99]
	v_mfma_f32_16x16x32_f16 v[68:71], v[194:197], v[172:175], v[68:71]
	v_mfma_f32_16x16x32_f16 v[64:67], v[202:205], v[172:175], v[64:67]
	s_barrier
	s_mov_b32 m0, s59
	ds_read_b128 v[136:139], v232 offset:49152
	ds_read_b128 v[148:151], v232 offset:50176
	ds_read_b128 v[152:155], v232 offset:51200
	ds_read_b128 v[156:159], v232 offset:52224
	ds_read_b128 v[160:163], v232 offset:53248
	ds_read_b128 v[164:167], v232 offset:54272
	ds_read_b128 v[168:171], v232 offset:55296
	ds_read_b128 v[172:175], v232 offset:56320
	global_load_lds_dwordx4 v176, s[94:95]
	s_mov_b32 m0, s60
	s_nop 0
	global_load_lds_dwordx4 v180, s[94:95]
	s_waitcnt vmcnt(10)
	s_barrier
	s_waitcnt lgkmcnt(0)
	v_mfma_f32_16x16x32_f16 v[60:63], v[72:75], v[136:139], v[60:63]
	v_mfma_f32_16x16x32_f16 v[56:59], v[88:91], v[136:139], v[56:59]
	v_mfma_f32_16x16x32_f16 v[44:47], v[72:75], v[152:155], v[44:47]
	v_mfma_f32_16x16x32_f16 v[40:43], v[88:91], v[152:155], v[40:43]
	v_mfma_f32_16x16x32_f16 v[28:31], v[72:75], v[160:163], v[28:31]
	v_mfma_f32_16x16x32_f16 v[24:27], v[88:91], v[160:163], v[24:27]
	v_mfma_f32_16x16x32_f16 v[12:15], v[72:75], v[168:171], v[12:15]
	v_mfma_f32_16x16x32_f16 v[8:11], v[88:91], v[168:171], v[8:11]
	v_mfma_f32_16x16x32_f16 v[60:63], v[80:83], v[148:151], v[60:63]
	v_mfma_f32_16x16x32_f16 v[56:59], v[92:95], v[148:151], v[56:59]
	v_mfma_f32_16x16x32_f16 v[44:47], v[80:83], v[156:159], v[44:47]
	v_mfma_f32_16x16x32_f16 v[40:43], v[92:95], v[156:159], v[40:43]
	v_mfma_f32_16x16x32_f16 v[28:31], v[80:83], v[164:167], v[28:31]
	v_mfma_f32_16x16x32_f16 v[24:27], v[92:95], v[164:167], v[24:27]
	v_mfma_f32_16x16x32_f16 v[12:15], v[80:83], v[172:175], v[12:15]
	v_mfma_f32_16x16x32_f16 v[8:11], v[92:95], v[172:175], v[8:11]
	s_barrier
	s_add_u32 s40, s40, 0xc080
	s_addc_u32 s41, s41, 0
	s_add_i32 s42, s42, s50
	s_mov_b32 m0, s42
	s_nop 0
	global_load_lds_dwordx4 v178, s[40:41]
	s_add_i32 m0, s42, 0x2000
	s_nop 0
	global_load_lds_dwordx4 v182, s[40:41]
	ds_read_b128 v[72:75], v231
	ds_read_b128 v[80:83], v231 offset:1024
	ds_read_b128 v[88:91], v231 offset:2048
	ds_read_b128 v[92:95], v231 offset:3072
	s_waitcnt vmcnt(6)
	s_barrier
	v_mfma_f32_16x16x32_f16 v[52:55], v[190:193], v[136:139], v[52:55]
	v_mfma_f32_16x16x32_f16 v[48:51], v[198:201], v[136:139], v[48:51]
	v_mfma_f32_16x16x32_f16 v[36:39], v[190:193], v[152:155], v[36:39]
	v_mfma_f32_16x16x32_f16 v[32:35], v[198:201], v[152:155], v[32:35]
	v_mfma_f32_16x16x32_f16 v[20:23], v[190:193], v[160:163], v[20:23]
	v_mfma_f32_16x16x32_f16 v[16:19], v[198:201], v[160:163], v[16:19]
	v_mfma_f32_16x16x32_f16 v[4:7], v[190:193], v[168:171], v[4:7]
	v_mfma_f32_16x16x32_f16 v[0:3], v[198:201], v[168:171], v[0:3]
	v_mfma_f32_16x16x32_f16 v[52:55], v[194:197], v[148:151], v[52:55]
	v_mfma_f32_16x16x32_f16 v[48:51], v[202:205], v[148:151], v[48:51]
	v_mfma_f32_16x16x32_f16 v[36:39], v[194:197], v[156:159], v[36:39]
	v_mfma_f32_16x16x32_f16 v[32:35], v[202:205], v[156:159], v[32:35]
	v_mfma_f32_16x16x32_f16 v[20:23], v[194:197], v[164:167], v[20:23]
	v_mfma_f32_16x16x32_f16 v[16:19], v[202:205], v[164:167], v[16:19]
	v_mfma_f32_16x16x32_f16 v[4:7], v[194:197], v[172:175], v[4:7]
	v_mfma_f32_16x16x32_f16 v[0:3], v[202:205], v[172:175], v[0:3]
	s_barrier
	s_add_i32 s87, s87, 2
	s_add_u32 s38, s38, 0x100
	s_addc_u32 s39, s39, 0
	s_add_u32 s85, s85, 0x100
	s_addc_u32 s86, s86, 0
	s_cmp_gt_u32 s87, 9
	s_cbranch_scc0 .LBB8_27
	s_lshl_b32 s92, s84, 8
	s_add_i32 s92, s92, s58
	s_lshl_b32 s93, s83, 8
	s_or_b32 s93, s93, s61
	v_lshlrev_b32_e32 v237, 2, v226
	s_lshl_b32 s96, s93, 2
	s_add_u32 s94, s16, s96
	s_addc_u32 s95, s17, 0
	global_load_dwordx4 v[72:75], v237, s[94:95] offset:0
	global_load_dwordx4 v[80:83], v237, s[94:95] offset:16
	global_load_dwordx4 v[88:91], v237, s[94:95] offset:128
	global_load_dwordx4 v[92:95], v237, s[94:95] offset:144
	s_add_u32 s94, s18, s96
	s_addc_u32 s95, s19, 0
	global_load_dwordx4 v[136:139], v237, s[94:95] offset:0
	global_load_dwordx4 v[148:151], v237, s[94:95] offset:16
	global_load_dwordx4 v[152:155], v237, s[94:95] offset:128
	global_load_dwordx4 v[156:159], v237, s[94:95] offset:144
	s_add_u32 s94, s14, s96
	s_addc_u32 s95, s15, 0
	global_load_dwordx4 v[160:163], v237, s[94:95] offset:0
	global_load_dwordx4 v[164:167], v237, s[94:95] offset:16
	global_load_dwordx4 v[168:171], v237, s[94:95] offset:128
	global_load_dwordx4 v[172:175], v237, s[94:95] offset:144
	v_lshlrev_b32_e32 v190, 3, v227
	s_lshl_b32 s96, s92, 3
	s_add_u32 s94, s12, s96
	s_addc_u32 s95, s13, 0
	global_load_dwordx2 v[238:239], v190, s[94:95] offset:0
	global_load_dwordx2 v[192:193], v190, s[94:95] offset:128
	global_load_dwordx2 v[194:195], v190, s[94:95] offset:256
	global_load_dwordx2 v[196:197], v190, s[94:95] offset:384
	global_load_dwordx2 v[198:199], v190, s[94:95] offset:1024
	global_load_dwordx2 v[200:201], v190, s[94:95] offset:1152
	global_load_dwordx2 v[202:203], v190, s[94:95] offset:1280
	global_load_dwordx2 v[204:205], v190, s[94:95] offset:1408
	v_mul_u32_u24_e32 v191, 0x600, v227
	v_lshl_add_u32 v191, v226, 1, v191
	s_mul_i32 s96, s92, 0x600
	s_lshl_b32 s97, s93, 1
	s_add_u32 s96, s96, s97
	s_add_u32 s98, s10, s96
	s_addc_u32 s99, s11, 0
	s_add_u32 s94, s98, 0x0
	s_addc_u32 s95, s99, 0
	global_load_dwordx4 v[208:211], v191, s[94:95] offset:0 nt
	global_load_dwordx4 v[212:215], v191, s[94:95] offset:64 nt
	s_add_u32 s94, s98, 0x6000
	s_addc_u32 s95, s99, 0
	global_load_dwordx4 v[216:219], v191, s[94:95] offset:0 nt
	global_load_dwordx4 v[220:223], v191, s[94:95] offset:64 nt
	v_add_u32_e32 v224, s92, v229
	v_mul_u32_u24_e32 v224, 0x600, v224
	s_lshl_b32 s97, s93, 1
	v_add3_u32 v224, v224, v230, s97
	s_lshl_b32 s96, s83, 2
	s_lshr_b32 s97, s61, 6
	s_add_u32 s96, s96, s97
	s_lshl_b32 s96, s96, 19
	s_lshl_b32 s97, s92, 3
	s_add_u32 s96, s96, s97
	s_add_u32 s100, s28, s96
	s_addc_u32 s101, s29, 0
	s_waitcnt vmcnt(19)
	v_pk_add_f32 v[72:73], v[72:73], v[136:137]
	v_pk_add_f32 v[74:75], v[74:75], v[138:139]
	s_waitcnt vmcnt(18)
	v_pk_add_f32 v[80:81], v[80:81], v[148:149]
	v_pk_add_f32 v[82:83], v[82:83], v[150:151]
	s_waitcnt vmcnt(17)
	v_pk_add_f32 v[88:89], v[88:89], v[152:153]
	v_pk_add_f32 v[90:91], v[90:91], v[154:155]
	s_waitcnt vmcnt(16)
	v_pk_add_f32 v[92:93], v[92:93], v[156:157]
	v_pk_add_f32 v[94:95], v[94:95], v[158:159]
	v_pk_add_f32 v[144:145], v[144:145], v[72:73]
	v_pk_add_f32 v[146:147], v[146:147], v[74:75]
	v_pk_add_f32 v[124:125], v[124:125], v[72:73]
	v_pk_add_f32 v[126:127], v[126:127], v[74:75]
	v_pk_add_f32 v[108:109], v[108:109], v[72:73]
	v_pk_add_f32 v[110:111], v[110:111], v[74:75]
	v_pk_add_f32 v[84:85], v[84:85], v[72:73]
	v_pk_add_f32 v[86:87], v[86:87], v[74:75]
	v_pk_add_f32 v[60:61], v[60:61], v[72:73]
	v_pk_add_f32 v[62:63], v[62:63], v[74:75]
	v_pk_add_f32 v[44:45], v[44:45], v[72:73]
	v_pk_add_f32 v[46:47], v[46:47], v[74:75]
	v_pk_add_f32 v[28:29], v[28:29], v[72:73]
	v_pk_add_f32 v[30:31], v[30:31], v[74:75]
	v_pk_add_f32 v[12:13], v[12:13], v[72:73]
	v_pk_add_f32 v[14:15], v[14:15], v[74:75]
	v_pk_add_f32 v[140:141], v[140:141], v[80:81]
	v_pk_add_f32 v[142:143], v[142:143], v[82:83]
	v_pk_add_f32 v[120:121], v[120:121], v[80:81]
	v_pk_add_f32 v[122:123], v[122:123], v[82:83]
	v_pk_add_f32 v[104:105], v[104:105], v[80:81]
	v_pk_add_f32 v[106:107], v[106:107], v[82:83]
	v_pk_add_f32 v[76:77], v[76:77], v[80:81]
	v_pk_add_f32 v[78:79], v[78:79], v[82:83]
	v_pk_add_f32 v[56:57], v[56:57], v[80:81]
	v_pk_add_f32 v[58:59], v[58:59], v[82:83]
	v_pk_add_f32 v[40:41], v[40:41], v[80:81]
	v_pk_add_f32 v[42:43], v[42:43], v[82:83]
	v_pk_add_f32 v[24:25], v[24:25], v[80:81]
	v_pk_add_f32 v[26:27], v[26:27], v[82:83]
	v_pk_add_f32 v[8:9], v[8:9], v[80:81]
	v_pk_add_f32 v[10:11], v[10:11], v[82:83]
	v_pk_add_f32 v[132:133], v[132:133], v[88:89]
	v_pk_add_f32 v[134:135], v[134:135], v[90:91]
	v_pk_add_f32 v[116:117], v[116:117], v[88:89]
	v_pk_add_f32 v[118:119], v[118:119], v[90:91]
	v_pk_add_f32 v[100:101], v[100:101], v[88:89]
	v_pk_add_f32 v[102:103], v[102:103], v[90:91]
	v_pk_add_f32 v[68:69], v[68:69], v[88:89]
	v_pk_add_f32 v[70:71], v[70:71], v[90:91]
	v_pk_add_f32 v[52:53], v[52:53], v[88:89]
	v_pk_add_f32 v[54:55], v[54:55], v[90:91]
	v_pk_add_f32 v[36:37], v[36:37], v[88:89]
	v_pk_add_f32 v[38:39], v[38:39], v[90:91]
	v_pk_add_f32 v[20:21], v[20:21], v[88:89]
	v_pk_add_f32 v[22:23], v[22:23], v[90:91]
	v_pk_add_f32 v[4:5], v[4:5], v[88:89]
	v_pk_add_f32 v[6:7], v[6:7], v[90:91]
	v_pk_add_f32 v[128:129], v[128:129], v[92:93]
	v_pk_add_f32 v[130:131], v[130:131], v[94:95]
	v_pk_add_f32 v[112:113], v[112:113], v[92:93]
	v_pk_add_f32 v[114:115], v[114:115], v[94:95]
	v_pk_add_f32 v[96:97], v[96:97], v[92:93]
	v_pk_add_f32 v[98:99], v[98:99], v[94:95]
	v_pk_add_f32 v[64:65], v[64:65], v[92:93]
	v_pk_add_f32 v[66:67], v[66:67], v[94:95]
	v_pk_add_f32 v[48:49], v[48:49], v[92:93]
	v_pk_add_f32 v[50:51], v[50:51], v[94:95]
	v_pk_add_f32 v[32:33], v[32:33], v[92:93]
	v_pk_add_f32 v[34:35], v[34:35], v[94:95]
	v_pk_add_f32 v[16:17], v[16:17], v[92:93]
	v_pk_add_f32 v[18:19], v[18:19], v[94:95]
	v_pk_add_f32 v[0:1], v[0:1], v[92:93]
	v_pk_add_f32 v[2:3], v[2:3], v[94:95]
	s_add_u32 s94, s98, 0xc000
	s_addc_u32 s95, s99, 0
	global_load_dwordx4 v[240:243], v191, s[94:95] offset:0 nt
	global_load_dwordx4 v[244:247], v191, s[94:95] offset:64 nt
	s_add_u32 s94, s98, 0x12000
	s_addc_u32 s95, s99, 0
	global_load_dwordx4 v[248:251], v191, s[94:95] offset:0 nt
	global_load_dwordx4 v[252:255], v191, s[94:95] offset:64 nt
	s_add_u32 s94, s98, 0x30000
	s_addc_u32 s95, s99, 0
	global_load_dwordx4 v[136:139], v191, s[94:95] offset:0 nt
	global_load_dwordx4 v[148:151], v191, s[94:95] offset:64 nt
	s_add_u32 s94, s98, 0x36000
	s_addc_u32 s95, s99, 0
	global_load_dwordx4 v[152:155], v191, s[94:95] offset:0 nt
	global_load_dwordx4 v[156:159], v191, s[94:95] offset:64 nt
	s_waitcnt vmcnt(19)
	s_waitcnt vmcnt(11)
	v_cvt_f32_f16_e32 v72, v208
	v_cvt_f32_f16_sdwa v73, v208 dst_sel:DWORD dst_unused:UNUSED_PAD src0_sel:WORD_1
	v_cvt_f32_f16_e32 v74, v209
	v_cvt_f32_f16_sdwa v75, v209 dst_sel:DWORD dst_unused:UNUSED_PAD src0_sel:WORD_1
	v_cvt_f32_f16_e32 v80, v210
	v_cvt_f32_f16_sdwa v81, v210 dst_sel:DWORD dst_unused:UNUSED_PAD src0_sel:WORD_1
	v_cvt_f32_f16_e32 v82, v211
	v_cvt_f32_f16_sdwa v83, v211 dst_sel:DWORD dst_unused:UNUSED_PAD src0_sel:WORD_1
	v_sub_f32_e32 v72, v72, v238
	v_sub_f32_e32 v73, v73, v238
	v_sub_f32_e32 v74, v74, v238
	v_sub_f32_e32 v75, v75, v238
	v_sub_f32_e32 v80, v80, v238
	v_sub_f32_e32 v81, v81, v238
	v_sub_f32_e32 v82, v82, v238
	v_sub_f32_e32 v83, v83, v238
	v_pk_mul_f32 v[72:73], v[238:239], v[72:73] op_sel:[1,0]
	v_pk_mul_f32 v[74:75], v[238:239], v[74:75] op_sel:[1,0]
	v_pk_mul_f32 v[80:81], v[238:239], v[80:81] op_sel:[1,0]
	v_pk_mul_f32 v[82:83], v[238:239], v[82:83] op_sel:[1,0]
	v_pk_fma_f32 v[144:145], v[72:73], v[160:161], v[144:145]
	v_pk_fma_f32 v[146:147], v[74:75], v[162:163], v[146:147]
	v_pk_fma_f32 v[140:141], v[80:81], v[164:165], v[140:141]
	v_pk_fma_f32 v[142:143], v[82:83], v[166:167], v[142:143]
	v_cvt_pk_f16_f32 v144, v144, v145
	v_cvt_pk_f16_f32 v145, v146, v147
	v_cvt_pk_f16_f32 v146, v140, v141
	v_cvt_pk_f16_f32 v147, v142, v143
	ds_write_b128 v235, v[144:147]
	v_fma_mix_f32 v206, v144, 1.0, 0 op_sel_hi:[1,0,0]
	v_fma_mix_f32 v207, v144, v144, 0 op_sel_hi:[1,1,0]
	v_fma_mix_f32 v206, v144, 1.0, v206 op_sel:[1,0,0] op_sel_hi:[1,0,0]
	v_fma_mix_f32 v207, v144, v144, v207 op_sel:[1,1,0] op_sel_hi:[1,1,0]
	v_fma_mix_f32 v206, v145, 1.0, v206 op_sel_hi:[1,0,0]
	v_fma_mix_f32 v207, v145, v145, v207 op_sel_hi:[1,1,0]
	v_fma_mix_f32 v206, v145, 1.0, v206 op_sel:[1,0,0] op_sel_hi:[1,0,0]
	v_fma_mix_f32 v207, v145, v145, v207 op_sel:[1,1,0] op_sel_hi:[1,1,0]
	v_fma_mix_f32 v206, v146, 1.0, v206 op_sel_hi:[1,0,0]
	v_fma_mix_f32 v207, v146, v146, v207 op_sel_hi:[1,1,0]
	v_fma_mix_f32 v206, v146, 1.0, v206 op_sel:[1,0,0] op_sel_hi:[1,0,0]
	v_fma_mix_f32 v207, v146, v146, v207 op_sel:[1,1,0] op_sel_hi:[1,1,0]
	v_fma_mix_f32 v206, v147, 1.0, v206 op_sel_hi:[1,0,0]
	v_fma_mix_f32 v207, v147, v147, v207 op_sel_hi:[1,1,0]
	v_fma_mix_f32 v206, v147, 1.0, v206 op_sel:[1,0,0] op_sel_hi:[1,0,0]
	v_fma_mix_f32 v207, v147, v147, v207 op_sel:[1,1,0] op_sel_hi:[1,1,0]
	s_waitcnt vmcnt(10)
	v_cvt_f32_f16_e32 v72, v212
	v_cvt_f32_f16_sdwa v73, v212 dst_sel:DWORD dst_unused:UNUSED_PAD src0_sel:WORD_1
	v_cvt_f32_f16_e32 v74, v213
	v_cvt_f32_f16_sdwa v75, v213 dst_sel:DWORD dst_unused:UNUSED_PAD src0_sel:WORD_1
	v_cvt_f32_f16_e32 v80, v214
	v_cvt_f32_f16_sdwa v81, v214 dst_sel:DWORD dst_unused:UNUSED_PAD src0_sel:WORD_1
	v_cvt_f32_f16_e32 v82, v215
	v_cvt_f32_f16_sdwa v83, v215 dst_sel:DWORD dst_unused:UNUSED_PAD src0_sel:WORD_1
	v_sub_f32_e32 v72, v72, v238
	v_sub_f32_e32 v73, v73, v238
	v_sub_f32_e32 v74, v74, v238
	v_sub_f32_e32 v75, v75, v238
	v_sub_f32_e32 v80, v80, v238
	v_sub_f32_e32 v81, v81, v238
	v_sub_f32_e32 v82, v82, v238
	v_sub_f32_e32 v83, v83, v238
	v_pk_mul_f32 v[72:73], v[238:239], v[72:73] op_sel:[1,0]
	v_pk_mul_f32 v[74:75], v[238:239], v[74:75] op_sel:[1,0]
	v_pk_mul_f32 v[80:81], v[238:239], v[80:81] op_sel:[1,0]
	v_pk_mul_f32 v[82:83], v[238:239], v[82:83] op_sel:[1,0]
	v_pk_fma_f32 v[132:133], v[72:73], v[168:169], v[132:133]
	v_pk_fma_f32 v[134:135], v[74:75], v[170:171], v[134:135]
	v_pk_fma_f32 v[128:129], v[80:81], v[172:173], v[128:129]
	v_pk_fma_f32 v[130:131], v[82:83], v[174:175], v[130:131]
	v_cvt_pk_f16_f32 v132, v132, v133
	v_cvt_pk_f16_f32 v133, v134, v135
	v_cvt_pk_f16_f32 v134, v128, v129
	v_cvt_pk_f16_f32 v135, v130, v131
	ds_write_b128 v235, v[132:135] offset:64
	v_fma_mix_f32 v206, v132, 1.0, v206 op_sel_hi:[1,0,0]
	v_fma_mix_f32 v207, v132, v132, v207 op_sel_hi:[1,1,0]
	v_fma_mix_f32 v206, v132, 1.0, v206 op_sel:[1,0,0] op_sel_hi:[1,0,0]
	v_fma_mix_f32 v207, v132, v132, v207 op_sel:[1,1,0] op_sel_hi:[1,1,0]
	v_fma_mix_f32 v206, v133, 1.0, v206 op_sel_hi:[1,0,0]
	v_fma_mix_f32 v207, v133, v133, v207 op_sel_hi:[1,1,0]
	v_fma_mix_f32 v206, v133, 1.0, v206 op_sel:[1,0,0] op_sel_hi:[1,0,0]
	v_fma_mix_f32 v207, v133, v133, v207 op_sel:[1,1,0] op_sel_hi:[1,1,0]
	v_fma_mix_f32 v206, v134, 1.0, v206 op_sel_hi:[1,0,0]
	v_fma_mix_f32 v207, v134, v134, v207 op_sel_hi:[1,1,0]
	v_fma_mix_f32 v206, v134, 1.0, v206 op_sel:[1,0,0] op_sel_hi:[1,0,0]
	v_fma_mix_f32 v207, v134, v134, v207 op_sel:[1,1,0] op_sel_hi:[1,1,0]
	v_fma_mix_f32 v206, v135, 1.0, v206 op_sel_hi:[1,0,0]
	v_fma_mix_f32 v207, v135, v135, v207 op_sel_hi:[1,1,0]
	v_fma_mix_f32 v206, v135, 1.0, v206 op_sel:[1,0,0] op_sel_hi:[1,0,0]
	v_fma_mix_f32 v207, v135, v135, v207 op_sel:[1,1,0] op_sel_hi:[1,1,0]
	ds_read_b128 v[88:91], v236
	ds_read_b128 v[92:95], v236 offset:1152
	s_waitcnt vmcnt(9)
	v_cvt_f32_f16_e32 v72, v216
	v_cvt_f32_f16_sdwa v73, v216 dst_sel:DWORD dst_unused:UNUSED_PAD src0_sel:WORD_1
	v_cvt_f32_f16_e32 v74, v217
	v_cvt_f32_f16_sdwa v75, v217 dst_sel:DWORD dst_unused:UNUSED_PAD src0_sel:WORD_1
	v_cvt_f32_f16_e32 v80, v218
	v_cvt_f32_f16_sdwa v81, v218 dst_sel:DWORD dst_unused:UNUSED_PAD src0_sel:WORD_1
	v_cvt_f32_f16_e32 v82, v219
	v_cvt_f32_f16_sdwa v83, v219 dst_sel:DWORD dst_unused:UNUSED_PAD src0_sel:WORD_1
	v_sub_f32_e32 v72, v72, v192
	v_sub_f32_e32 v73, v73, v192
	v_sub_f32_e32 v74, v74, v192
	v_sub_f32_e32 v75, v75, v192
	v_sub_f32_e32 v80, v80, v192
	v_sub_f32_e32 v81, v81, v192
	v_sub_f32_e32 v82, v82, v192
	v_sub_f32_e32 v83, v83, v192
	v_pk_mul_f32 v[72:73], v[192:193], v[72:73] op_sel:[1,0]
	v_pk_mul_f32 v[74:75], v[192:193], v[74:75] op_sel:[1,0]
	v_pk_mul_f32 v[80:81], v[192:193], v[80:81] op_sel:[1,0]
	v_pk_mul_f32 v[82:83], v[192:193], v[82:83] op_sel:[1,0]
	v_pk_fma_f32 v[124:125], v[72:73], v[160:161], v[124:125]
	v_pk_fma_f32 v[126:127], v[74:75], v[162:163], v[126:127]
	v_pk_fma_f32 v[120:121], v[80:81], v[164:165], v[120:121]
	v_pk_fma_f32 v[122:123], v[82:83], v[166:167], v[122:123]
	v_cvt_pk_f16_f32 v124, v124, v125
	v_cvt_pk_f16_f32 v125, v126, v127
	v_cvt_pk_f16_f32 v126, v120, v121
	v_cvt_pk_f16_f32 v127, v122, v123
	s_waitcnt lgkmcnt(0)
	buffer_store_dwordx4 v[88:91], v224, s[24:27], 0 offen nt
	v_add_u32_e32 v82, 0x3000, v224
	buffer_store_dwordx4 v[92:95], v82, s[24:27], 0 offen nt
	ds_write_b128 v235, v[124:127]
	v_fma_mix_f32 v140, v124, 1.0, 0 op_sel_hi:[1,0,0]
	v_fma_mix_f32 v141, v124, v124, 0 op_sel_hi:[1,1,0]
	v_fma_mix_f32 v140, v124, 1.0, v140 op_sel:[1,0,0] op_sel_hi:[1,0,0]
	v_fma_mix_f32 v141, v124, v124, v141 op_sel:[1,1,0] op_sel_hi:[1,1,0]
	v_fma_mix_f32 v140, v125, 1.0, v140 op_sel_hi:[1,0,0]
	v_fma_mix_f32 v141, v125, v125, v141 op_sel_hi:[1,1,0]
	v_fma_mix_f32 v140, v125, 1.0, v140 op_sel:[1,0,0] op_sel_hi:[1,0,0]
	v_fma_mix_f32 v141, v125, v125, v141 op_sel:[1,1,0] op_sel_hi:[1,1,0]
	v_fma_mix_f32 v140, v126, 1.0, v140 op_sel_hi:[1,0,0]
	v_fma_mix_f32 v141, v126, v126, v141 op_sel_hi:[1,1,0]
	v_fma_mix_f32 v140, v126, 1.0, v140 op_sel:[1,0,0] op_sel_hi:[1,0,0]
	v_fma_mix_f32 v141, v126, v126, v141 op_sel:[1,1,0] op_sel_hi:[1,1,0]
	v_fma_mix_f32 v140, v127, 1.0, v140 op_sel_hi:[1,0,0]
	v_fma_mix_f32 v141, v127, v127, v141 op_sel_hi:[1,1,0]
	v_fma_mix_f32 v140, v127, 1.0, v140 op_sel:[1,0,0] op_sel_hi:[1,0,0]
	v_fma_mix_f32 v141, v127, v127, v141 op_sel:[1,1,0] op_sel_hi:[1,1,0]
	s_waitcnt vmcnt(10)
	v_cvt_f32_f16_e32 v72, v220
	v_cvt_f32_f16_sdwa v73, v220 dst_sel:DWORD dst_unused:UNUSED_PAD src0_sel:WORD_1
	v_cvt_f32_f16_e32 v74, v221
	v_cvt_f32_f16_sdwa v75, v221 dst_sel:DWORD dst_unused:UNUSED_PAD src0_sel:WORD_1
	v_cvt_f32_f16_e32 v80, v222
	v_cvt_f32_f16_sdwa v81, v222 dst_sel:DWORD dst_unused:UNUSED_PAD src0_sel:WORD_1
	v_cvt_f32_f16_e32 v82, v223
	v_cvt_f32_f16_sdwa v83, v223 dst_sel:DWORD dst_unused:UNUSED_PAD src0_sel:WORD_1
	v_sub_f32_e32 v72, v72, v192
	v_sub_f32_e32 v73, v73, v192
	v_sub_f32_e32 v74, v74, v192
	v_sub_f32_e32 v75, v75, v192
	v_sub_f32_e32 v80, v80, v192
	v_sub_f32_e32 v81, v81, v192
	v_sub_f32_e32 v82, v82, v192
	v_sub_f32_e32 v83, v83, v192
	v_pk_mul_f32 v[72:73], v[192:193], v[72:73] op_sel:[1,0]
	v_pk_mul_f32 v[74:75], v[192:193], v[74:75] op_sel:[1,0]
	v_pk_mul_f32 v[80:81], v[192:193], v[80:81] op_sel:[1,0]
	v_pk_mul_f32 v[82:83], v[192:193], v[82:83] op_sel:[1,0]
	v_pk_fma_f32 v[116:117], v[72:73], v[168:169], v[116:117]
	v_pk_fma_f32 v[118:119], v[74:75], v[170:171], v[118:119]
	v_pk_fma_f32 v[112:113], v[80:81], v[172:173], v[112:113]
	v_pk_fma_f32 v[114:115], v[82:83], v[174:175], v[114:115]
	v_cvt_pk_f16_f32 v116, v116, v117
	v_cvt_pk_f16_f32 v117, v118, v119
	v_cvt_pk_f16_f32 v118, v112, v113
	v_cvt_pk_f16_f32 v119, v114, v115
	ds_write_b128 v235, v[116:119] offset:64
	v_fma_mix_f32 v140, v116, 1.0, v140 op_sel_hi:[1,0,0]
	v_fma_mix_f32 v141, v116, v116, v141 op_sel_hi:[1,1,0]
	v_fma_mix_f32 v140, v116, 1.0, v140 op_sel:[1,0,0] op_sel_hi:[1,0,0]
	v_fma_mix_f32 v141, v116, v116, v141 op_sel:[1,1,0] op_sel_hi:[1,1,0]
	v_fma_mix_f32 v140, v117, 1.0, v140 op_sel_hi:[1,0,0]
	v_fma_mix_f32 v141, v117, v117, v141 op_sel_hi:[1,1,0]
	v_fma_mix_f32 v140, v117, 1.0, v140 op_sel:[1,0,0] op_sel_hi:[1,0,0]
	v_fma_mix_f32 v141, v117, v117, v141 op_sel:[1,1,0] op_sel_hi:[1,1,0]
	v_fma_mix_f32 v140, v118, 1.0, v140 op_sel_hi:[1,0,0]
	v_fma_mix_f32 v141, v118, v118, v141 op_sel_hi:[1,1,0]
	v_fma_mix_f32 v140, v118, 1.0, v140 op_sel:[1,0,0] op_sel_hi:[1,0,0]
	v_fma_mix_f32 v141, v118, v118, v141 op_sel:[1,1,0] op_sel_hi:[1,1,0]
	v_fma_mix_f32 v140, v119, 1.0, v140 op_sel_hi:[1,0,0]
	v_fma_mix_f32 v141, v119, v119, v141 op_sel_hi:[1,1,0]
	v_fma_mix_f32 v140, v119, 1.0, v140 op_sel:[1,0,0] op_sel_hi:[1,0,0]
	v_fma_mix_f32 v141, v119, v119, v141 op_sel:[1,1,0] op_sel_hi:[1,1,0]
	ds_read_b128 v[208:211], v236
	ds_read_b128 v[128:131], v236 offset:1152
	s_add_u32 s94, s98, 0x3c000
	s_addc_u32 s95, s99, 0
	global_load_dwordx4 v[212:215], v191, s[94:95] offset:0 nt
	global_load_dwordx4 v[144:147], v191, s[94:95] offset:64 nt
	s_add_u32 s94, s98, 0x42000
	s_addc_u32 s95, s99, 0
	global_load_dwordx4 v[132:135], v191, s[94:95] offset:0 nt
	global_load_dwordx4 v[88:91], v191, s[94:95] offset:64 nt
	s_waitcnt vmcnt(13)
	v_cvt_f32_f16_e32 v72, v240
	v_cvt_f32_f16_sdwa v73, v240 dst_sel:DWORD dst_unused:UNUSED_PAD src0_sel:WORD_1
	v_cvt_f32_f16_e32 v74, v241
	v_cvt_f32_f16_sdwa v75, v241 dst_sel:DWORD dst_unused:UNUSED_PAD src0_sel:WORD_1
	v_cvt_f32_f16_e32 v80, v242
	v_cvt_f32_f16_sdwa v81, v242 dst_sel:DWORD dst_unused:UNUSED_PAD src0_sel:WORD_1
	v_cvt_f32_f16_e32 v82, v243
	v_cvt_f32_f16_sdwa v83, v243 dst_sel:DWORD dst_unused:UNUSED_PAD src0_sel:WORD_1
	v_sub_f32_e32 v72, v72, v194
	v_sub_f32_e32 v73, v73, v194
	v_sub_f32_e32 v74, v74, v194
	v_sub_f32_e32 v75, v75, v194
	v_sub_f32_e32 v80, v80, v194
	v_sub_f32_e32 v81, v81, v194
	v_sub_f32_e32 v82, v82, v194
	v_sub_f32_e32 v83, v83, v194
	v_pk_mul_f32 v[72:73], v[194:195], v[72:73] op_sel:[1,0]
	v_pk_mul_f32 v[74:75], v[194:195], v[74:75] op_sel:[1,0]
	v_pk_mul_f32 v[80:81], v[194:195], v[80:81] op_sel:[1,0]
	v_pk_mul_f32 v[82:83], v[194:195], v[82:83] op_sel:[1,0]
	v_pk_fma_f32 v[108:109], v[72:73], v[160:161], v[108:109]
	v_pk_fma_f32 v[110:111], v[74:75], v[162:163], v[110:111]
	v_pk_fma_f32 v[104:105], v[80:81], v[164:165], v[104:105]
	v_pk_fma_f32 v[106:107], v[82:83], v[166:167], v[106:107]
	v_cvt_pk_f16_f32 v108, v108, v109
	v_cvt_pk_f16_f32 v109, v110, v111
	v_cvt_pk_f16_f32 v110, v104, v105
	v_cvt_pk_f16_f32 v111, v106, v107
	s_waitcnt lgkmcnt(0)
	v_add_u32_e32 v83, 0x6000, v224
	buffer_store_dwordx4 v[208:211], v83, s[24:27], 0 offen nt
	v_add_u32_e32 v82, 0x9000, v224
	buffer_store_dwordx4 v[128:131], v82, s[24:27], 0 offen nt
	ds_write_b128 v235, v[108:111]
	v_fma_mix_f32 v142, v108, 1.0, 0 op_sel_hi:[1,0,0]
	v_fma_mix_f32 v143, v108, v108, 0 op_sel_hi:[1,1,0]
	v_fma_mix_f32 v142, v108, 1.0, v142 op_sel:[1,0,0] op_sel_hi:[1,0,0]
	v_fma_mix_f32 v143, v108, v108, v143 op_sel:[1,1,0] op_sel_hi:[1,1,0]
	v_fma_mix_f32 v142, v109, 1.0, v142 op_sel_hi:[1,0,0]
	v_fma_mix_f32 v143, v109, v109, v143 op_sel_hi:[1,1,0]
	v_fma_mix_f32 v142, v109, 1.0, v142 op_sel:[1,0,0] op_sel_hi:[1,0,0]
	v_fma_mix_f32 v143, v109, v109, v143 op_sel:[1,1,0] op_sel_hi:[1,1,0]
	v_fma_mix_f32 v142, v110, 1.0, v142 op_sel_hi:[1,0,0]
	v_fma_mix_f32 v143, v110, v110, v143 op_sel_hi:[1,1,0]
	v_fma_mix_f32 v142, v110, 1.0, v142 op_sel:[1,0,0] op_sel_hi:[1,0,0]
	v_fma_mix_f32 v143, v110, v110, v143 op_sel:[1,1,0] op_sel_hi:[1,1,0]
	v_fma_mix_f32 v142, v111, 1.0, v142 op_sel_hi:[1,0,0]
	v_fma_mix_f32 v143, v111, v111, v143 op_sel_hi:[1,1,0]
	v_fma_mix_f32 v142, v111, 1.0, v142 op_sel:[1,0,0] op_sel_hi:[1,0,0]
	v_fma_mix_f32 v143, v111, v111, v143 op_sel:[1,1,0] op_sel_hi:[1,1,0]
	s_waitcnt vmcnt(14)
	v_cvt_f32_f16_e32 v72, v244
	v_cvt_f32_f16_sdwa v73, v244 dst_sel:DWORD dst_unused:UNUSED_PAD src0_sel:WORD_1
	v_cvt_f32_f16_e32 v74, v245
	v_cvt_f32_f16_sdwa v75, v245 dst_sel:DWORD dst_unused:UNUSED_PAD src0_sel:WORD_1
	v_cvt_f32_f16_e32 v80, v246
	v_cvt_f32_f16_sdwa v81, v246 dst_sel:DWORD dst_unused:UNUSED_PAD src0_sel:WORD_1
	v_cvt_f32_f16_e32 v82, v247
	v_cvt_f32_f16_sdwa v83, v247 dst_sel:DWORD dst_unused:UNUSED_PAD src0_sel:WORD_1
	v_sub_f32_e32 v72, v72, v194
	v_sub_f32_e32 v73, v73, v194
	v_sub_f32_e32 v74, v74, v194
	v_sub_f32_e32 v75, v75, v194
	v_sub_f32_e32 v80, v80, v194
	v_sub_f32_e32 v81, v81, v194
	v_sub_f32_e32 v82, v82, v194
	v_sub_f32_e32 v83, v83, v194
	v_pk_mul_f32 v[72:73], v[194:195], v[72:73] op_sel:[1,0]
	v_pk_mul_f32 v[74:75], v[194:195], v[74:75] op_sel:[1,0]
	v_pk_mul_f32 v[80:81], v[194:195], v[80:81] op_sel:[1,0]
	v_pk_mul_f32 v[82:83], v[194:195], v[82:83] op_sel:[1,0]
	v_pk_fma_f32 v[100:101], v[72:73], v[168:169], v[100:101]
	v_pk_fma_f32 v[102:103], v[74:75], v[170:171], v[102:103]
	v_pk_fma_f32 v[96:97], v[80:81], v[172:173], v[96:97]
	v_pk_fma_f32 v[98:99], v[82:83], v[174:175], v[98:99]
	v_cvt_pk_f16_f32 v100, v100, v101
	v_cvt_pk_f16_f32 v101, v102, v103
	v_cvt_pk_f16_f32 v102, v96, v97
	v_cvt_pk_f16_f32 v103, v98, v99
	ds_write_b128 v235, v[100:103] offset:64
	v_fma_mix_f32 v142, v100, 1.0, v142 op_sel_hi:[1,0,0]
	v_fma_mix_f32 v143, v100, v100, v143 op_sel_hi:[1,1,0]
	v_fma_mix_f32 v142, v100, 1.0, v142 op_sel:[1,0,0] op_sel_hi:[1,0,0]
	v_fma_mix_f32 v143, v100, v100, v143 op_sel:[1,1,0] op_sel_hi:[1,1,0]
	v_fma_mix_f32 v142, v101, 1.0, v142 op_sel_hi:[1,0,0]
	v_fma_mix_f32 v143, v101, v101, v143 op_sel_hi:[1,1,0]
	v_fma_mix_f32 v142, v101, 1.0, v142 op_sel:[1,0,0] op_sel_hi:[1,0,0]
	v_fma_mix_f32 v143, v101, v101, v143 op_sel:[1,1,0] op_sel_hi:[1,1,0]
	v_fma_mix_f32 v142, v102, 1.0, v142 op_sel_hi:[1,0,0]
	v_fma_mix_f32 v143, v102, v102, v143 op_sel_hi:[1,1,0]
	v_fma_mix_f32 v142, v102, 1.0, v142 op_sel:[1,0,0] op_sel_hi:[1,0,0]
	v_fma_mix_f32 v143, v102, v102, v143 op_sel:[1,1,0] op_sel_hi:[1,1,0]
	v_fma_mix_f32 v142, v103, 1.0, v142 op_sel_hi:[1,0,0]
	v_fma_mix_f32 v143, v103, v103, v143 op_sel_hi:[1,1,0]
	v_fma_mix_f32 v142, v103, 1.0, v142 op_sel:[1,0,0] op_sel_hi:[1,0,0]
	v_fma_mix_f32 v143, v103, v103, v143 op_sel:[1,1,0] op_sel_hi:[1,1,0]
	ds_read_b128 v[92:95], v236
	ds_read_b128 v[120:123], v236 offset:1152
	s_waitcnt vmcnt(13)
	v_cvt_f32_f16_e32 v72, v248
	v_cvt_f32_f16_sdwa v73, v248 dst_sel:DWORD dst_unused:UNUSED_PAD src0_sel:WORD_1
	v_cvt_f32_f16_e32 v74, v249
	v_cvt_f32_f16_sdwa v75, v249 dst_sel:DWORD dst_unused:UNUSED_PAD src0_sel:WORD_1
	v_cvt_f32_f16_e32 v80, v250
	v_cvt_f32_f16_sdwa v81, v250 dst_sel:DWORD dst_unused:UNUSED_PAD src0_sel:WORD_1
	v_cvt_f32_f16_e32 v82, v251
	v_cvt_f32_f16_sdwa v83, v251 dst_sel:DWORD dst_unused:UNUSED_PAD src0_sel:WORD_1
	v_sub_f32_e32 v72, v72, v196
	v_sub_f32_e32 v73, v73, v196
	v_sub_f32_e32 v74, v74, v196
	v_sub_f32_e32 v75, v75, v196
	v_sub_f32_e32 v80, v80, v196
	v_sub_f32_e32 v81, v81, v196
	v_sub_f32_e32 v82, v82, v196
	v_sub_f32_e32 v83, v83, v196
	v_pk_mul_f32 v[72:73], v[196:197], v[72:73] op_sel:[1,0]
	v_pk_mul_f32 v[74:75], v[196:197], v[74:75] op_sel:[1,0]
	v_pk_mul_f32 v[80:81], v[196:197], v[80:81] op_sel:[1,0]
	v_pk_mul_f32 v[82:83], v[196:197], v[82:83] op_sel:[1,0]
	v_pk_fma_f32 v[84:85], v[72:73], v[160:161], v[84:85]
	v_pk_fma_f32 v[86:87], v[74:75], v[162:163], v[86:87]
	v_pk_fma_f32 v[76:77], v[80:81], v[164:165], v[76:77]
	v_pk_fma_f32 v[78:79], v[82:83], v[166:167], v[78:79]
	v_cvt_pk_f16_f32 v84, v84, v85
	v_cvt_pk_f16_f32 v85, v86, v87
	v_cvt_pk_f16_f32 v86, v76, v77
	v_cvt_pk_f16_f32 v87, v78, v79
	s_waitcnt lgkmcnt(0)
	v_add_u32_e32 v83, 0xc000, v224
	buffer_store_dwordx4 v[92:95], v83, s[24:27], 0 offen nt
	v_add_u32_e32 v82, 0xf000, v224
	buffer_store_dwordx4 v[120:123], v82, s[24:27], 0 offen nt
	ds_write_b128 v235, v[84:87]
	v_fma_mix_f32 v216, v84, 1.0, 0 op_sel_hi:[1,0,0]
	v_fma_mix_f32 v217, v84, v84, 0 op_sel_hi:[1,1,0]
	v_fma_mix_f32 v216, v84, 1.0, v216 op_sel:[1,0,0] op_sel_hi:[1,0,0]
	v_fma_mix_f32 v217, v84, v84, v217 op_sel:[1,1,0] op_sel_hi:[1,1,0]
	v_fma_mix_f32 v216, v85, 1.0, v216 op_sel_hi:[1,0,0]
	v_fma_mix_f32 v217, v85, v85, v217 op_sel_hi:[1,1,0]
	v_fma_mix_f32 v216, v85, 1.0, v216 op_sel:[1,0,0] op_sel_hi:[1,0,0]
	v_fma_mix_f32 v217, v85, v85, v217 op_sel:[1,1,0] op_sel_hi:[1,1,0]
	v_fma_mix_f32 v216, v86, 1.0, v216 op_sel_hi:[1,0,0]
	v_fma_mix_f32 v217, v86, v86, v217 op_sel_hi:[1,1,0]
	v_fma_mix_f32 v216, v86, 1.0, v216 op_sel:[1,0,0] op_sel_hi:[1,0,0]
	v_fma_mix_f32 v217, v86, v86, v217 op_sel:[1,1,0] op_sel_hi:[1,1,0]
	v_fma_mix_f32 v216, v87, 1.0, v216 op_sel_hi:[1,0,0]
	v_fma_mix_f32 v217, v87, v87, v217 op_sel_hi:[1,1,0]
	v_fma_mix_f32 v216, v87, 1.0, v216 op_sel:[1,0,0] op_sel_hi:[1,0,0]
	v_fma_mix_f32 v217, v87, v87, v217 op_sel:[1,1,0] op_sel_hi:[1,1,0]
	s_waitcnt vmcnt(14)
	v_cvt_f32_f16_e32 v72, v252
	v_cvt_f32_f16_sdwa v73, v252 dst_sel:DWORD dst_unused:UNUSED_PAD src0_sel:WORD_1
	v_cvt_f32_f16_e32 v74, v253
	v_cvt_f32_f16_sdwa v75, v253 dst_sel:DWORD dst_unused:UNUSED_PAD src0_sel:WORD_1
	v_cvt_f32_f16_e32 v80, v254
	v_cvt_f32_f16_sdwa v81, v254 dst_sel:DWORD dst_unused:UNUSED_PAD src0_sel:WORD_1
	v_cvt_f32_f16_e32 v82, v255
	v_cvt_f32_f16_sdwa v83, v255 dst_sel:DWORD dst_unused:UNUSED_PAD src0_sel:WORD_1
	v_sub_f32_e32 v72, v72, v196
	v_sub_f32_e32 v73, v73, v196
	v_sub_f32_e32 v74, v74, v196
	v_sub_f32_e32 v75, v75, v196
	v_sub_f32_e32 v80, v80, v196
	v_sub_f32_e32 v81, v81, v196
	v_sub_f32_e32 v82, v82, v196
	v_sub_f32_e32 v83, v83, v196
	v_pk_mul_f32 v[72:73], v[196:197], v[72:73] op_sel:[1,0]
	v_pk_mul_f32 v[74:75], v[196:197], v[74:75] op_sel:[1,0]
	v_pk_mul_f32 v[80:81], v[196:197], v[80:81] op_sel:[1,0]
	v_pk_mul_f32 v[82:83], v[196:197], v[82:83] op_sel:[1,0]
	v_pk_fma_f32 v[68:69], v[72:73], v[168:169], v[68:69]
	v_pk_fma_f32 v[70:71], v[74:75], v[170:171], v[70:71]
	v_pk_fma_f32 v[64:65], v[80:81], v[172:173], v[64:65]
	v_pk_fma_f32 v[66:67], v[82:83], v[174:175], v[66:67]
	v_cvt_pk_f16_f32 v68, v68, v69
	v_cvt_pk_f16_f32 v69, v70, v71
	v_cvt_pk_f16_f32 v70, v64, v65
	v_cvt_pk_f16_f32 v71, v66, v67
	ds_write_b128 v235, v[68:71] offset:64
	v_fma_mix_f32 v216, v68, 1.0, v216 op_sel_hi:[1,0,0]
	v_fma_mix_f32 v217, v68, v68, v217 op_sel_hi:[1,1,0]
	v_fma_mix_f32 v216, v68, 1.0, v216 op_sel:[1,0,0] op_sel_hi:[1,0,0]
	v_fma_mix_f32 v217, v68, v68, v217 op_sel:[1,1,0] op_sel_hi:[1,1,0]
	v_fma_mix_f32 v216, v69, 1.0, v216 op_sel_hi:[1,0,0]
	v_fma_mix_f32 v217, v69, v69, v217 op_sel_hi:[1,1,0]
	v_fma_mix_f32 v216, v69, 1.0, v216 op_sel:[1,0,0] op_sel_hi:[1,0,0]
	v_fma_mix_f32 v217, v69, v69, v217 op_sel:[1,1,0] op_sel_hi:[1,1,0]
	v_fma_mix_f32 v216, v70, 1.0, v216 op_sel_hi:[1,0,0]
	v_fma_mix_f32 v217, v70, v70, v217 op_sel_hi:[1,1,0]
	v_fma_mix_f32 v216, v70, 1.0, v216 op_sel:[1,0,0] op_sel_hi:[1,0,0]
	v_fma_mix_f32 v217, v70, v70, v217 op_sel:[1,1,0] op_sel_hi:[1,1,0]
	v_fma_mix_f32 v216, v71, 1.0, v216 op_sel_hi:[1,0,0]
	v_fma_mix_f32 v217, v71, v71, v217 op_sel_hi:[1,1,0]
	v_fma_mix_f32 v216, v71, 1.0, v216 op_sel:[1,0,0] op_sel_hi:[1,0,0]
	v_fma_mix_f32 v217, v71, v71, v217 op_sel:[1,1,0] op_sel_hi:[1,1,0]
	ds_read_b128 v[112:115], v236
	ds_read_b128 v[220:223], v236 offset:1152
	s_waitcnt vmcnt(13)
	v_cvt_f32_f16_e32 v72, v136
	v_cvt_f32_f16_sdwa v73, v136 dst_sel:DWORD dst_unused:UNUSED_PAD src0_sel:WORD_1
	v_cvt_f32_f16_e32 v74, v137
	v_cvt_f32_f16_sdwa v75, v137 dst_sel:DWORD dst_unused:UNUSED_PAD src0_sel:WORD_1
	v_cvt_f32_f16_e32 v80, v138
	v_cvt_f32_f16_sdwa v81, v138 dst_sel:DWORD dst_unused:UNUSED_PAD src0_sel:WORD_1
	v_cvt_f32_f16_e32 v82, v139
	v_cvt_f32_f16_sdwa v83, v139 dst_sel:DWORD dst_unused:UNUSED_PAD src0_sel:WORD_1
	v_sub_f32_e32 v72, v72, v198
	v_sub_f32_e32 v73, v73, v198
	v_sub_f32_e32 v74, v74, v198
	v_sub_f32_e32 v75, v75, v198
	v_sub_f32_e32 v80, v80, v198
	v_sub_f32_e32 v81, v81, v198
	v_sub_f32_e32 v82, v82, v198
	v_sub_f32_e32 v83, v83, v198
	v_pk_mul_f32 v[72:73], v[198:199], v[72:73] op_sel:[1,0]
	v_pk_mul_f32 v[74:75], v[198:199], v[74:75] op_sel:[1,0]
	v_pk_mul_f32 v[80:81], v[198:199], v[80:81] op_sel:[1,0]
	v_pk_mul_f32 v[82:83], v[198:199], v[82:83] op_sel:[1,0]
	v_pk_fma_f32 v[60:61], v[72:73], v[160:161], v[60:61]
	v_pk_fma_f32 v[62:63], v[74:75], v[162:163], v[62:63]
	v_pk_fma_f32 v[56:57], v[80:81], v[164:165], v[56:57]
	v_pk_fma_f32 v[58:59], v[82:83], v[166:167], v[58:59]
	v_cvt_pk_f16_f32 v60, v60, v61
	v_cvt_pk_f16_f32 v61, v62, v63
	v_cvt_pk_f16_f32 v62, v56, v57
	v_cvt_pk_f16_f32 v63, v58, v59
	s_waitcnt lgkmcnt(0)
	v_add_u32_e32 v83, 0x12000, v224
	buffer_store_dwordx4 v[112:115], v83, s[24:27], 0 offen nt
	v_add_u32_e32 v82, 0x15000, v224
	buffer_store_dwordx4 v[220:223], v82, s[24:27], 0 offen nt
	ds_write_b128 v235, v[60:63]
	v_fma_mix_f32 v218, v60, 1.0, 0 op_sel_hi:[1,0,0]
	v_fma_mix_f32 v219, v60, v60, 0 op_sel_hi:[1,1,0]
	v_fma_mix_f32 v218, v60, 1.0, v218 op_sel:[1,0,0] op_sel_hi:[1,0,0]
	v_fma_mix_f32 v219, v60, v60, v219 op_sel:[1,1,0] op_sel_hi:[1,1,0]
	v_fma_mix_f32 v218, v61, 1.0, v218 op_sel_hi:[1,0,0]
	v_fma_mix_f32 v219, v61, v61, v219 op_sel_hi:[1,1,0]
	v_fma_mix_f32 v218, v61, 1.0, v218 op_sel:[1,0,0] op_sel_hi:[1,0,0]
	v_fma_mix_f32 v219, v61, v61, v219 op_sel:[1,1,0] op_sel_hi:[1,1,0]
	v_fma_mix_f32 v218, v62, 1.0, v218 op_sel_hi:[1,0,0]
	v_fma_mix_f32 v219, v62, v62, v219 op_sel_hi:[1,1,0]
	v_fma_mix_f32 v218, v62, 1.0, v218 op_sel:[1,0,0] op_sel_hi:[1,0,0]
	v_fma_mix_f32 v219, v62, v62, v219 op_sel:[1,1,0] op_sel_hi:[1,1,0]
	v_fma_mix_f32 v218, v63, 1.0, v218 op_sel_hi:[1,0,0]
	v_fma_mix_f32 v219, v63, v63, v219 op_sel_hi:[1,1,0]
	v_fma_mix_f32 v218, v63, 1.0, v218 op_sel:[1,0,0] op_sel_hi:[1,0,0]
	v_fma_mix_f32 v219, v63, v63, v219 op_sel:[1,1,0] op_sel_hi:[1,1,0]
	s_waitcnt vmcnt(14)
	v_cvt_f32_f16_e32 v72, v148
	v_cvt_f32_f16_sdwa v73, v148 dst_sel:DWORD dst_unused:UNUSED_PAD src0_sel:WORD_1
	v_cvt_f32_f16_e32 v74, v149
	v_cvt_f32_f16_sdwa v75, v149 dst_sel:DWORD dst_unused:UNUSED_PAD src0_sel:WORD_1
	v_cvt_f32_f16_e32 v80, v150
	v_cvt_f32_f16_sdwa v81, v150 dst_sel:DWORD dst_unused:UNUSED_PAD src0_sel:WORD_1
	v_cvt_f32_f16_e32 v82, v151
	v_cvt_f32_f16_sdwa v83, v151 dst_sel:DWORD dst_unused:UNUSED_PAD src0_sel:WORD_1
	v_sub_f32_e32 v72, v72, v198
	v_sub_f32_e32 v73, v73, v198
	v_sub_f32_e32 v74, v74, v198
	v_sub_f32_e32 v75, v75, v198
	v_sub_f32_e32 v80, v80, v198
	v_sub_f32_e32 v81, v81, v198
	v_sub_f32_e32 v82, v82, v198
	v_sub_f32_e32 v83, v83, v198
	v_pk_mul_f32 v[72:73], v[198:199], v[72:73] op_sel:[1,0]
	v_pk_mul_f32 v[74:75], v[198:199], v[74:75] op_sel:[1,0]
	v_pk_mul_f32 v[80:81], v[198:199], v[80:81] op_sel:[1,0]
	v_pk_mul_f32 v[82:83], v[198:199], v[82:83] op_sel:[1,0]
	v_pk_fma_f32 v[52:53], v[72:73], v[168:169], v[52:53]
	v_pk_fma_f32 v[54:55], v[74:75], v[170:171], v[54:55]
	v_pk_fma_f32 v[48:49], v[80:81], v[172:173], v[48:49]
	v_pk_fma_f32 v[50:51], v[82:83], v[174:175], v[50:51]
	v_cvt_pk_f16_f32 v52, v52, v53
	v_cvt_pk_f16_f32 v53, v54, v55
	v_cvt_pk_f16_f32 v54, v48, v49
	v_cvt_pk_f16_f32 v55, v50, v51
	ds_write_b128 v235, v[52:55] offset:64
	v_fma_mix_f32 v218, v52, 1.0, v218 op_sel_hi:[1,0,0]
	v_fma_mix_f32 v219, v52, v52, v219 op_sel_hi:[1,1,0]
	v_fma_mix_f32 v218, v52, 1.0, v218 op_sel:[1,0,0] op_sel_hi:[1,0,0]
	v_fma_mix_f32 v219, v52, v52, v219 op_sel:[1,1,0] op_sel_hi:[1,1,0]
	v_fma_mix_f32 v218, v53, 1.0, v218 op_sel_hi:[1,0,0]
	v_fma_mix_f32 v219, v53, v53, v219 op_sel_hi:[1,1,0]
	v_fma_mix_f32 v218, v53, 1.0, v218 op_sel:[1,0,0] op_sel_hi:[1,0,0]
	v_fma_mix_f32 v219, v53, v53, v219 op_sel:[1,1,0] op_sel_hi:[1,1,0]
	v_fma_mix_f32 v218, v54, 1.0, v218 op_sel_hi:[1,0,0]
	v_fma_mix_f32 v219, v54, v54, v219 op_sel_hi:[1,1,0]
	v_fma_mix_f32 v218, v54, 1.0, v218 op_sel:[1,0,0] op_sel_hi:[1,0,0]
	v_fma_mix_f32 v219, v54, v54, v219 op_sel:[1,1,0] op_sel_hi:[1,1,0]
	v_fma_mix_f32 v218, v55, 1.0, v218 op_sel_hi:[1,0,0]
	v_fma_mix_f32 v219, v55, v55, v219 op_sel_hi:[1,1,0]
	v_fma_mix_f32 v218, v55, 1.0, v218 op_sel:[1,0,0] op_sel_hi:[1,0,0]
	v_fma_mix_f32 v219, v55, v55, v219 op_sel:[1,1,0] op_sel_hi:[1,1,0]
	ds_read_b128 v[124:127], v236
	ds_read_b128 v[116:119], v236 offset:1152
	s_waitcnt vmcnt(13)
	v_cvt_f32_f16_e32 v72, v152
	v_cvt_f32_f16_sdwa v73, v152 dst_sel:DWORD dst_unused:UNUSED_PAD src0_sel:WORD_1
	v_cvt_f32_f16_e32 v74, v153
	v_cvt_f32_f16_sdwa v75, v153 dst_sel:DWORD dst_unused:UNUSED_PAD src0_sel:WORD_1
	v_cvt_f32_f16_e32 v80, v154
	v_cvt_f32_f16_sdwa v81, v154 dst_sel:DWORD dst_unused:UNUSED_PAD src0_sel:WORD_1
	v_cvt_f32_f16_e32 v82, v155
	v_cvt_f32_f16_sdwa v83, v155 dst_sel:DWORD dst_unused:UNUSED_PAD src0_sel:WORD_1
	v_sub_f32_e32 v72, v72, v200
	v_sub_f32_e32 v73, v73, v200
	v_sub_f32_e32 v74, v74, v200
	v_sub_f32_e32 v75, v75, v200
	v_sub_f32_e32 v80, v80, v200
	v_sub_f32_e32 v81, v81, v200
	v_sub_f32_e32 v82, v82, v200
	v_sub_f32_e32 v83, v83, v200
	v_pk_mul_f32 v[72:73], v[200:201], v[72:73] op_sel:[1,0]
	v_pk_mul_f32 v[74:75], v[200:201], v[74:75] op_sel:[1,0]
	v_pk_mul_f32 v[80:81], v[200:201], v[80:81] op_sel:[1,0]
	v_pk_mul_f32 v[82:83], v[200:201], v[82:83] op_sel:[1,0]
	v_pk_fma_f32 v[44:45], v[72:73], v[160:161], v[44:45]
	v_pk_fma_f32 v[46:47], v[74:75], v[162:163], v[46:47]
	v_pk_fma_f32 v[40:41], v[80:81], v[164:165], v[40:41]
	v_pk_fma_f32 v[42:43], v[82:83], v[166:167], v[42:43]
	v_cvt_pk_f16_f32 v44, v44, v45
	v_cvt_pk_f16_f32 v45, v46, v47
	v_cvt_pk_f16_f32 v46, v40, v41
	v_cvt_pk_f16_f32 v47, v42, v43
	s_waitcnt lgkmcnt(0)
	v_add_u32_e32 v83, 0x30000, v224
	buffer_store_dwordx4 v[124:127], v83, s[24:27], 0 offen nt
	v_add_u32_e32 v82, 0x33000, v224
	buffer_store_dwordx4 v[116:119], v82, s[24:27], 0 offen nt
	ds_write_b128 v235, v[44:47]
	v_fma_mix_f32 v208, v44, 1.0, 0 op_sel_hi:[1,0,0]
	v_fma_mix_f32 v209, v44, v44, 0 op_sel_hi:[1,1,0]
	v_fma_mix_f32 v208, v44, 1.0, v208 op_sel:[1,0,0] op_sel_hi:[1,0,0]
	v_fma_mix_f32 v209, v44, v44, v209 op_sel:[1,1,0] op_sel_hi:[1,1,0]
	v_fma_mix_f32 v208, v45, 1.0, v208 op_sel_hi:[1,0,0]
	v_fma_mix_f32 v209, v45, v45, v209 op_sel_hi:[1,1,0]
	v_fma_mix_f32 v208, v45, 1.0, v208 op_sel:[1,0,0] op_sel_hi:[1,0,0]
	v_fma_mix_f32 v209, v45, v45, v209 op_sel:[1,1,0] op_sel_hi:[1,1,0]
	v_fma_mix_f32 v208, v46, 1.0, v208 op_sel_hi:[1,0,0]
	v_fma_mix_f32 v209, v46, v46, v209 op_sel_hi:[1,1,0]
	v_fma_mix_f32 v208, v46, 1.0, v208 op_sel:[1,0,0] op_sel_hi:[1,0,0]
	v_fma_mix_f32 v209, v46, v46, v209 op_sel:[1,1,0] op_sel_hi:[1,1,0]
	v_fma_mix_f32 v208, v47, 1.0, v208 op_sel_hi:[1,0,0]
	v_fma_mix_f32 v209, v47, v47, v209 op_sel_hi:[1,1,0]
	v_fma_mix_f32 v208, v47, 1.0, v208 op_sel:[1,0,0] op_sel_hi:[1,0,0]
	v_fma_mix_f32 v209, v47, v47, v209 op_sel:[1,1,0] op_sel_hi:[1,1,0]
	s_waitcnt vmcnt(14)
	v_cvt_f32_f16_e32 v72, v156
	v_cvt_f32_f16_sdwa v73, v156 dst_sel:DWORD dst_unused:UNUSED_PAD src0_sel:WORD_1
	v_cvt_f32_f16_e32 v74, v157
	v_cvt_f32_f16_sdwa v75, v157 dst_sel:DWORD dst_unused:UNUSED_PAD src0_sel:WORD_1
	v_cvt_f32_f16_e32 v80, v158
	v_cvt_f32_f16_sdwa v81, v158 dst_sel:DWORD dst_unused:UNUSED_PAD src0_sel:WORD_1
	v_cvt_f32_f16_e32 v82, v159
	v_cvt_f32_f16_sdwa v83, v159 dst_sel:DWORD dst_unused:UNUSED_PAD src0_sel:WORD_1
	v_sub_f32_e32 v72, v72, v200
	v_sub_f32_e32 v73, v73, v200
	v_sub_f32_e32 v74, v74, v200
	v_sub_f32_e32 v75, v75, v200
	v_sub_f32_e32 v80, v80, v200
	v_sub_f32_e32 v81, v81, v200
	v_sub_f32_e32 v82, v82, v200
	v_sub_f32_e32 v83, v83, v200
	v_pk_mul_f32 v[72:73], v[200:201], v[72:73] op_sel:[1,0]
	v_pk_mul_f32 v[74:75], v[200:201], v[74:75] op_sel:[1,0]
	v_pk_mul_f32 v[80:81], v[200:201], v[80:81] op_sel:[1,0]
	v_pk_mul_f32 v[82:83], v[200:201], v[82:83] op_sel:[1,0]
	v_pk_fma_f32 v[36:37], v[72:73], v[168:169], v[36:37]
	v_pk_fma_f32 v[38:39], v[74:75], v[170:171], v[38:39]
	v_pk_fma_f32 v[32:33], v[80:81], v[172:173], v[32:33]
	v_pk_fma_f32 v[34:35], v[82:83], v[174:175], v[34:35]
	v_cvt_pk_f16_f32 v36, v36, v37
	v_cvt_pk_f16_f32 v37, v38, v39
	v_cvt_pk_f16_f32 v38, v32, v33
	v_cvt_pk_f16_f32 v39, v34, v35
	ds_write_b128 v235, v[36:39] offset:64
	v_fma_mix_f32 v208, v36, 1.0, v208 op_sel_hi:[1,0,0]
	v_fma_mix_f32 v209, v36, v36, v209 op_sel_hi:[1,1,0]
	v_fma_mix_f32 v208, v36, 1.0, v208 op_sel:[1,0,0] op_sel_hi:[1,0,0]
	v_fma_mix_f32 v209, v36, v36, v209 op_sel:[1,1,0] op_sel_hi:[1,1,0]
	v_fma_mix_f32 v208, v37, 1.0, v208 op_sel_hi:[1,0,0]
	v_fma_mix_f32 v209, v37, v37, v209 op_sel_hi:[1,1,0]
	v_fma_mix_f32 v208, v37, 1.0, v208 op_sel:[1,0,0] op_sel_hi:[1,0,0]
	v_fma_mix_f32 v209, v37, v37, v209 op_sel:[1,1,0] op_sel_hi:[1,1,0]
	v_fma_mix_f32 v208, v38, 1.0, v208 op_sel_hi:[1,0,0]
	v_fma_mix_f32 v209, v38, v38, v209 op_sel_hi:[1,1,0]
	v_fma_mix_f32 v208, v38, 1.0, v208 op_sel:[1,0,0] op_sel_hi:[1,0,0]
	v_fma_mix_f32 v209, v38, v38, v209 op_sel:[1,1,0] op_sel_hi:[1,1,0]
	v_fma_mix_f32 v208, v39, 1.0, v208 op_sel_hi:[1,0,0]
	v_fma_mix_f32 v209, v39, v39, v209 op_sel_hi:[1,1,0]
	v_fma_mix_f32 v208, v39, 1.0, v208 op_sel:[1,0,0] op_sel_hi:[1,0,0]
	v_fma_mix_f32 v209, v39, v39, v209 op_sel:[1,1,0] op_sel_hi:[1,1,0]
	ds_read_b128 v[128:131], v236
	ds_read_b128 v[104:107], v236 offset:1152
	s_waitcnt vmcnt(11)
	v_cvt_f32_f16_e32 v72, v212
	v_cvt_f32_f16_sdwa v73, v212 dst_sel:DWORD dst_unused:UNUSED_PAD src0_sel:WORD_1
	v_cvt_f32_f16_e32 v74, v213
	v_cvt_f32_f16_sdwa v75, v213 dst_sel:DWORD dst_unused:UNUSED_PAD src0_sel:WORD_1
	v_cvt_f32_f16_e32 v80, v214
	v_cvt_f32_f16_sdwa v81, v214 dst_sel:DWORD dst_unused:UNUSED_PAD src0_sel:WORD_1
	v_cvt_f32_f16_e32 v82, v215
	v_cvt_f32_f16_sdwa v83, v215 dst_sel:DWORD dst_unused:UNUSED_PAD src0_sel:WORD_1
	v_sub_f32_e32 v72, v72, v202
	v_sub_f32_e32 v73, v73, v202
	v_sub_f32_e32 v74, v74, v202
	v_sub_f32_e32 v75, v75, v202
	v_sub_f32_e32 v80, v80, v202
	v_sub_f32_e32 v81, v81, v202
	v_sub_f32_e32 v82, v82, v202
	v_sub_f32_e32 v83, v83, v202
	v_pk_mul_f32 v[72:73], v[202:203], v[72:73] op_sel:[1,0]
	v_pk_mul_f32 v[74:75], v[202:203], v[74:75] op_sel:[1,0]
	v_pk_mul_f32 v[80:81], v[202:203], v[80:81] op_sel:[1,0]
	v_pk_mul_f32 v[82:83], v[202:203], v[82:83] op_sel:[1,0]
	v_pk_fma_f32 v[28:29], v[72:73], v[160:161], v[28:29]
	v_pk_fma_f32 v[30:31], v[74:75], v[162:163], v[30:31]
	v_pk_fma_f32 v[24:25], v[80:81], v[164:165], v[24:25]
	v_pk_fma_f32 v[26:27], v[82:83], v[166:167], v[26:27]
	v_cvt_pk_f16_f32 v28, v28, v29
	v_cvt_pk_f16_f32 v29, v30, v31
	v_cvt_pk_f16_f32 v30, v24, v25
	v_cvt_pk_f16_f32 v31, v26, v27
	s_waitcnt lgkmcnt(0)
	v_add_u32_e32 v83, 0x36000, v224
	buffer_store_dwordx4 v[128:131], v83, s[24:27], 0 offen nt
	v_add_u32_e32 v82, 0x39000, v224
	buffer_store_dwordx4 v[104:107], v82, s[24:27], 0 offen nt
	ds_write_b128 v235, v[28:31]
	v_fma_mix_f32 v210, v28, 1.0, 0 op_sel_hi:[1,0,0]
	v_fma_mix_f32 v211, v28, v28, 0 op_sel_hi:[1,1,0]
	v_fma_mix_f32 v210, v28, 1.0, v210 op_sel:[1,0,0] op_sel_hi:[1,0,0]
	v_fma_mix_f32 v211, v28, v28, v211 op_sel:[1,1,0] op_sel_hi:[1,1,0]
	v_fma_mix_f32 v210, v29, 1.0, v210 op_sel_hi:[1,0,0]
	v_fma_mix_f32 v211, v29, v29, v211 op_sel_hi:[1,1,0]
	v_fma_mix_f32 v210, v29, 1.0, v210 op_sel:[1,0,0] op_sel_hi:[1,0,0]
	v_fma_mix_f32 v211, v29, v29, v211 op_sel:[1,1,0] op_sel_hi:[1,1,0]
	v_fma_mix_f32 v210, v30, 1.0, v210 op_sel_hi:[1,0,0]
	v_fma_mix_f32 v211, v30, v30, v211 op_sel_hi:[1,1,0]
	v_fma_mix_f32 v210, v30, 1.0, v210 op_sel:[1,0,0] op_sel_hi:[1,0,0]
	v_fma_mix_f32 v211, v30, v30, v211 op_sel:[1,1,0] op_sel_hi:[1,1,0]
	v_fma_mix_f32 v210, v31, 1.0, v210 op_sel_hi:[1,0,0]
	v_fma_mix_f32 v211, v31, v31, v211 op_sel_hi:[1,1,0]
	v_fma_mix_f32 v210, v31, 1.0, v210 op_sel:[1,0,0] op_sel_hi:[1,0,0]
	v_fma_mix_f32 v211, v31, v31, v211 op_sel:[1,1,0] op_sel_hi:[1,1,0]
	s_waitcnt vmcnt(12)
	v_cvt_f32_f16_e32 v72, v144
	v_cvt_f32_f16_sdwa v73, v144 dst_sel:DWORD dst_unused:UNUSED_PAD src0_sel:WORD_1
	v_cvt_f32_f16_e32 v74, v145
	v_cvt_f32_f16_sdwa v75, v145 dst_sel:DWORD dst_unused:UNUSED_PAD src0_sel:WORD_1
	v_cvt_f32_f16_e32 v80, v146
	v_cvt_f32_f16_sdwa v81, v146 dst_sel:DWORD dst_unused:UNUSED_PAD src0_sel:WORD_1
	v_cvt_f32_f16_e32 v82, v147
	v_cvt_f32_f16_sdwa v83, v147 dst_sel:DWORD dst_unused:UNUSED_PAD src0_sel:WORD_1
	v_sub_f32_e32 v72, v72, v202
	v_sub_f32_e32 v73, v73, v202
	v_sub_f32_e32 v74, v74, v202
	v_sub_f32_e32 v75, v75, v202
	v_sub_f32_e32 v80, v80, v202
	v_sub_f32_e32 v81, v81, v202
	v_sub_f32_e32 v82, v82, v202
	v_sub_f32_e32 v83, v83, v202
	v_pk_mul_f32 v[72:73], v[202:203], v[72:73] op_sel:[1,0]
	v_pk_mul_f32 v[74:75], v[202:203], v[74:75] op_sel:[1,0]
	v_pk_mul_f32 v[80:81], v[202:203], v[80:81] op_sel:[1,0]
	v_pk_mul_f32 v[82:83], v[202:203], v[82:83] op_sel:[1,0]
	v_pk_fma_f32 v[20:21], v[72:73], v[168:169], v[20:21]
	v_pk_fma_f32 v[22:23], v[74:75], v[170:171], v[22:23]
	v_pk_fma_f32 v[16:17], v[80:81], v[172:173], v[16:17]
	v_pk_fma_f32 v[18:19], v[82:83], v[174:175], v[18:19]
	v_cvt_pk_f16_f32 v20, v20, v21
	v_cvt_pk_f16_f32 v21, v22, v23
	v_cvt_pk_f16_f32 v22, v16, v17
	v_cvt_pk_f16_f32 v23, v18, v19
	ds_write_b128 v235, v[20:23] offset:64
	v_fma_mix_f32 v210, v20, 1.0, v210 op_sel_hi:[1,0,0]
	v_fma_mix_f32 v211, v20, v20, v211 op_sel_hi:[1,1,0]
	v_fma_mix_f32 v210, v20, 1.0, v210 op_sel:[1,0,0] op_sel_hi:[1,0,0]
	v_fma_mix_f32 v211, v20, v20, v211 op_sel:[1,1,0] op_sel_hi:[1,1,0]
	v_fma_mix_f32 v210, v21, 1.0, v210 op_sel_hi:[1,0,0]
	v_fma_mix_f32 v211, v21, v21, v211 op_sel_hi:[1,1,0]
	v_fma_mix_f32 v210, v21, 1.0, v210 op_sel:[1,0,0] op_sel_hi:[1,0,0]
	v_fma_mix_f32 v211, v21, v21, v211 op_sel:[1,1,0] op_sel_hi:[1,1,0]
	v_fma_mix_f32 v210, v22, 1.0, v210 op_sel_hi:[1,0,0]
	v_fma_mix_f32 v211, v22, v22, v211 op_sel_hi:[1,1,0]
	v_fma_mix_f32 v210, v22, 1.0, v210 op_sel:[1,0,0] op_sel_hi:[1,0,0]
	v_fma_mix_f32 v211, v22, v22, v211 op_sel:[1,1,0] op_sel_hi:[1,1,0]
	v_fma_mix_f32 v210, v23, 1.0, v210 op_sel_hi:[1,0,0]
	v_fma_mix_f32 v211, v23, v23, v211 op_sel_hi:[1,1,0]
	v_fma_mix_f32 v210, v23, 1.0, v210 op_sel:[1,0,0] op_sel_hi:[1,0,0]
	v_fma_mix_f32 v211, v23, v23, v211 op_sel:[1,1,0] op_sel_hi:[1,1,0]
	ds_read_b128 v[240:243], v236
	ds_read_b128 v[96:99], v236 offset:1152
	s_waitcnt vmcnt(11)
	v_cvt_f32_f16_e32 v72, v132
	v_cvt_f32_f16_sdwa v73, v132 dst_sel:DWORD dst_unused:UNUSED_PAD src0_sel:WORD_1
	v_cvt_f32_f16_e32 v74, v133
	v_cvt_f32_f16_sdwa v75, v133 dst_sel:DWORD dst_unused:UNUSED_PAD src0_sel:WORD_1
	v_cvt_f32_f16_e32 v80, v134
	v_cvt_f32_f16_sdwa v81, v134 dst_sel:DWORD dst_unused:UNUSED_PAD src0_sel:WORD_1
	v_cvt_f32_f16_e32 v82, v135
	v_cvt_f32_f16_sdwa v83, v135 dst_sel:DWORD dst_unused:UNUSED_PAD src0_sel:WORD_1
	v_sub_f32_e32 v72, v72, v204
	v_sub_f32_e32 v73, v73, v204
	v_sub_f32_e32 v74, v74, v204
	v_sub_f32_e32 v75, v75, v204
	v_sub_f32_e32 v80, v80, v204
	v_sub_f32_e32 v81, v81, v204
	v_sub_f32_e32 v82, v82, v204
	v_sub_f32_e32 v83, v83, v204
	v_pk_mul_f32 v[72:73], v[204:205], v[72:73] op_sel:[1,0]
	v_pk_mul_f32 v[74:75], v[204:205], v[74:75] op_sel:[1,0]
	v_pk_mul_f32 v[80:81], v[204:205], v[80:81] op_sel:[1,0]
	v_pk_mul_f32 v[82:83], v[204:205], v[82:83] op_sel:[1,0]
	v_pk_fma_f32 v[12:13], v[72:73], v[160:161], v[12:13]
	v_pk_fma_f32 v[14:15], v[74:75], v[162:163], v[14:15]
	v_pk_fma_f32 v[8:9], v[80:81], v[164:165], v[8:9]
	v_pk_fma_f32 v[10:11], v[82:83], v[166:167], v[10:11]
	v_cvt_pk_f16_f32 v12, v12, v13
	v_cvt_pk_f16_f32 v13, v14, v15
	v_cvt_pk_f16_f32 v14, v8, v9
	v_cvt_pk_f16_f32 v15, v10, v11
	s_waitcnt lgkmcnt(0)
	v_add_u32_e32 v83, 0x3c000, v224
	buffer_store_dwordx4 v[240:243], v83, s[24:27], 0 offen nt
	v_add_u32_e32 v82, 0x3f000, v224
	buffer_store_dwordx4 v[96:99], v82, s[24:27], 0 offen nt
	ds_write_b128 v235, v[12:15]
	v_fma_mix_f32 v244, v12, 1.0, 0 op_sel_hi:[1,0,0]
	v_fma_mix_f32 v245, v12, v12, 0 op_sel_hi:[1,1,0]
	v_fma_mix_f32 v244, v12, 1.0, v244 op_sel:[1,0,0] op_sel_hi:[1,0,0]
	v_fma_mix_f32 v245, v12, v12, v245 op_sel:[1,1,0] op_sel_hi:[1,1,0]
	v_fma_mix_f32 v244, v13, 1.0, v244 op_sel_hi:[1,0,0]
	v_fma_mix_f32 v245, v13, v13, v245 op_sel_hi:[1,1,0]
	v_fma_mix_f32 v244, v13, 1.0, v244 op_sel:[1,0,0] op_sel_hi:[1,0,0]
	v_fma_mix_f32 v245, v13, v13, v245 op_sel:[1,1,0] op_sel_hi:[1,1,0]
	v_fma_mix_f32 v244, v14, 1.0, v244 op_sel_hi:[1,0,0]
	v_fma_mix_f32 v245, v14, v14, v245 op_sel_hi:[1,1,0]
	v_fma_mix_f32 v244, v14, 1.0, v244 op_sel:[1,0,0] op_sel_hi:[1,0,0]
	v_fma_mix_f32 v245, v14, v14, v245 op_sel:[1,1,0] op_sel_hi:[1,1,0]
	v_fma_mix_f32 v244, v15, 1.0, v244 op_sel_hi:[1,0,0]
	v_fma_mix_f32 v245, v15, v15, v245 op_sel_hi:[1,1,0]
	v_fma_mix_f32 v244, v15, 1.0, v244 op_sel:[1,0,0] op_sel_hi:[1,0,0]
	v_fma_mix_f32 v245, v15, v15, v245 op_sel:[1,1,0] op_sel_hi:[1,1,0]
	s_waitcnt vmcnt(12)
	v_cvt_f32_f16_e32 v72, v88
	v_cvt_f32_f16_sdwa v73, v88 dst_sel:DWORD dst_unused:UNUSED_PAD src0_sel:WORD_1
	v_cvt_f32_f16_e32 v74, v89
	v_cvt_f32_f16_sdwa v75, v89 dst_sel:DWORD dst_unused:UNUSED_PAD src0_sel:WORD_1
	v_cvt_f32_f16_e32 v80, v90
	v_cvt_f32_f16_sdwa v81, v90 dst_sel:DWORD dst_unused:UNUSED_PAD src0_sel:WORD_1
	v_cvt_f32_f16_e32 v82, v91
	v_cvt_f32_f16_sdwa v83, v91 dst_sel:DWORD dst_unused:UNUSED_PAD src0_sel:WORD_1
	v_sub_f32_e32 v72, v72, v204
	v_sub_f32_e32 v73, v73, v204
	v_sub_f32_e32 v74, v74, v204
	v_sub_f32_e32 v75, v75, v204
	v_sub_f32_e32 v80, v80, v204
	v_sub_f32_e32 v81, v81, v204
	v_sub_f32_e32 v82, v82, v204
	v_sub_f32_e32 v83, v83, v204
	v_pk_mul_f32 v[72:73], v[204:205], v[72:73] op_sel:[1,0]
	v_pk_mul_f32 v[74:75], v[204:205], v[74:75] op_sel:[1,0]
	v_pk_mul_f32 v[80:81], v[204:205], v[80:81] op_sel:[1,0]
	v_pk_mul_f32 v[82:83], v[204:205], v[82:83] op_sel:[1,0]
	v_pk_fma_f32 v[4:5], v[72:73], v[168:169], v[4:5]
	v_pk_fma_f32 v[6:7], v[74:75], v[170:171], v[6:7]
	v_pk_fma_f32 v[0:1], v[80:81], v[172:173], v[0:1]
	v_pk_fma_f32 v[2:3], v[82:83], v[174:175], v[2:3]
	v_cvt_pk_f16_f32 v4, v4, v5
	v_cvt_pk_f16_f32 v5, v6, v7
	v_cvt_pk_f16_f32 v6, v0, v1
	v_cvt_pk_f16_f32 v7, v2, v3
	ds_write_b128 v235, v[4:7] offset:64
	v_fma_mix_f32 v244, v4, 1.0, v244 op_sel_hi:[1,0,0]
	v_fma_mix_f32 v245, v4, v4, v245 op_sel_hi:[1,1,0]
	v_fma_mix_f32 v244, v4, 1.0, v244 op_sel:[1,0,0] op_sel_hi:[1,0,0]
	v_fma_mix_f32 v245, v4, v4, v245 op_sel:[1,1,0] op_sel_hi:[1,1,0]
	v_fma_mix_f32 v244, v5, 1.0, v244 op_sel_hi:[1,0,0]
	v_fma_mix_f32 v245, v5, v5, v245 op_sel_hi:[1,1,0]
	v_fma_mix_f32 v244, v5, 1.0, v244 op_sel:[1,0,0] op_sel_hi:[1,0,0]
	v_fma_mix_f32 v245, v5, v5, v245 op_sel:[1,1,0] op_sel_hi:[1,1,0]
	v_fma_mix_f32 v244, v6, 1.0, v244 op_sel_hi:[1,0,0]
	v_fma_mix_f32 v245, v6, v6, v245 op_sel_hi:[1,1,0]
	v_fma_mix_f32 v244, v6, 1.0, v244 op_sel:[1,0,0] op_sel_hi:[1,0,0]
	v_fma_mix_f32 v245, v6, v6, v245 op_sel:[1,1,0] op_sel_hi:[1,1,0]
	v_fma_mix_f32 v244, v7, 1.0, v244 op_sel_hi:[1,0,0]
	v_fma_mix_f32 v245, v7, v7, v245 op_sel_hi:[1,1,0]
	v_fma_mix_f32 v244, v7, 1.0, v244 op_sel:[1,0,0] op_sel_hi:[1,0,0]
	v_fma_mix_f32 v245, v7, v7, v245 op_sel:[1,1,0] op_sel_hi:[1,1,0]
	ds_read_b128 v[108:111], v236
	ds_read_b128 v[100:103], v236 offset:1152
	s_waitcnt lgkmcnt(0)
	v_add_u32_e32 v83, 0x42000, v224
	buffer_store_dwordx4 v[108:111], v83, s[24:27], 0 offen nt
	v_add_u32_e32 v82, 0x45000, v224
	buffer_store_dwordx4 v[100:103], v82, s[24:27], 0 offen nt
	v_xor_b32_e32 v225, 16, v234
	v_lshlrev_b32_e32 v225, 2, v225
	v_xor_b32_e32 v246, 32, v234
	v_lshlrev_b32_e32 v246, 2, v246
	ds_bpermute_b32 v92, v225, v206
	ds_bpermute_b32 v93, v225, v207
	ds_bpermute_b32 v94, v225, v140
	ds_bpermute_b32 v95, v225, v141
	ds_bpermute_b32 v120, v225, v142
	ds_bpermute_b32 v121, v225, v143
	ds_bpermute_b32 v122, v225, v216
	ds_bpermute_b32 v123, v225, v217
	s_waitcnt lgkmcnt(0)
	v_pk_add_f32 v[206:207], v[206:207], v[92:93]
	v_pk_add_f32 v[140:141], v[140:141], v[94:95]
	v_pk_add_f32 v[142:143], v[142:143], v[120:121]
	v_pk_add_f32 v[216:217], v[216:217], v[122:123]
	ds_bpermute_b32 v92, v225, v218
	ds_bpermute_b32 v93, v225, v219
	ds_bpermute_b32 v94, v225, v208
	ds_bpermute_b32 v95, v225, v209
	ds_bpermute_b32 v120, v225, v210
	ds_bpermute_b32 v121, v225, v211
	ds_bpermute_b32 v122, v225, v244
	ds_bpermute_b32 v123, v225, v245
	s_waitcnt lgkmcnt(0)
	v_pk_add_f32 v[218:219], v[218:219], v[92:93]
	v_pk_add_f32 v[208:209], v[208:209], v[94:95]
	v_pk_add_f32 v[210:211], v[210:211], v[120:121]
	v_pk_add_f32 v[244:245], v[244:245], v[122:123]
	ds_bpermute_b32 v92, v246, v206
	ds_bpermute_b32 v93, v246, v207
	ds_bpermute_b32 v94, v246, v140
	ds_bpermute_b32 v95, v246, v141
	ds_bpermute_b32 v120, v246, v142
	ds_bpermute_b32 v121, v246, v143
	ds_bpermute_b32 v122, v246, v216
	ds_bpermute_b32 v123, v246, v217
	s_waitcnt lgkmcnt(0)
	v_pk_add_f32 v[206:207], v[206:207], v[92:93]
	v_pk_add_f32 v[140:141], v[140:141], v[94:95]
	v_pk_add_f32 v[142:143], v[142:143], v[120:121]
	v_pk_add_f32 v[216:217], v[216:217], v[122:123]
	ds_bpermute_b32 v92, v246, v218
	ds_bpermute_b32 v93, v246, v219
	ds_bpermute_b32 v94, v246, v208
	ds_bpermute_b32 v95, v246, v209
	ds_bpermute_b32 v120, v246, v210
	ds_bpermute_b32 v121, v246, v211
	ds_bpermute_b32 v122, v246, v244
	ds_bpermute_b32 v123, v246, v245
	s_waitcnt lgkmcnt(0)
	v_pk_add_f32 v[218:219], v[218:219], v[92:93]
	v_pk_add_f32 v[208:209], v[208:209], v[94:95]
	v_pk_add_f32 v[210:211], v[210:211], v[120:121]
	v_pk_add_f32 v[244:245], v[244:245], v[122:123]
	s_mov_b64 exec, 0xffff
	global_store_dwordx2 v190, v[206:207], s[100:101] offset:0
	global_store_dwordx2 v190, v[140:141], s[100:101] offset:128
	global_store_dwordx2 v190, v[142:143], s[100:101] offset:256
	global_store_dwordx2 v190, v[216:217], s[100:101] offset:384
	global_store_dwordx2 v190, v[218:219], s[100:101] offset:1024
	global_store_dwordx2 v190, v[208:209], s[100:101] offset:1152
	global_store_dwordx2 v190, v[210:211], s[100:101] offset:1280
	global_store_dwordx2 v190, v[244:245], s[100:101] offset:1408
	s_mov_b64 exec, -1
	s_mov_b32 s83, s81
	s_mov_b32 s84, s82
	s_mov_b64 s[40:41], s[0:1]
	s_mov_b64 s[38:39], s[8:9]
	s_mov_b64 vcc, s[6:7]
	s_cbranch_vccz .LBB8_12
	s_waitcnt vmcnt(0)
	s_cmpk_gt_u32 s44, 0xff
	s_cbranch_scc1 .LBB8_31
	s_barrier

.LBB8_32:
	s_endpgm
	s_endpgm
	s_endpgm
	s_endpgm
	s_endpgm
	s_endpgm
	s_endpgm
	s_endpgm
	s_endpgm
	s_endpgm
	s_endpgm
	s_endpgm
	s_endpgm
	s_endpgm
	s_endpgm
	s_endpgm
	s_endpgm
	s_endpgm
	s_endpgm
	s_endpgm
	s_endpgm
	s_endpgm
	.section	.rodata,"a",@progbits
	.p2align	6, 0x0

.LBB9_26:
	s_lshl_b32 s34, s70, 8
	s_add_i32 s34, s34, s48
	v_or_b32_e32 v250, s34, v167
	v_ashrrev_i32_e32 v251, 31, v250
	v_lshl_add_u64 v[250:251], v[250:251], 3, s[12:13]
	s_lshl_b32 s35, s68, 8
	s_or_b32 s35, s35, s51
	v_or_b32_e32 v252, s35, v166
	v_ashrrev_i32_e32 v253, 31, v252
	v_lshl_add_u64 v[252:253], v[252:253], 2, s[14:15]
	global_load_dword v226, v[250:251], off offset:4
	global_load_dword v227, v[250:251], off offset:132
	global_load_dword v228, v[250:251], off offset:260
	global_load_dword v229, v[250:251], off offset:388
	global_load_dword v230, v[250:251], off offset:1028
	global_load_dword v231, v[250:251], off offset:1156
	global_load_dword v232, v[250:251], off offset:1284
	global_load_dword v233, v[250:251], off offset:1412
	global_load_dwordx4 v[234:237], v[252:253], off
	global_load_dwordx4 v[238:241], v[252:253], off offset:16
	global_load_dwordx4 v[242:245], v[252:253], off offset:128
	global_load_dwordx4 v[246:249], v[252:253], off offset:144
	s_add_u32 s28, s28, 0x30080
	s_addc_u32 s29, s29, 0
	s_add_u32 s71, s30, 0x100
	v_mov_b32_e32 v0, 0
	s_addc_u32 s72, s31, 0
	s_mov_b32 s73, -2
	v_mov_b32_e32 v1, v0
	v_mov_b32_e32 v2, v0
	v_mov_b32_e32 v3, v0
	v_mov_b32_e32 v4, v0
	v_mov_b32_e32 v5, v0
	v_mov_b32_e32 v6, v0
	v_mov_b32_e32 v7, v0
	v_mov_b32_e32 v12, v0
	v_mov_b32_e32 v13, v0
	v_mov_b32_e32 v14, v0
	v_mov_b32_e32 v15, v0
	v_mov_b32_e32 v20, v0
	v_mov_b32_e32 v21, v0
	v_mov_b32_e32 v22, v0
	v_mov_b32_e32 v23, v0
	v_mov_b32_e32 v28, v0
	v_mov_b32_e32 v29, v0
	v_mov_b32_e32 v30, v0
	v_mov_b32_e32 v31, v0
	v_mov_b32_e32 v36, v0
	v_mov_b32_e32 v37, v0
	v_mov_b32_e32 v38, v0
	v_mov_b32_e32 v39, v0
	v_mov_b32_e32 v44, v0
	v_mov_b32_e32 v45, v0
	v_mov_b32_e32 v46, v0
	v_mov_b32_e32 v47, v0
	v_mov_b32_e32 v52, v0
	v_mov_b32_e32 v53, v0
	v_mov_b32_e32 v54, v0
	v_mov_b32_e32 v55, v0
	v_mov_b32_e32 v8, v0
	v_mov_b32_e32 v9, v0
	v_mov_b32_e32 v10, v0
	v_mov_b32_e32 v11, v0
	v_mov_b32_e32 v16, v0
	v_mov_b32_e32 v17, v0
	v_mov_b32_e32 v18, v0
	v_mov_b32_e32 v19, v0
	v_mov_b32_e32 v24, v0
	v_mov_b32_e32 v25, v0
	v_mov_b32_e32 v26, v0
	v_mov_b32_e32 v27, v0
	v_mov_b32_e32 v32, v0
	v_mov_b32_e32 v33, v0
	v_mov_b32_e32 v34, v0
	v_mov_b32_e32 v35, v0
	v_mov_b32_e32 v40, v0
	v_mov_b32_e32 v41, v0
	v_mov_b32_e32 v42, v0
	v_mov_b32_e32 v43, v0
	v_mov_b32_e32 v48, v0
	v_mov_b32_e32 v49, v0
	v_mov_b32_e32 v50, v0
	v_mov_b32_e32 v51, v0
	v_mov_b32_e32 v56, v0
	v_mov_b32_e32 v57, v0
	v_mov_b32_e32 v58, v0
	v_mov_b32_e32 v59, v0
	v_mov_b32_e32 v60, v0
	v_mov_b32_e32 v61, v0
	v_mov_b32_e32 v62, v0
	v_mov_b32_e32 v63, v0
	v_mov_b32_e32 v64, v0
	v_mov_b32_e32 v65, v0
	v_mov_b32_e32 v66, v0
	v_mov_b32_e32 v67, v0
	v_mov_b32_e32 v68, v0
	v_mov_b32_e32 v69, v0
	v_mov_b32_e32 v70, v0
	v_mov_b32_e32 v71, v0
	v_mov_b32_e32 v76, v0
	v_mov_b32_e32 v77, v0
	v_mov_b32_e32 v78, v0
	v_mov_b32_e32 v79, v0
	v_mov_b32_e32 v84, v0
	v_mov_b32_e32 v85, v0
	v_mov_b32_e32 v86, v0
	v_mov_b32_e32 v87, v0
	v_mov_b32_e32 v92, v0
	v_mov_b32_e32 v93, v0
	v_mov_b32_e32 v94, v0
	v_mov_b32_e32 v95, v0
	v_mov_b32_e32 v100, v0
	v_mov_b32_e32 v101, v0
	v_mov_b32_e32 v102, v0
	v_mov_b32_e32 v103, v0
	v_mov_b32_e32 v112, v0
	v_mov_b32_e32 v113, v0
	v_mov_b32_e32 v114, v0
	v_mov_b32_e32 v115, v0
	v_mov_b32_e32 v116, v0
	v_mov_b32_e32 v117, v0
	v_mov_b32_e32 v118, v0
	v_mov_b32_e32 v119, v0
	v_mov_b32_e32 v72, v0
	v_mov_b32_e32 v73, v0
	v_mov_b32_e32 v74, v0
	v_mov_b32_e32 v75, v0
	v_mov_b32_e32 v80, v0
	v_mov_b32_e32 v81, v0
	v_mov_b32_e32 v82, v0
	v_mov_b32_e32 v83, v0
	v_mov_b32_e32 v88, v0
	v_mov_b32_e32 v89, v0
	v_mov_b32_e32 v90, v0
	v_mov_b32_e32 v91, v0
	v_mov_b32_e32 v96, v0
	v_mov_b32_e32 v97, v0
	v_mov_b32_e32 v98, v0
	v_mov_b32_e32 v99, v0
	v_mov_b32_e32 v104, v0
	v_mov_b32_e32 v105, v0
	v_mov_b32_e32 v106, v0
	v_mov_b32_e32 v107, v0
	v_mov_b32_e32 v108, v0
	v_mov_b32_e32 v109, v0
	v_mov_b32_e32 v110, v0
	v_mov_b32_e32 v111, v0
	v_mov_b32_e32 v120, v0
	v_mov_b32_e32 v121, v0
	v_mov_b32_e32 v122, v0
	v_mov_b32_e32 v123, v0
	v_mov_b32_e32 v124, v0
	v_mov_b32_e32 v125, v0
	v_mov_b32_e32 v126, v0
	v_mov_b32_e32 v127, v0
	ds_read_b128 v[128:131], v172
	ds_read_b128 v[132:135], v172 offset:1024
	ds_read_b128 v[136:139], v172 offset:2048
	ds_read_b128 v[140:143], v172 offset:3072
.LBB9_27:
	s_add_u32 s30, s28, 0xfffd0080
	s_addc_u32 s31, s29, -1
	s_cmp_eq_u32 s73, 8
	s_cselect_b32 s35, s9, s31
	s_cselect_b32 s34, s8, s30
	s_cselect_b32 s31, s1, s72
	s_cselect_b32 s30, s0, s71
	s_add_i32 m0, s43, 0xc000
	ds_read_b128 v[158:161], v173
	ds_read_b128 v[162:165], v173 offset:1024
	ds_read_b128 v[178:181], v173 offset:2048
	ds_read_b128 v[182:185], v173 offset:3072
	ds_read_b128 v[186:189], v173 offset:4096
	ds_read_b128 v[190:193], v173 offset:5120
	ds_read_b128 v[194:197], v173 offset:6144
	ds_read_b128 v[198:201], v173 offset:7168
	global_load_lds_dwordx4 v152, s[28:29]
	s_add_i32 m0, s43, 0xe000
	s_nop 0
	global_load_lds_dwordx4 v154, s[28:29]
	s_waitcnt lgkmcnt(8)
	s_barrier
	s_waitcnt lgkmcnt(0)
	v_mfma_f32_16x16x32_f16 v[124:127], v[128:131], v[158:161], v[124:127]
	v_mfma_f32_16x16x32_f16 v[120:123], v[136:139], v[158:161], v[120:123]
	v_mfma_f32_16x16x32_f16 v[108:111], v[128:131], v[178:181], v[108:111]
	v_mfma_f32_16x16x32_f16 v[104:107], v[136:139], v[178:181], v[104:107]
	v_mfma_f32_16x16x32_f16 v[96:99], v[128:131], v[186:189], v[96:99]
	v_mfma_f32_16x16x32_f16 v[88:91], v[136:139], v[186:189], v[88:91]
	v_mfma_f32_16x16x32_f16 v[80:83], v[128:131], v[194:197], v[80:83]
	v_mfma_f32_16x16x32_f16 v[72:75], v[136:139], v[194:197], v[72:75]
	v_mfma_f32_16x16x32_f16 v[124:127], v[132:135], v[162:165], v[124:127]
	v_mfma_f32_16x16x32_f16 v[120:123], v[140:143], v[162:165], v[120:123]
	v_mfma_f32_16x16x32_f16 v[108:111], v[132:135], v[182:185], v[108:111]
	v_mfma_f32_16x16x32_f16 v[104:107], v[140:143], v[182:185], v[104:107]
	v_mfma_f32_16x16x32_f16 v[96:99], v[132:135], v[190:193], v[96:99]
	v_mfma_f32_16x16x32_f16 v[88:91], v[140:143], v[190:193], v[88:91]
	v_mfma_f32_16x16x32_f16 v[80:83], v[132:135], v[198:201], v[80:83]
	v_mfma_f32_16x16x32_f16 v[72:75], v[140:143], v[198:201], v[72:75]
	s_barrier
	s_add_i32 s74, s65, s42
	s_add_u32 s78, s30, 0x80
	s_addc_u32 s79, s31, 0
	s_mov_b32 m0, s74
	ds_read_b128 v[202:205], v174
	ds_read_b128 v[206:209], v174 offset:1024
	ds_read_b128 v[210:213], v174 offset:2048
	ds_read_b128 v[214:217], v174 offset:3072
	global_load_lds_dwordx4 v146, s[30:31]
	s_add_i32 m0, s74, 0x2000
	s_nop 0
	global_load_lds_dwordx4 v150, s[30:31]
	s_barrier
	s_waitcnt lgkmcnt(0)
	v_mfma_f32_16x16x32_f16 v[116:119], v[202:205], v[158:161], v[116:119]
	v_mfma_f32_16x16x32_f16 v[112:115], v[210:213], v[158:161], v[112:115]
	v_mfma_f32_16x16x32_f16 v[100:103], v[202:205], v[178:181], v[100:103]
	v_mfma_f32_16x16x32_f16 v[92:95], v[210:213], v[178:181], v[92:95]
	v_mfma_f32_16x16x32_f16 v[84:87], v[202:205], v[186:189], v[84:87]
	v_mfma_f32_16x16x32_f16 v[76:79], v[210:213], v[186:189], v[76:79]
	v_mfma_f32_16x16x32_f16 v[68:71], v[202:205], v[194:197], v[68:71]
	v_mfma_f32_16x16x32_f16 v[64:67], v[210:213], v[194:197], v[64:67]
	v_mfma_f32_16x16x32_f16 v[116:119], v[206:209], v[162:165], v[116:119]
	v_mfma_f32_16x16x32_f16 v[112:115], v[214:217], v[162:165], v[112:115]
	v_mfma_f32_16x16x32_f16 v[100:103], v[206:209], v[182:185], v[100:103]
	v_mfma_f32_16x16x32_f16 v[92:95], v[214:217], v[182:185], v[92:95]
	v_mfma_f32_16x16x32_f16 v[84:87], v[206:209], v[190:193], v[84:87]
	v_mfma_f32_16x16x32_f16 v[76:79], v[214:217], v[190:193], v[76:79]
	v_mfma_f32_16x16x32_f16 v[68:71], v[206:209], v[198:201], v[68:71]
	v_mfma_f32_16x16x32_f16 v[64:67], v[214:217], v[198:201], v[64:67]
	s_barrier
	s_mov_b32 m0, s43
	s_add_u32 s80, s34, 0x80
	s_addc_u32 s81, s35, 0
	ds_read_b128 v[158:161], v173 offset:16384
	ds_read_b128 v[162:165], v173 offset:17408
	ds_read_b128 v[178:181], v173 offset:18432
	ds_read_b128 v[182:185], v173 offset:19456
	ds_read_b128 v[186:189], v173 offset:20480
	ds_read_b128 v[190:193], v173 offset:21504
	ds_read_b128 v[194:197], v173 offset:22528
	ds_read_b128 v[198:201], v173 offset:23552
	global_load_lds_dwordx4 v144, s[34:35]
	s_mov_b32 m0, s44
	s_nop 0
	global_load_lds_dwordx4 v148, s[34:35]
	s_waitcnt vmcnt(10)
	s_barrier
	s_waitcnt lgkmcnt(0)
	v_mfma_f32_16x16x32_f16 v[60:63], v[128:131], v[158:161], v[60:63]
	v_mfma_f32_16x16x32_f16 v[56:59], v[136:139], v[158:161], v[56:59]
	v_mfma_f32_16x16x32_f16 v[48:51], v[128:131], v[178:181], v[48:51]
	v_mfma_f32_16x16x32_f16 v[40:43], v[136:139], v[178:181], v[40:43]
	v_mfma_f32_16x16x32_f16 v[32:35], v[128:131], v[186:189], v[32:35]
	v_mfma_f32_16x16x32_f16 v[24:27], v[136:139], v[186:189], v[24:27]
	v_mfma_f32_16x16x32_f16 v[16:19], v[128:131], v[194:197], v[16:19]
	v_mfma_f32_16x16x32_f16 v[8:11], v[136:139], v[194:197], v[8:11]
	v_mfma_f32_16x16x32_f16 v[60:63], v[132:135], v[162:165], v[60:63]
	v_mfma_f32_16x16x32_f16 v[56:59], v[140:143], v[162:165], v[56:59]
	v_mfma_f32_16x16x32_f16 v[48:51], v[132:135], v[182:185], v[48:51]
	v_mfma_f32_16x16x32_f16 v[40:43], v[140:143], v[182:185], v[40:43]
	v_mfma_f32_16x16x32_f16 v[32:35], v[132:135], v[190:193], v[32:35]
	v_mfma_f32_16x16x32_f16 v[24:27], v[140:143], v[190:193], v[24:27]
	v_mfma_f32_16x16x32_f16 v[16:19], v[132:135], v[198:201], v[16:19]
	v_mfma_f32_16x16x32_f16 v[8:11], v[140:143], v[198:201], v[8:11]
	s_barrier
	s_add_u32 s74, s30, 0xc000
	s_addc_u32 s75, s31, 0
	s_add_i32 s76, s66, s42
	s_mov_b32 m0, s76
	s_nop 0
	global_load_lds_dwordx4 v146, s[74:75]
	s_add_i32 m0, s76, 0x2000
	s_nop 0
	global_load_lds_dwordx4 v150, s[74:75]
	s_add_i32 s74, 0, 0x18000
	v_add_u32_e32 v140, s74, v168
	ds_read_b128 v[128:131], v140
	ds_read_b128 v[132:135], v140 offset:1024
	ds_read_b128 v[136:139], v140 offset:2048
	ds_read_b128 v[140:143], v140 offset:3072
	s_waitcnt vmcnt(6)
	s_barrier
	v_mfma_f32_16x16x32_f16 v[52:55], v[202:205], v[158:161], v[52:55]
	v_mfma_f32_16x16x32_f16 v[44:47], v[210:213], v[158:161], v[44:47]
	v_mfma_f32_16x16x32_f16 v[36:39], v[202:205], v[178:181], v[36:39]
	v_mfma_f32_16x16x32_f16 v[28:31], v[210:213], v[178:181], v[28:31]
	v_mfma_f32_16x16x32_f16 v[20:23], v[202:205], v[186:189], v[20:23]
	v_mfma_f32_16x16x32_f16 v[12:15], v[210:213], v[186:189], v[12:15]
	v_mfma_f32_16x16x32_f16 v[4:7], v[202:205], v[194:197], v[4:7]
	v_mfma_f32_16x16x32_f16 v[0:3], v[210:213], v[194:197], v[0:3]
	v_mfma_f32_16x16x32_f16 v[52:55], v[206:209], v[162:165], v[52:55]
	v_mfma_f32_16x16x32_f16 v[44:47], v[214:217], v[162:165], v[44:47]
	v_mfma_f32_16x16x32_f16 v[36:39], v[206:209], v[182:185], v[36:39]
	v_mfma_f32_16x16x32_f16 v[28:31], v[214:217], v[182:185], v[28:31]
	v_mfma_f32_16x16x32_f16 v[20:23], v[206:209], v[190:193], v[20:23]
	v_mfma_f32_16x16x32_f16 v[12:15], v[214:217], v[190:193], v[12:15]
	v_mfma_f32_16x16x32_f16 v[4:7], v[206:209], v[198:201], v[4:7]
	v_mfma_f32_16x16x32_f16 v[0:3], v[214:217], v[198:201], v[0:3]
	s_barrier
	s_add_u32 s34, s34, 0x30000
	s_addc_u32 s35, s35, 0
	s_mov_b32 m0, s45
	ds_read_b128 v[158:161], v173 offset:32768
	ds_read_b128 v[162:165], v173 offset:33792
	ds_read_b128 v[178:181], v173 offset:34816
	ds_read_b128 v[182:185], v173 offset:35840
	ds_read_b128 v[186:189], v173 offset:36864
	ds_read_b128 v[190:193], v173 offset:37888
	ds_read_b128 v[194:197], v173 offset:38912
	ds_read_b128 v[198:201], v173 offset:39936
	global_load_lds_dwordx4 v144, s[34:35]
	s_mov_b32 m0, s46
	s_nop 0
	global_load_lds_dwordx4 v148, s[34:35]
	s_waitcnt lgkmcnt(8)
	s_barrier
	s_waitcnt lgkmcnt(0)
	v_mfma_f32_16x16x32_f16 v[124:127], v[128:131], v[158:161], v[124:127]
	v_mfma_f32_16x16x32_f16 v[120:123], v[136:139], v[158:161], v[120:123]
	v_mfma_f32_16x16x32_f16 v[108:111], v[128:131], v[178:181], v[108:111]
	v_mfma_f32_16x16x32_f16 v[104:107], v[136:139], v[178:181], v[104:107]
	v_mfma_f32_16x16x32_f16 v[96:99], v[128:131], v[186:189], v[96:99]
	v_mfma_f32_16x16x32_f16 v[88:91], v[136:139], v[186:189], v[88:91]
	v_mfma_f32_16x16x32_f16 v[80:83], v[128:131], v[194:197], v[80:83]
	v_mfma_f32_16x16x32_f16 v[72:75], v[136:139], v[194:197], v[72:75]
	v_mfma_f32_16x16x32_f16 v[124:127], v[132:135], v[162:165], v[124:127]
	v_mfma_f32_16x16x32_f16 v[120:123], v[140:143], v[162:165], v[120:123]
	v_mfma_f32_16x16x32_f16 v[108:111], v[132:135], v[182:185], v[108:111]
	v_mfma_f32_16x16x32_f16 v[104:107], v[140:143], v[182:185], v[104:107]
	v_mfma_f32_16x16x32_f16 v[96:99], v[132:135], v[190:193], v[96:99]
	v_mfma_f32_16x16x32_f16 v[88:91], v[140:143], v[190:193], v[88:91]
	v_mfma_f32_16x16x32_f16 v[80:83], v[132:135], v[198:201], v[80:83]
	v_mfma_f32_16x16x32_f16 v[72:75], v[140:143], v[198:201], v[72:75]
	s_barrier
	s_add_i32 s34, 0, 0x1c000
	s_add_i32 s35, s74, s42
	v_add_u32_e32 v177, s34, v168
	s_mov_b32 m0, s35
	ds_read_b128 v[202:205], v177
	ds_read_b128 v[206:209], v177 offset:1024
	ds_read_b128 v[210:213], v177 offset:2048
	ds_read_b128 v[214:217], v177 offset:3072
	global_load_lds_dwordx4 v146, s[78:79]
	s_add_i32 m0, s35, 0x2000
	s_nop 0
	global_load_lds_dwordx4 v150, s[78:79]
	s_barrier
	s_waitcnt lgkmcnt(0)
	v_mfma_f32_16x16x32_f16 v[116:119], v[202:205], v[158:161], v[116:119]
	v_mfma_f32_16x16x32_f16 v[112:115], v[210:213], v[158:161], v[112:115]
	v_mfma_f32_16x16x32_f16 v[100:103], v[202:205], v[178:181], v[100:103]
	v_mfma_f32_16x16x32_f16 v[92:95], v[210:213], v[178:181], v[92:95]
	v_mfma_f32_16x16x32_f16 v[84:87], v[202:205], v[186:189], v[84:87]
	v_mfma_f32_16x16x32_f16 v[76:79], v[210:213], v[186:189], v[76:79]
	v_mfma_f32_16x16x32_f16 v[68:71], v[202:205], v[194:197], v[68:71]
	v_mfma_f32_16x16x32_f16 v[64:67], v[210:213], v[194:197], v[64:67]
	v_mfma_f32_16x16x32_f16 v[116:119], v[206:209], v[162:165], v[116:119]
	v_mfma_f32_16x16x32_f16 v[112:115], v[214:217], v[162:165], v[112:115]
	v_mfma_f32_16x16x32_f16 v[100:103], v[206:209], v[182:185], v[100:103]
	v_mfma_f32_16x16x32_f16 v[92:95], v[214:217], v[182:185], v[92:95]
	v_mfma_f32_16x16x32_f16 v[84:87], v[206:209], v[190:193], v[84:87]
	v_mfma_f32_16x16x32_f16 v[76:79], v[214:217], v[190:193], v[76:79]
	v_mfma_f32_16x16x32_f16 v[68:71], v[206:209], v[198:201], v[68:71]
	v_mfma_f32_16x16x32_f16 v[64:67], v[214:217], v[198:201], v[64:67]
	s_barrier
	s_mov_b32 m0, s49
	ds_read_b128 v[158:161], v173 offset:49152
	ds_read_b128 v[162:165], v173 offset:50176
	ds_read_b128 v[178:181], v173 offset:51200
	ds_read_b128 v[182:185], v173 offset:52224
	ds_read_b128 v[186:189], v173 offset:53248
	ds_read_b128 v[190:193], v173 offset:54272
	ds_read_b128 v[194:197], v173 offset:55296
	ds_read_b128 v[198:201], v173 offset:56320
	global_load_lds_dwordx4 v144, s[80:81]
	s_mov_b32 m0, s50
	s_nop 0
	global_load_lds_dwordx4 v148, s[80:81]
	s_waitcnt vmcnt(10)
	s_barrier
	s_waitcnt lgkmcnt(0)
	v_mfma_f32_16x16x32_f16 v[60:63], v[128:131], v[158:161], v[60:63]
	v_mfma_f32_16x16x32_f16 v[56:59], v[136:139], v[158:161], v[56:59]
	v_mfma_f32_16x16x32_f16 v[48:51], v[128:131], v[178:181], v[48:51]
	v_mfma_f32_16x16x32_f16 v[40:43], v[136:139], v[178:181], v[40:43]
	v_mfma_f32_16x16x32_f16 v[32:35], v[128:131], v[186:189], v[32:35]
	v_mfma_f32_16x16x32_f16 v[24:27], v[136:139], v[186:189], v[24:27]
	v_mfma_f32_16x16x32_f16 v[16:19], v[128:131], v[194:197], v[16:19]
	v_mfma_f32_16x16x32_f16 v[8:11], v[136:139], v[194:197], v[8:11]
	v_mfma_f32_16x16x32_f16 v[60:63], v[132:135], v[162:165], v[60:63]
	v_mfma_f32_16x16x32_f16 v[56:59], v[140:143], v[162:165], v[56:59]
	v_mfma_f32_16x16x32_f16 v[48:51], v[132:135], v[182:185], v[48:51]
	v_mfma_f32_16x16x32_f16 v[40:43], v[140:143], v[182:185], v[40:43]
	v_mfma_f32_16x16x32_f16 v[32:35], v[132:135], v[190:193], v[32:35]
	v_mfma_f32_16x16x32_f16 v[24:27], v[140:143], v[190:193], v[24:27]
	v_mfma_f32_16x16x32_f16 v[16:19], v[132:135], v[198:201], v[16:19]
	v_mfma_f32_16x16x32_f16 v[8:11], v[140:143], v[198:201], v[8:11]
	s_barrier
	s_add_u32 s30, s30, 0xc080
	s_addc_u32 s31, s31, 0
	s_add_i32 s34, s34, s42
	s_mov_b32 m0, s34
	s_nop 0
	global_load_lds_dwordx4 v146, s[30:31]
	s_add_i32 m0, s34, 0x2000
	s_nop 0
	global_load_lds_dwordx4 v150, s[30:31]
	ds_read_b128 v[128:131], v172
	ds_read_b128 v[132:135], v172 offset:1024
	ds_read_b128 v[136:139], v172 offset:2048
	ds_read_b128 v[140:143], v172 offset:3072
	s_waitcnt vmcnt(6)
	s_barrier
	v_mfma_f32_16x16x32_f16 v[52:55], v[202:205], v[158:161], v[52:55]
	v_mfma_f32_16x16x32_f16 v[44:47], v[210:213], v[158:161], v[44:47]
	v_mfma_f32_16x16x32_f16 v[36:39], v[202:205], v[178:181], v[36:39]
	v_mfma_f32_16x16x32_f16 v[28:31], v[210:213], v[178:181], v[28:31]
	v_mfma_f32_16x16x32_f16 v[20:23], v[202:205], v[186:189], v[20:23]
	v_mfma_f32_16x16x32_f16 v[12:15], v[210:213], v[186:189], v[12:15]
	v_mfma_f32_16x16x32_f16 v[4:7], v[202:205], v[194:197], v[4:7]
	v_mfma_f32_16x16x32_f16 v[0:3], v[210:213], v[194:197], v[0:3]
	v_mfma_f32_16x16x32_f16 v[52:55], v[206:209], v[162:165], v[52:55]
	v_mfma_f32_16x16x32_f16 v[44:47], v[214:217], v[162:165], v[44:47]
	v_mfma_f32_16x16x32_f16 v[36:39], v[206:209], v[182:185], v[36:39]
	v_mfma_f32_16x16x32_f16 v[28:31], v[214:217], v[182:185], v[28:31]
	v_mfma_f32_16x16x32_f16 v[20:23], v[206:209], v[190:193], v[20:23]
	v_mfma_f32_16x16x32_f16 v[12:15], v[214:217], v[190:193], v[12:15]
	v_mfma_f32_16x16x32_f16 v[4:7], v[206:209], v[198:201], v[4:7]
	v_mfma_f32_16x16x32_f16 v[0:3], v[214:217], v[198:201], v[0:3]
	s_barrier
	s_add_i32 s73, s73, 2
	s_add_u32 s28, s28, 0x100
	s_addc_u32 s29, s29, 0
	s_add_u32 s71, s71, 0x100
	s_addc_u32 s72, s72, 0
	s_cmp_gt_u32 s73, 9
	s_cbranch_scc0 .LBB9_27
	s_lshl_b32 s28, s70, 8
	s_add_i32 s28, s28, s48
	s_lshl_b32 s29, s68, 8
	s_or_b32 s29, s29, s51
	s_waitcnt vmcnt(6)
	v_pk_fma_f32 v[126:127], v[126:127], v[226:227], v[236:237] op_sel_hi:[1,0,1]
	v_pk_fma_f32 v[124:125], v[124:125], v[226:227], v[234:235] op_sel_hi:[1,0,1]
	v_pk_fma_f32 v[122:123], v[122:123], v[226:227], v[240:241] op_sel_hi:[1,0,1]
	v_pk_fma_f32 v[120:121], v[120:121], v[226:227], v[238:239] op_sel_hi:[1,0,1]
	v_cvt_pk_f16_f32 v124, v124, v125
	v_cvt_pk_f16_f32 v125, v126, v127
	v_cvt_pk_f16_f32 v126, v120, v121
	v_cvt_pk_f16_f32 v123, v122, v123
	v_pk_fma_f32 v[118:119], v[118:119], v[226:227], v[244:245] op_sel_hi:[1,0,1]
	v_pk_fma_f32 v[116:117], v[116:117], v[226:227], v[242:243] op_sel_hi:[1,0,1]
	v_pk_fma_f32 v[114:115], v[114:115], v[226:227], v[248:249] op_sel_hi:[1,0,1]
	v_pk_fma_f32 v[112:113], v[112:113], v[226:227], v[246:247] op_sel_hi:[1,0,1]
	v_pk_max_f16 v120, v124, 0
	v_pk_max_f16 v121, v125, 0
	v_pk_max_f16 v122, v126, 0
	v_pk_max_f16 v123, v123, 0
	v_cvt_pk_f16_f32 v116, v116, v117
	v_cvt_pk_f16_f32 v117, v118, v119
	v_cvt_pk_f16_f32 v118, v112, v113
	v_cvt_pk_f16_f32 v115, v114, v115
	v_pk_fma_f32 v[110:111], v[110:111], v[226:227], v[236:237] op_sel:[0,1,0]
	v_pk_fma_f32 v[108:109], v[108:109], v[226:227], v[234:235] op_sel:[0,1,0]
	v_pk_fma_f32 v[106:107], v[106:107], v[226:227], v[240:241] op_sel:[0,1,0]
	v_pk_fma_f32 v[104:105], v[104:105], v[226:227], v[238:239] op_sel:[0,1,0]
	v_pk_fma_f32 v[102:103], v[102:103], v[226:227], v[244:245] op_sel:[0,1,0]
	v_pk_fma_f32 v[100:101], v[100:101], v[226:227], v[242:243] op_sel:[0,1,0]
	v_pk_fma_f32 v[94:95], v[94:95], v[226:227], v[248:249] op_sel:[0,1,0]
	v_pk_fma_f32 v[92:93], v[92:93], v[226:227], v[246:247] op_sel:[0,1,0]
	ds_write_b128 v175, v[120:123]
	v_or_b32_e32 v120, s28, v169
	v_pk_max_f16 v112, v116, 0
	v_pk_max_f16 v113, v117, 0
	v_pk_max_f16 v114, v118, 0
	v_pk_max_f16 v115, v115, 0
	v_cvt_pk_f16_f32 v108, v108, v109
	v_cvt_pk_f16_f32 v109, v110, v111
	v_cvt_pk_f16_f32 v110, v104, v105
	v_cvt_pk_f16_f32 v107, v106, v107
	v_cvt_pk_f16_f32 v100, v100, v101
	v_cvt_pk_f16_f32 v101, v102, v103
	v_cvt_pk_f16_f32 v102, v92, v93
	v_cvt_pk_f16_f32 v95, v94, v95
	ds_write_b128 v175, v[112:115] offset:64
	v_mul_lo_u32 v116, v120, s10
	v_pk_max_f16 v104, v108, 0
	v_pk_max_f16 v105, v109, 0
	v_pk_max_f16 v106, v110, 0
	v_pk_max_f16 v107, v107, 0
	v_pk_max_f16 v92, v100, 0
	v_pk_max_f16 v93, v101, 0
	v_pk_max_f16 v94, v102, 0
	v_pk_max_f16 v95, v95, 0
	ds_read_b128 v[112:115], v176
	v_add_u32_e32 v120, s29, v116
	ds_read_b128 v[116:119], v176 offset:1152
	ds_write_b128 v175, v[104:107]
	ds_write_b128 v175, v[92:95] offset:64
	ds_read_b128 v[92:95], v176
	ds_read_b128 v[100:103], v176 offset:1152
	v_lshlrev_b32_e32 v121, 1, v120
	v_add_u32_e32 v122, v121, v170
	v_add_u32_e32 v104, s55, v121
	s_waitcnt lgkmcnt(0)
	buffer_store_dwordx4 v[112:115], v122, s[20:23], 0 offen nt
	v_add_u32_e32 v105, v104, v170
	v_pk_fma_f32 v[90:91], v[90:91], v[228:229], v[240:241] op_sel_hi:[1,0,1]
	v_add_u32_e32 v112, v121, v171
	buffer_store_dwordx4 v[116:119], v112, s[20:23], 0 offen nt
	buffer_store_dwordx4 v[92:95], v105, s[20:23], 0 offen nt
	v_pk_fma_f32 v[88:89], v[88:89], v[228:229], v[238:239] op_sel_hi:[1,0,1]
	v_pk_fma_f32 v[86:87], v[86:87], v[228:229], v[244:245] op_sel_hi:[1,0,1]
	v_pk_fma_f32 v[92:93], v[98:99], v[228:229], v[236:237] op_sel_hi:[1,0,1]
	v_pk_fma_f32 v[94:95], v[96:97], v[228:229], v[234:235] op_sel_hi:[1,0,1]
	v_pk_fma_f32 v[84:85], v[84:85], v[228:229], v[242:243] op_sel_hi:[1,0,1]
	v_pk_fma_f32 v[78:79], v[78:79], v[228:229], v[248:249] op_sel_hi:[1,0,1]
	v_pk_fma_f32 v[76:77], v[76:77], v[228:229], v[246:247] op_sel_hi:[1,0,1]
	v_cvt_pk_f16_f32 v94, v94, v95
	v_cvt_pk_f16_f32 v92, v92, v93
	v_cvt_pk_f16_f32 v93, v88, v89
	v_cvt_pk_f16_f32 v91, v90, v91
	v_cvt_pk_f16_f32 v84, v84, v85
	v_cvt_pk_f16_f32 v85, v86, v87
	v_cvt_pk_f16_f32 v86, v76, v77
	v_cvt_pk_f16_f32 v79, v78, v79
	v_pk_max_f16 v88, v94, 0
	v_pk_max_f16 v89, v92, 0
	v_pk_max_f16 v90, v93, 0
	v_pk_max_f16 v91, v91, 0
	v_pk_max_f16 v76, v84, 0
	v_pk_max_f16 v77, v85, 0
	v_pk_max_f16 v78, v86, 0
	v_pk_max_f16 v79, v79, 0
	ds_write_b128 v175, v[88:91]
	ds_write_b128 v175, v[76:79] offset:64
	ds_read_b128 v[76:79], v176
	ds_read_b128 v[84:87], v176 offset:1152
	v_add_u32_e32 v88, s55, v104
	v_add_u32_e32 v105, v104, v171
	v_add_u32_e32 v89, v88, v170
	buffer_store_dwordx4 v[100:103], v105, s[20:23], 0 offen nt
	s_waitcnt lgkmcnt(1)
	buffer_store_dwordx4 v[76:79], v89, s[20:23], 0 offen nt
	v_pk_fma_f32 v[74:75], v[74:75], v[228:229], v[240:241] op_sel:[0,1,0]
	v_pk_fma_f32 v[72:73], v[72:73], v[228:229], v[238:239] op_sel:[0,1,0]
	v_add_u32_e32 v76, v88, v171
	s_waitcnt lgkmcnt(0)
	buffer_store_dwordx4 v[84:87], v76, s[20:23], 0 offen nt
	v_pk_fma_f32 v[76:77], v[82:83], v[228:229], v[236:237] op_sel:[0,1,0]
	v_pk_fma_f32 v[78:79], v[80:81], v[228:229], v[234:235] op_sel:[0,1,0]
	v_pk_fma_f32 v[70:71], v[70:71], v[228:229], v[244:245] op_sel:[0,1,0]
	v_pk_fma_f32 v[68:69], v[68:69], v[228:229], v[242:243] op_sel:[0,1,0]
	v_pk_fma_f32 v[66:67], v[66:67], v[228:229], v[248:249] op_sel:[0,1,0]
	v_pk_fma_f32 v[64:65], v[64:65], v[228:229], v[246:247] op_sel:[0,1,0]
	v_cvt_pk_f16_f32 v78, v78, v79
	v_cvt_pk_f16_f32 v76, v76, v77
	v_cvt_pk_f16_f32 v77, v72, v73
	v_cvt_pk_f16_f32 v75, v74, v75
	v_cvt_pk_f16_f32 v68, v68, v69
	v_cvt_pk_f16_f32 v69, v70, v71
	v_cvt_pk_f16_f32 v70, v64, v65
	v_cvt_pk_f16_f32 v67, v66, v67
	v_pk_fma_f32 v[62:63], v[62:63], v[230:231], v[236:237] op_sel_hi:[1,0,1]
	v_pk_fma_f32 v[60:61], v[60:61], v[230:231], v[234:235] op_sel_hi:[1,0,1]
	v_pk_fma_f32 v[58:59], v[58:59], v[230:231], v[240:241] op_sel_hi:[1,0,1]
	v_pk_fma_f32 v[56:57], v[56:57], v[230:231], v[238:239] op_sel_hi:[1,0,1]
	v_pk_fma_f32 v[54:55], v[54:55], v[230:231], v[244:245] op_sel_hi:[1,0,1]
	v_pk_fma_f32 v[52:53], v[52:53], v[230:231], v[242:243] op_sel_hi:[1,0,1]
	v_pk_fma_f32 v[46:47], v[46:47], v[230:231], v[248:249] op_sel_hi:[1,0,1]
	v_pk_fma_f32 v[44:45], v[44:45], v[230:231], v[246:247] op_sel_hi:[1,0,1]
	v_pk_max_f16 v72, v78, 0
	v_pk_max_f16 v73, v76, 0
	v_pk_max_f16 v74, v77, 0
	v_pk_max_f16 v75, v75, 0
	v_pk_max_f16 v64, v68, 0
	v_pk_max_f16 v65, v69, 0
	v_pk_max_f16 v66, v70, 0
	v_pk_max_f16 v67, v67, 0
	v_cvt_pk_f16_f32 v60, v60, v61
	v_cvt_pk_f16_f32 v61, v62, v63
	v_cvt_pk_f16_f32 v62, v56, v57
	v_cvt_pk_f16_f32 v59, v58, v59
	v_cvt_pk_f16_f32 v52, v52, v53
	v_cvt_pk_f16_f32 v53, v54, v55
	v_cvt_pk_f16_f32 v54, v44, v45
	v_cvt_pk_f16_f32 v47, v46, v47
	ds_write_b128 v175, v[72:75]
	ds_write_b128 v175, v[64:67] offset:64
	v_pk_max_f16 v56, v60, 0
	v_pk_max_f16 v57, v61, 0
	v_pk_max_f16 v58, v62, 0
	v_pk_max_f16 v59, v59, 0
	v_pk_max_f16 v44, v52, 0
	v_pk_max_f16 v45, v53, 0
	v_pk_max_f16 v46, v54, 0
	v_pk_max_f16 v47, v47, 0
	ds_read_b128 v[64:67], v176
	ds_read_b128 v[68:71], v176 offset:1152
	ds_write_b128 v175, v[56:59]
	ds_write_b128 v175, v[44:47] offset:64
	ds_read_b128 v[44:47], v176
	ds_read_b128 v[52:55], v176 offset:1152
	v_add_u32_e32 v72, s56, v120
	v_lshlrev_b32_e32 v73, 1, v72
	v_add_u32_e32 v74, v73, v170
	v_add_u32_e32 v56, s62, v88
	s_waitcnt lgkmcnt(5)
	buffer_store_dwordx4 v[64:67], v74, s[20:23], 0 offen nt
	v_add_u32_e32 v57, v56, v170
	v_pk_fma_f32 v[42:43], v[42:43], v[230:231], v[240:241] op_sel:[0,1,0]
	v_add_u32_e32 v64, v73, v171
	s_waitcnt lgkmcnt(4)
	buffer_store_dwordx4 v[68:71], v64, s[20:23], 0 offen nt
	s_waitcnt lgkmcnt(1)
	buffer_store_dwordx4 v[44:47], v57, s[20:23], 0 offen nt
	v_pk_fma_f32 v[40:41], v[40:41], v[230:231], v[238:239] op_sel:[0,1,0]
	v_pk_fma_f32 v[38:39], v[38:39], v[230:231], v[244:245] op_sel:[0,1,0]
	v_add_u32_e32 v44, v56, v171
	s_waitcnt lgkmcnt(0)
	buffer_store_dwordx4 v[52:55], v44, s[20:23], 0 offen nt
	v_pk_fma_f32 v[44:45], v[50:51], v[230:231], v[236:237] op_sel:[0,1,0]
	v_pk_fma_f32 v[46:47], v[48:49], v[230:231], v[234:235] op_sel:[0,1,0]
	v_pk_fma_f32 v[36:37], v[36:37], v[230:231], v[242:243] op_sel:[0,1,0]
	v_pk_fma_f32 v[30:31], v[30:31], v[230:231], v[248:249] op_sel:[0,1,0]
	v_pk_fma_f32 v[28:29], v[28:29], v[230:231], v[246:247] op_sel:[0,1,0]
	v_cvt_pk_f16_f32 v46, v46, v47
	v_cvt_pk_f16_f32 v44, v44, v45
	v_cvt_pk_f16_f32 v45, v40, v41
	v_cvt_pk_f16_f32 v43, v42, v43
	v_cvt_pk_f16_f32 v36, v36, v37
	v_cvt_pk_f16_f32 v37, v38, v39
	v_cvt_pk_f16_f32 v38, v28, v29
	v_cvt_pk_f16_f32 v31, v30, v31
	v_pk_max_f16 v40, v46, 0
	v_pk_max_f16 v41, v44, 0
	v_pk_max_f16 v42, v45, 0
	v_pk_max_f16 v43, v43, 0
	v_pk_max_f16 v28, v36, 0
	v_pk_max_f16 v29, v37, 0
	v_pk_max_f16 v30, v38, 0
	v_pk_max_f16 v31, v31, 0
	ds_write_b128 v175, v[40:43]
	ds_write_b128 v175, v[28:31] offset:64
	ds_read_b128 v[28:31], v176
	ds_read_b128 v[36:39], v176 offset:1152
	v_add_u32_e32 v40, s63, v72
	v_lshlrev_b32_e32 v41, 1, v40
	v_add_u32_e32 v42, v41, v170
	s_waitcnt lgkmcnt(1)
	buffer_store_dwordx4 v[28:31], v42, s[20:23], 0 offen nt
	v_pk_fma_f32 v[26:27], v[26:27], v[232:233], v[240:241] op_sel_hi:[1,0,1]
	v_pk_fma_f32 v[24:25], v[24:25], v[232:233], v[238:239] op_sel_hi:[1,0,1]
	v_add_u32_e32 v28, v41, v171
	s_waitcnt lgkmcnt(0)
	buffer_store_dwordx4 v[36:39], v28, s[20:23], 0 offen nt
	v_pk_fma_f32 v[28:29], v[34:35], v[232:233], v[236:237] op_sel_hi:[1,0,1]
	v_pk_fma_f32 v[30:31], v[32:33], v[232:233], v[234:235] op_sel_hi:[1,0,1]
	v_pk_fma_f32 v[22:23], v[22:23], v[232:233], v[244:245] op_sel_hi:[1,0,1]
	v_pk_fma_f32 v[20:21], v[20:21], v[232:233], v[242:243] op_sel_hi:[1,0,1]
	v_pk_fma_f32 v[14:15], v[14:15], v[232:233], v[248:249] op_sel_hi:[1,0,1]
	v_pk_fma_f32 v[12:13], v[12:13], v[232:233], v[246:247] op_sel_hi:[1,0,1]
	v_cvt_pk_f16_f32 v30, v30, v31
	v_cvt_pk_f16_f32 v28, v28, v29
	v_cvt_pk_f16_f32 v29, v24, v25
	v_cvt_pk_f16_f32 v27, v26, v27
	v_cvt_pk_f16_f32 v20, v20, v21
	v_cvt_pk_f16_f32 v21, v22, v23
	v_cvt_pk_f16_f32 v22, v12, v13
	v_cvt_pk_f16_f32 v15, v14, v15
	v_pk_max_f16 v24, v30, 0
	v_pk_max_f16 v25, v28, 0
	v_pk_max_f16 v26, v29, 0
	v_pk_max_f16 v27, v27, 0
	v_pk_max_f16 v12, v20, 0
	v_pk_max_f16 v13, v21, 0
	v_pk_max_f16 v14, v22, 0
	v_pk_max_f16 v15, v15, 0
	ds_write_b128 v175, v[24:27]
	ds_write_b128 v175, v[12:15] offset:64
	ds_read_b128 v[12:15], v176
	ds_read_b128 v[20:23], v176 offset:1152
	v_add_u32_e32 v24, s64, v40
	v_lshlrev_b32_e32 v25, 1, v24
	v_add_u32_e32 v26, v25, v170
	s_waitcnt lgkmcnt(1)
	buffer_store_dwordx4 v[12:15], v26, s[20:23], 0 offen nt
	v_pk_fma_f32 v[10:11], v[10:11], v[232:233], v[240:241] op_sel:[0,1,0]
	v_pk_fma_f32 v[8:9], v[8:9], v[232:233], v[238:239] op_sel:[0,1,0]
	v_pk_fma_f32 v[12:13], v[18:19], v[232:233], v[236:237] op_sel:[0,1,0]
	v_pk_fma_f32 v[14:15], v[16:17], v[232:233], v[234:235] op_sel:[0,1,0]
	v_pk_fma_f32 v[6:7], v[6:7], v[232:233], v[244:245] op_sel:[0,1,0]
	v_pk_fma_f32 v[4:5], v[4:5], v[232:233], v[242:243] op_sel:[0,1,0]
	v_pk_fma_f32 v[2:3], v[2:3], v[232:233], v[248:249] op_sel:[0,1,0]
	v_pk_fma_f32 v[0:1], v[0:1], v[232:233], v[246:247] op_sel:[0,1,0]
	v_cvt_pk_f16_f32 v14, v14, v15
	v_cvt_pk_f16_f32 v12, v12, v13
	v_cvt_pk_f16_f32 v13, v8, v9
	v_cvt_pk_f16_f32 v11, v10, v11
	v_cvt_pk_f16_f32 v4, v4, v5
	v_cvt_pk_f16_f32 v5, v6, v7
	v_cvt_pk_f16_f32 v6, v0, v1
	v_cvt_pk_f16_f32 v3, v2, v3
	v_pk_max_f16 v8, v14, 0
	v_pk_max_f16 v9, v12, 0
	v_pk_max_f16 v10, v13, 0
	v_pk_max_f16 v11, v11, 0
	v_pk_max_f16 v0, v4, 0
	v_pk_max_f16 v1, v5, 0
	v_pk_max_f16 v2, v6, 0
	v_pk_max_f16 v3, v3, 0
	ds_write_b128 v175, v[8:11]
	ds_write_b128 v175, v[0:3] offset:64
	ds_read_b128 v[0:3], v176
	ds_read_b128 v[4:7], v176 offset:1152
	v_add_lshl_u32 v8, v24, s64, 1
	v_add_u32_e32 v25, v25, v171
	v_add_u32_e32 v9, v8, v170
	s_waitcnt lgkmcnt(4)
	buffer_store_dwordx4 v[20:23], v25, s[20:23], 0 offen nt
	s_waitcnt lgkmcnt(1)
	buffer_store_dwordx4 v[0:3], v9, s[20:23], 0 offen nt
	s_mov_b32 s68, s67
	s_mov_b32 s70, s69
	v_add_u32_e32 v0, v8, v171
	s_mov_b64 s[30:31], s[0:1]
	s_mov_b64 s[28:29], s[8:9]
	s_mov_b64 vcc, s[6:7]
	s_waitcnt lgkmcnt(0)
	buffer_store_dwordx4 v[4:7], v0, s[20:23], 0 offen nt
	s_cbranch_vccz .LBB9_12
	s_waitcnt vmcnt(0)
	s_cmpk_gt_u32 s36, 0xff
	s_cbranch_scc1 .LBB9_31
	s_barrier

.LBB9_32:
	s_endpgm
	s_endpgm
	s_endpgm
	s_endpgm
	s_endpgm
	s_endpgm
	s_endpgm
	s_endpgm
	s_endpgm
	s_endpgm
	s_endpgm
	s_endpgm
	s_endpgm
	s_endpgm
	s_endpgm
	s_endpgm
	s_endpgm
	s_endpgm
	s_endpgm
	s_endpgm
	s_endpgm
	s_endpgm
	s_endpgm
	s_endpgm
	s_endpgm
	s_endpgm
	s_endpgm
	s_endpgm
	s_endpgm
	.section	.rodata,"a",@progbits
	.p2align	6, 0x0

.LBB10_26:
	s_add_u32 s38, s38, 0xc0080
	s_addc_u32 s39, s39, 0
	s_add_u32 s85, s40, 0x100
	v_mov_b32_e32 v0, 0
	s_addc_u32 s86, s41, 0
	s_mov_b32 s87, -2
	v_mov_b32_e32 v1, v0
	v_mov_b32_e32 v2, v0
	v_mov_b32_e32 v3, v0
	v_mov_b32_e32 v4, v0
	v_mov_b32_e32 v5, v0
	v_mov_b32_e32 v6, v0
	v_mov_b32_e32 v7, v0
	v_mov_b32_e32 v16, v0
	v_mov_b32_e32 v17, v0
	v_mov_b32_e32 v18, v0
	v_mov_b32_e32 v19, v0
	v_mov_b32_e32 v20, v0
	v_mov_b32_e32 v21, v0
	v_mov_b32_e32 v22, v0
	v_mov_b32_e32 v23, v0
	v_mov_b32_e32 v32, v0
	v_mov_b32_e32 v33, v0
	v_mov_b32_e32 v34, v0
	v_mov_b32_e32 v35, v0
	v_mov_b32_e32 v36, v0
	v_mov_b32_e32 v37, v0
	v_mov_b32_e32 v38, v0
	v_mov_b32_e32 v39, v0
	v_mov_b32_e32 v48, v0
	v_mov_b32_e32 v49, v0
	v_mov_b32_e32 v50, v0
	v_mov_b32_e32 v51, v0
	v_mov_b32_e32 v52, v0
	v_mov_b32_e32 v53, v0
	v_mov_b32_e32 v54, v0
	v_mov_b32_e32 v55, v0
	v_mov_b32_e32 v8, v0
	v_mov_b32_e32 v9, v0
	v_mov_b32_e32 v10, v0
	v_mov_b32_e32 v11, v0
	v_mov_b32_e32 v12, v0
	v_mov_b32_e32 v13, v0
	v_mov_b32_e32 v14, v0
	v_mov_b32_e32 v15, v0
	v_mov_b32_e32 v24, v0
	v_mov_b32_e32 v25, v0
	v_mov_b32_e32 v26, v0
	v_mov_b32_e32 v27, v0
	v_mov_b32_e32 v28, v0
	v_mov_b32_e32 v29, v0
	v_mov_b32_e32 v30, v0
	v_mov_b32_e32 v31, v0
	v_mov_b32_e32 v40, v0
	v_mov_b32_e32 v41, v0
	v_mov_b32_e32 v42, v0
	v_mov_b32_e32 v43, v0
	v_mov_b32_e32 v44, v0
	v_mov_b32_e32 v45, v0
	v_mov_b32_e32 v46, v0
	v_mov_b32_e32 v47, v0
	v_mov_b32_e32 v56, v0
	v_mov_b32_e32 v57, v0
	v_mov_b32_e32 v58, v0
	v_mov_b32_e32 v59, v0
	v_mov_b32_e32 v60, v0
	v_mov_b32_e32 v61, v0
	v_mov_b32_e32 v62, v0
	v_mov_b32_e32 v63, v0
	v_mov_b32_e32 v64, v0
	v_mov_b32_e32 v65, v0
	v_mov_b32_e32 v66, v0
	v_mov_b32_e32 v67, v0
	v_mov_b32_e32 v68, v0
	v_mov_b32_e32 v69, v0
	v_mov_b32_e32 v70, v0
	v_mov_b32_e32 v71, v0
	v_mov_b32_e32 v96, v0
	v_mov_b32_e32 v97, v0
	v_mov_b32_e32 v98, v0
	v_mov_b32_e32 v99, v0
	v_mov_b32_e32 v100, v0
	v_mov_b32_e32 v101, v0
	v_mov_b32_e32 v102, v0
	v_mov_b32_e32 v103, v0
	v_mov_b32_e32 v112, v0
	v_mov_b32_e32 v113, v0
	v_mov_b32_e32 v114, v0
	v_mov_b32_e32 v115, v0
	v_mov_b32_e32 v116, v0
	v_mov_b32_e32 v117, v0
	v_mov_b32_e32 v118, v0
	v_mov_b32_e32 v119, v0
	v_mov_b32_e32 v128, v0
	v_mov_b32_e32 v129, v0
	v_mov_b32_e32 v130, v0
	v_mov_b32_e32 v131, v0
	v_mov_b32_e32 v132, v0
	v_mov_b32_e32 v133, v0
	v_mov_b32_e32 v134, v0
	v_mov_b32_e32 v135, v0
	v_mov_b32_e32 v76, v0
	v_mov_b32_e32 v77, v0
	v_mov_b32_e32 v78, v0
	v_mov_b32_e32 v79, v0
	v_mov_b32_e32 v84, v0
	v_mov_b32_e32 v85, v0
	v_mov_b32_e32 v86, v0
	v_mov_b32_e32 v87, v0
	v_mov_b32_e32 v104, v0
	v_mov_b32_e32 v105, v0
	v_mov_b32_e32 v106, v0
	v_mov_b32_e32 v107, v0
	v_mov_b32_e32 v108, v0
	v_mov_b32_e32 v109, v0
	v_mov_b32_e32 v110, v0
	v_mov_b32_e32 v111, v0
	v_mov_b32_e32 v120, v0
	v_mov_b32_e32 v121, v0
	v_mov_b32_e32 v122, v0
	v_mov_b32_e32 v123, v0
	v_mov_b32_e32 v124, v0
	v_mov_b32_e32 v125, v0
	v_mov_b32_e32 v126, v0
	v_mov_b32_e32 v127, v0
	v_mov_b32_e32 v140, v0
	v_mov_b32_e32 v141, v0
	v_mov_b32_e32 v142, v0
	v_mov_b32_e32 v143, v0
	v_mov_b32_e32 v144, v0
	v_mov_b32_e32 v145, v0
	v_mov_b32_e32 v146, v0
	v_mov_b32_e32 v147, v0
	ds_read_b128 v[72:75], v231
	ds_read_b128 v[80:83], v231 offset:1024
	ds_read_b128 v[88:91], v231 offset:2048
	ds_read_b128 v[92:95], v231 offset:3072
.LBB10_27:
	s_add_u32 s40, s38, 0xfff40080
	s_addc_u32 s41, s39, -1
	s_cmp_eq_u32 s87, 44
	s_cselect_b32 s43, s9, s41
	s_cselect_b32 s42, s8, s40
	s_cselect_b32 s41, s1, s86
	s_cselect_b32 s40, s0, s85
	s_add_i32 m0, s51, 0xc000
	ds_read_b128 v[136:139], v232
	ds_read_b128 v[148:151], v232 offset:1024
	ds_read_b128 v[152:155], v232 offset:2048
	ds_read_b128 v[156:159], v232 offset:3072
	ds_read_b128 v[160:163], v232 offset:4096
	ds_read_b128 v[164:167], v232 offset:5120
	ds_read_b128 v[168:171], v232 offset:6144
	ds_read_b128 v[172:175], v232 offset:7168
	global_load_lds_dwordx4 v184, s[38:39]
	s_add_i32 m0, s51, 0xe000
	s_nop 0
	global_load_lds_dwordx4 v186, s[38:39]
	s_waitcnt lgkmcnt(8)
	s_barrier
	s_waitcnt lgkmcnt(0)
	v_mfma_f32_16x16x32_f16 v[144:147], v[72:75], v[136:139], v[144:147]
	v_mfma_f32_16x16x32_f16 v[140:143], v[88:91], v[136:139], v[140:143]
	v_mfma_f32_16x16x32_f16 v[124:127], v[72:75], v[152:155], v[124:127]
	v_mfma_f32_16x16x32_f16 v[120:123], v[88:91], v[152:155], v[120:123]
	v_mfma_f32_16x16x32_f16 v[108:111], v[72:75], v[160:163], v[108:111]
	v_mfma_f32_16x16x32_f16 v[104:107], v[88:91], v[160:163], v[104:107]
	v_mfma_f32_16x16x32_f16 v[84:87], v[72:75], v[168:171], v[84:87]
	v_mfma_f32_16x16x32_f16 v[76:79], v[88:91], v[168:171], v[76:79]
	v_mfma_f32_16x16x32_f16 v[144:147], v[80:83], v[148:151], v[144:147]
	v_mfma_f32_16x16x32_f16 v[140:143], v[92:95], v[148:151], v[140:143]
	v_mfma_f32_16x16x32_f16 v[124:127], v[80:83], v[156:159], v[124:127]
	v_mfma_f32_16x16x32_f16 v[120:123], v[92:95], v[156:159], v[120:123]
	v_mfma_f32_16x16x32_f16 v[108:111], v[80:83], v[164:167], v[108:111]
	v_mfma_f32_16x16x32_f16 v[104:107], v[92:95], v[164:167], v[104:107]
	v_mfma_f32_16x16x32_f16 v[84:87], v[80:83], v[172:175], v[84:87]
	v_mfma_f32_16x16x32_f16 v[76:79], v[92:95], v[172:175], v[76:79]
	s_barrier
	s_add_i32 s88, s69, s50
	s_add_u32 s92, s40, 0x80
	s_addc_u32 s93, s41, 0
	s_mov_b32 m0, s88
	ds_read_b128 v[190:193], v233
	ds_read_b128 v[194:197], v233 offset:1024
	ds_read_b128 v[198:201], v233 offset:2048
	ds_read_b128 v[202:205], v233 offset:3072
	global_load_lds_dwordx4 v178, s[40:41]
	s_add_i32 m0, s88, 0x2000
	s_nop 0
	global_load_lds_dwordx4 v182, s[40:41]
	s_barrier
	s_waitcnt lgkmcnt(0)
	v_mfma_f32_16x16x32_f16 v[132:135], v[190:193], v[136:139], v[132:135]
	v_mfma_f32_16x16x32_f16 v[128:131], v[198:201], v[136:139], v[128:131]
	v_mfma_f32_16x16x32_f16 v[116:119], v[190:193], v[152:155], v[116:119]
	v_mfma_f32_16x16x32_f16 v[112:115], v[198:201], v[152:155], v[112:115]
	v_mfma_f32_16x16x32_f16 v[100:103], v[190:193], v[160:163], v[100:103]
	v_mfma_f32_16x16x32_f16 v[96:99], v[198:201], v[160:163], v[96:99]
	v_mfma_f32_16x16x32_f16 v[68:71], v[190:193], v[168:171], v[68:71]
	v_mfma_f32_16x16x32_f16 v[64:67], v[198:201], v[168:171], v[64:67]
	v_mfma_f32_16x16x32_f16 v[132:135], v[194:197], v[148:151], v[132:135]
	v_mfma_f32_16x16x32_f16 v[128:131], v[202:205], v[148:151], v[128:131]
	v_mfma_f32_16x16x32_f16 v[116:119], v[194:197], v[156:159], v[116:119]
	v_mfma_f32_16x16x32_f16 v[112:115], v[202:205], v[156:159], v[112:115]
	v_mfma_f32_16x16x32_f16 v[100:103], v[194:197], v[164:167], v[100:103]
	v_mfma_f32_16x16x32_f16 v[96:99], v[202:205], v[164:167], v[96:99]
	v_mfma_f32_16x16x32_f16 v[68:71], v[194:197], v[172:175], v[68:71]
	v_mfma_f32_16x16x32_f16 v[64:67], v[202:205], v[172:175], v[64:67]
	s_barrier
	s_mov_b32 m0, s51
	s_add_u32 s94, s42, 0x80
	s_addc_u32 s95, s43, 0
	ds_read_b128 v[136:139], v232 offset:16384
	ds_read_b128 v[148:151], v232 offset:17408
	ds_read_b128 v[152:155], v232 offset:18432
	ds_read_b128 v[156:159], v232 offset:19456
	ds_read_b128 v[160:163], v232 offset:20480
	ds_read_b128 v[164:167], v232 offset:21504
	ds_read_b128 v[168:171], v232 offset:22528
	ds_read_b128 v[172:175], v232 offset:23552
	global_load_lds_dwordx4 v176, s[42:43]
	s_mov_b32 m0, s52
	s_nop 0
	global_load_lds_dwordx4 v180, s[42:43]
	s_waitcnt vmcnt(10)
	s_barrier
	s_waitcnt lgkmcnt(0)
	v_mfma_f32_16x16x32_f16 v[60:63], v[72:75], v[136:139], v[60:63]
	v_mfma_f32_16x16x32_f16 v[56:59], v[88:91], v[136:139], v[56:59]
	v_mfma_f32_16x16x32_f16 v[44:47], v[72:75], v[152:155], v[44:47]
	v_mfma_f32_16x16x32_f16 v[40:43], v[88:91], v[152:155], v[40:43]
	v_mfma_f32_16x16x32_f16 v[28:31], v[72:75], v[160:163], v[28:31]
	v_mfma_f32_16x16x32_f16 v[24:27], v[88:91], v[160:163], v[24:27]
	v_mfma_f32_16x16x32_f16 v[12:15], v[72:75], v[168:171], v[12:15]
	v_mfma_f32_16x16x32_f16 v[8:11], v[88:91], v[168:171], v[8:11]
	v_mfma_f32_16x16x32_f16 v[60:63], v[80:83], v[148:151], v[60:63]
	v_mfma_f32_16x16x32_f16 v[56:59], v[92:95], v[148:151], v[56:59]
	v_mfma_f32_16x16x32_f16 v[44:47], v[80:83], v[156:159], v[44:47]
	v_mfma_f32_16x16x32_f16 v[40:43], v[92:95], v[156:159], v[40:43]
	v_mfma_f32_16x16x32_f16 v[28:31], v[80:83], v[164:167], v[28:31]
	v_mfma_f32_16x16x32_f16 v[24:27], v[92:95], v[164:167], v[24:27]
	v_mfma_f32_16x16x32_f16 v[12:15], v[80:83], v[172:175], v[12:15]
	v_mfma_f32_16x16x32_f16 v[8:11], v[92:95], v[172:175], v[8:11]
	s_barrier
	s_add_u32 s88, s40, 0x30000
	s_addc_u32 s89, s41, 0
	s_add_i32 s90, s70, s50
	s_mov_b32 m0, s90
	s_nop 0
	global_load_lds_dwordx4 v178, s[88:89]
	s_add_i32 m0, s90, 0x2000
	s_nop 0
	global_load_lds_dwordx4 v182, s[88:89]
	s_add_i32 s88, 0, 0x18000
	v_add_u32_e32 v92, s88, v228
	ds_read_b128 v[72:75], v92
	ds_read_b128 v[80:83], v92 offset:1024
	ds_read_b128 v[88:91], v92 offset:2048
	ds_read_b128 v[92:95], v92 offset:3072
	s_waitcnt vmcnt(6)
	s_barrier
	v_mfma_f32_16x16x32_f16 v[52:55], v[190:193], v[136:139], v[52:55]
	v_mfma_f32_16x16x32_f16 v[48:51], v[198:201], v[136:139], v[48:51]
	v_mfma_f32_16x16x32_f16 v[36:39], v[190:193], v[152:155], v[36:39]
	v_mfma_f32_16x16x32_f16 v[32:35], v[198:201], v[152:155], v[32:35]
	v_mfma_f32_16x16x32_f16 v[20:23], v[190:193], v[160:163], v[20:23]
	v_mfma_f32_16x16x32_f16 v[16:19], v[198:201], v[160:163], v[16:19]
	v_mfma_f32_16x16x32_f16 v[4:7], v[190:193], v[168:171], v[4:7]
	v_mfma_f32_16x16x32_f16 v[0:3], v[198:201], v[168:171], v[0:3]
	v_mfma_f32_16x16x32_f16 v[52:55], v[194:197], v[148:151], v[52:55]
	v_mfma_f32_16x16x32_f16 v[48:51], v[202:205], v[148:151], v[48:51]
	v_mfma_f32_16x16x32_f16 v[36:39], v[194:197], v[156:159], v[36:39]
	v_mfma_f32_16x16x32_f16 v[32:35], v[202:205], v[156:159], v[32:35]
	v_mfma_f32_16x16x32_f16 v[20:23], v[194:197], v[164:167], v[20:23]
	v_mfma_f32_16x16x32_f16 v[16:19], v[202:205], v[164:167], v[16:19]
	v_mfma_f32_16x16x32_f16 v[4:7], v[194:197], v[172:175], v[4:7]
	v_mfma_f32_16x16x32_f16 v[0:3], v[202:205], v[172:175], v[0:3]
	s_barrier
	s_add_u32 s42, s42, 0xc0000
	s_addc_u32 s43, s43, 0
	s_mov_b32 m0, s53
	ds_read_b128 v[136:139], v232 offset:32768
	ds_read_b128 v[148:151], v232 offset:33792
	ds_read_b128 v[152:155], v232 offset:34816
	ds_read_b128 v[156:159], v232 offset:35840
	ds_read_b128 v[160:163], v232 offset:36864
	ds_read_b128 v[164:167], v232 offset:37888
	ds_read_b128 v[168:171], v232 offset:38912
	ds_read_b128 v[172:175], v232 offset:39936
	global_load_lds_dwordx4 v176, s[42:43]
	s_mov_b32 m0, s54
	s_nop 0
	global_load_lds_dwordx4 v180, s[42:43]
	s_waitcnt lgkmcnt(8)
	s_barrier
	s_waitcnt lgkmcnt(0)
	v_mfma_f32_16x16x32_f16 v[144:147], v[72:75], v[136:139], v[144:147]
	v_mfma_f32_16x16x32_f16 v[140:143], v[88:91], v[136:139], v[140:143]
	v_mfma_f32_16x16x32_f16 v[124:127], v[72:75], v[152:155], v[124:127]
	v_mfma_f32_16x16x32_f16 v[120:123], v[88:91], v[152:155], v[120:123]
	v_mfma_f32_16x16x32_f16 v[108:111], v[72:75], v[160:163], v[108:111]
	v_mfma_f32_16x16x32_f16 v[104:107], v[88:91], v[160:163], v[104:107]
	v_mfma_f32_16x16x32_f16 v[84:87], v[72:75], v[168:171], v[84:87]
	v_mfma_f32_16x16x32_f16 v[76:79], v[88:91], v[168:171], v[76:79]
	v_mfma_f32_16x16x32_f16 v[144:147], v[80:83], v[148:151], v[144:147]
	v_mfma_f32_16x16x32_f16 v[140:143], v[92:95], v[148:151], v[140:143]
	v_mfma_f32_16x16x32_f16 v[124:127], v[80:83], v[156:159], v[124:127]
	v_mfma_f32_16x16x32_f16 v[120:123], v[92:95], v[156:159], v[120:123]
	v_mfma_f32_16x16x32_f16 v[108:111], v[80:83], v[164:167], v[108:111]
	v_mfma_f32_16x16x32_f16 v[104:107], v[92:95], v[164:167], v[104:107]
	v_mfma_f32_16x16x32_f16 v[84:87], v[80:83], v[172:175], v[84:87]
	v_mfma_f32_16x16x32_f16 v[76:79], v[92:95], v[172:175], v[76:79]
	s_barrier
	s_add_i32 s42, 0, 0x1c000
	s_add_i32 s43, s88, s50
	v_add_u32_e32 v202, s42, v228
	s_mov_b32 m0, s43
	ds_read_b128 v[190:193], v202
	ds_read_b128 v[194:197], v202 offset:1024
	ds_read_b128 v[198:201], v202 offset:2048
	ds_read_b128 v[202:205], v202 offset:3072
	global_load_lds_dwordx4 v178, s[92:93]
	s_add_i32 m0, s43, 0x2000
	s_nop 0
	global_load_lds_dwordx4 v182, s[92:93]
	s_barrier
	s_waitcnt lgkmcnt(0)
	v_mfma_f32_16x16x32_f16 v[132:135], v[190:193], v[136:139], v[132:135]
	v_mfma_f32_16x16x32_f16 v[128:131], v[198:201], v[136:139], v[128:131]
	v_mfma_f32_16x16x32_f16 v[116:119], v[190:193], v[152:155], v[116:119]
	v_mfma_f32_16x16x32_f16 v[112:115], v[198:201], v[152:155], v[112:115]
	v_mfma_f32_16x16x32_f16 v[100:103], v[190:193], v[160:163], v[100:103]
	v_mfma_f32_16x16x32_f16 v[96:99], v[198:201], v[160:163], v[96:99]
	v_mfma_f32_16x16x32_f16 v[68:71], v[190:193], v[168:171], v[68:71]
	v_mfma_f32_16x16x32_f16 v[64:67], v[198:201], v[168:171], v[64:67]
	v_mfma_f32_16x16x32_f16 v[132:135], v[194:197], v[148:151], v[132:135]
	v_mfma_f32_16x16x32_f16 v[128:131], v[202:205], v[148:151], v[128:131]
	v_mfma_f32_16x16x32_f16 v[116:119], v[194:197], v[156:159], v[116:119]
	v_mfma_f32_16x16x32_f16 v[112:115], v[202:205], v[156:159], v[112:115]
	v_mfma_f32_16x16x32_f16 v[100:103], v[194:197], v[164:167], v[100:103]
	v_mfma_f32_16x16x32_f16 v[96:99], v[202:205], v[164:167], v[96:99]
	v_mfma_f32_16x16x32_f16 v[68:71], v[194:197], v[172:175], v[68:71]
	v_mfma_f32_16x16x32_f16 v[64:67], v[202:205], v[172:175], v[64:67]
	s_barrier
	s_mov_b32 m0, s58
	ds_read_b128 v[136:139], v232 offset:49152
	ds_read_b128 v[148:151], v232 offset:50176
	ds_read_b128 v[152:155], v232 offset:51200
	ds_read_b128 v[156:159], v232 offset:52224
	ds_read_b128 v[160:163], v232 offset:53248
	ds_read_b128 v[164:167], v232 offset:54272
	ds_read_b128 v[168:171], v232 offset:55296
	ds_read_b128 v[172:175], v232 offset:56320
	global_load_lds_dwordx4 v176, s[94:95]
	s_mov_b32 m0, s59
	s_nop 0
	global_load_lds_dwordx4 v180, s[94:95]
	s_waitcnt vmcnt(10)
	s_barrier
	s_waitcnt lgkmcnt(0)
	v_mfma_f32_16x16x32_f16 v[60:63], v[72:75], v[136:139], v[60:63]
	v_mfma_f32_16x16x32_f16 v[56:59], v[88:91], v[136:139], v[56:59]
	v_mfma_f32_16x16x32_f16 v[44:47], v[72:75], v[152:155], v[44:47]
	v_mfma_f32_16x16x32_f16 v[40:43], v[88:91], v[152:155], v[40:43]
	v_mfma_f32_16x16x32_f16 v[28:31], v[72:75], v[160:163], v[28:31]
	v_mfma_f32_16x16x32_f16 v[24:27], v[88:91], v[160:163], v[24:27]
	v_mfma_f32_16x16x32_f16 v[12:15], v[72:75], v[168:171], v[12:15]
	v_mfma_f32_16x16x32_f16 v[8:11], v[88:91], v[168:171], v[8:11]
	v_mfma_f32_16x16x32_f16 v[60:63], v[80:83], v[148:151], v[60:63]
	v_mfma_f32_16x16x32_f16 v[56:59], v[92:95], v[148:151], v[56:59]
	v_mfma_f32_16x16x32_f16 v[44:47], v[80:83], v[156:159], v[44:47]
	v_mfma_f32_16x16x32_f16 v[40:43], v[92:95], v[156:159], v[40:43]
	v_mfma_f32_16x16x32_f16 v[28:31], v[80:83], v[164:167], v[28:31]
	v_mfma_f32_16x16x32_f16 v[24:27], v[92:95], v[164:167], v[24:27]
	v_mfma_f32_16x16x32_f16 v[12:15], v[80:83], v[172:175], v[12:15]
	v_mfma_f32_16x16x32_f16 v[8:11], v[92:95], v[172:175], v[8:11]
	s_barrier
	s_add_u32 s40, s40, 0x30080
	s_addc_u32 s41, s41, 0
	s_add_i32 s42, s42, s50
	s_mov_b32 m0, s42
	s_nop 0
	global_load_lds_dwordx4 v178, s[40:41]
	s_add_i32 m0, s42, 0x2000
	s_nop 0
	global_load_lds_dwordx4 v182, s[40:41]
	ds_read_b128 v[72:75], v231
	ds_read_b128 v[80:83], v231 offset:1024
	ds_read_b128 v[88:91], v231 offset:2048
	ds_read_b128 v[92:95], v231 offset:3072
	s_waitcnt vmcnt(6)
	s_barrier
	v_mfma_f32_16x16x32_f16 v[52:55], v[190:193], v[136:139], v[52:55]
	v_mfma_f32_16x16x32_f16 v[48:51], v[198:201], v[136:139], v[48:51]
	v_mfma_f32_16x16x32_f16 v[36:39], v[190:193], v[152:155], v[36:39]
	v_mfma_f32_16x16x32_f16 v[32:35], v[198:201], v[152:155], v[32:35]
	v_mfma_f32_16x16x32_f16 v[20:23], v[190:193], v[160:163], v[20:23]
	v_mfma_f32_16x16x32_f16 v[16:19], v[198:201], v[160:163], v[16:19]
	v_mfma_f32_16x16x32_f16 v[4:7], v[190:193], v[168:171], v[4:7]
	v_mfma_f32_16x16x32_f16 v[0:3], v[198:201], v[168:171], v[0:3]
	v_mfma_f32_16x16x32_f16 v[52:55], v[194:197], v[148:151], v[52:55]
	v_mfma_f32_16x16x32_f16 v[48:51], v[202:205], v[148:151], v[48:51]
	v_mfma_f32_16x16x32_f16 v[36:39], v[194:197], v[156:159], v[36:39]
	v_mfma_f32_16x16x32_f16 v[32:35], v[202:205], v[156:159], v[32:35]
	v_mfma_f32_16x16x32_f16 v[20:23], v[194:197], v[164:167], v[20:23]
	v_mfma_f32_16x16x32_f16 v[16:19], v[202:205], v[164:167], v[16:19]
	v_mfma_f32_16x16x32_f16 v[4:7], v[194:197], v[172:175], v[4:7]
	v_mfma_f32_16x16x32_f16 v[0:3], v[202:205], v[172:175], v[0:3]
	s_barrier
	s_add_i32 s87, s87, 2
	s_add_u32 s38, s38, 0x100
	s_addc_u32 s39, s39, 0
	s_add_u32 s85, s85, 0x100
	s_addc_u32 s86, s86, 0
	s_cmp_gt_u32 s87, 45
	s_cbranch_scc0 .LBB10_27
	s_lshl_b32 s92, s84, 8
	s_add_i32 s92, s92, s57
	s_lshl_b32 s93, s83, 8
	s_or_b32 s93, s93, s60
	v_lshlrev_b32_e32 v237, 2, v226
	s_lshl_b32 s96, s93, 2
	s_add_u32 s94, s16, s96
	s_addc_u32 s95, s17, 0
	global_load_dwordx4 v[72:75], v237, s[94:95] offset:0
	global_load_dwordx4 v[80:83], v237, s[94:95] offset:16
	global_load_dwordx4 v[88:91], v237, s[94:95] offset:128
	global_load_dwordx4 v[92:95], v237, s[94:95] offset:144
	s_add_u32 s94, s18, s96
	s_addc_u32 s95, s19, 0
	global_load_dwordx4 v[136:139], v237, s[94:95] offset:0
	global_load_dwordx4 v[148:151], v237, s[94:95] offset:16
	global_load_dwordx4 v[152:155], v237, s[94:95] offset:128
	global_load_dwordx4 v[156:159], v237, s[94:95] offset:144
	s_add_u32 s94, s14, s96
	s_addc_u32 s95, s15, 0
	global_load_dwordx4 v[160:163], v237, s[94:95] offset:0
	global_load_dwordx4 v[164:167], v237, s[94:95] offset:16
	global_load_dwordx4 v[168:171], v237, s[94:95] offset:128
	global_load_dwordx4 v[172:175], v237, s[94:95] offset:144
	v_lshlrev_b32_e32 v190, 3, v227
	s_lshl_b32 s96, s92, 3
	s_add_u32 s94, s12, s96
	s_addc_u32 s95, s13, 0
	global_load_dwordx2 v[238:239], v190, s[94:95] offset:0
	global_load_dwordx2 v[192:193], v190, s[94:95] offset:128
	global_load_dwordx2 v[194:195], v190, s[94:95] offset:256
	global_load_dwordx2 v[196:197], v190, s[94:95] offset:384
	global_load_dwordx2 v[198:199], v190, s[94:95] offset:1024
	global_load_dwordx2 v[200:201], v190, s[94:95] offset:1152
	global_load_dwordx2 v[202:203], v190, s[94:95] offset:1280
	global_load_dwordx2 v[204:205], v190, s[94:95] offset:1408
	v_mul_u32_u24_e32 v191, 0x600, v227
	v_lshl_add_u32 v191, v226, 1, v191
	s_mul_i32 s96, s92, 0x600
	s_lshl_b32 s97, s93, 1
	s_add_u32 s96, s96, s97
	s_add_u32 s98, s10, s96
	s_addc_u32 s99, s11, 0
	s_add_u32 s94, s98, 0x0
	s_addc_u32 s95, s99, 0
	global_load_dwordx4 v[208:211], v191, s[94:95] offset:0 nt
	global_load_dwordx4 v[212:215], v191, s[94:95] offset:64 nt
	s_add_u32 s94, s98, 0x6000
	s_addc_u32 s95, s99, 0
	global_load_dwordx4 v[216:219], v191, s[94:95] offset:0 nt
	global_load_dwordx4 v[220:223], v191, s[94:95] offset:64 nt
	v_add_u32_e32 v224, s92, v229
	v_mul_u32_u24_e32 v224, 0x600, v224
	s_lshl_b32 s97, s93, 1
	v_add3_u32 v224, v224, v230, s97
	s_lshl_b32 s96, s83, 2
	s_lshr_b32 s97, s60, 6
	s_add_u32 s96, s96, s97
	s_lshl_b32 s96, s96, 19
	s_lshl_b32 s97, s92, 3
	s_add_u32 s96, s96, s97
	s_add_u32 s100, s28, s96
	s_addc_u32 s101, s29, 0
	s_waitcnt vmcnt(19)
	v_pk_add_f32 v[72:73], v[72:73], v[136:137]
	v_pk_add_f32 v[74:75], v[74:75], v[138:139]
	s_waitcnt vmcnt(18)
	v_pk_add_f32 v[80:81], v[80:81], v[148:149]
	v_pk_add_f32 v[82:83], v[82:83], v[150:151]
	s_waitcnt vmcnt(17)
	v_pk_add_f32 v[88:89], v[88:89], v[152:153]
	v_pk_add_f32 v[90:91], v[90:91], v[154:155]
	s_waitcnt vmcnt(16)
	v_pk_add_f32 v[92:93], v[92:93], v[156:157]
	v_pk_add_f32 v[94:95], v[94:95], v[158:159]
	v_pk_add_f32 v[144:145], v[144:145], v[72:73]
	v_pk_add_f32 v[146:147], v[146:147], v[74:75]
	v_pk_add_f32 v[124:125], v[124:125], v[72:73]
	v_pk_add_f32 v[126:127], v[126:127], v[74:75]
	v_pk_add_f32 v[108:109], v[108:109], v[72:73]
	v_pk_add_f32 v[110:111], v[110:111], v[74:75]
	v_pk_add_f32 v[84:85], v[84:85], v[72:73]
	v_pk_add_f32 v[86:87], v[86:87], v[74:75]
	v_pk_add_f32 v[60:61], v[60:61], v[72:73]
	v_pk_add_f32 v[62:63], v[62:63], v[74:75]
	v_pk_add_f32 v[44:45], v[44:45], v[72:73]
	v_pk_add_f32 v[46:47], v[46:47], v[74:75]
	v_pk_add_f32 v[28:29], v[28:29], v[72:73]
	v_pk_add_f32 v[30:31], v[30:31], v[74:75]
	v_pk_add_f32 v[12:13], v[12:13], v[72:73]
	v_pk_add_f32 v[14:15], v[14:15], v[74:75]
	v_pk_add_f32 v[140:141], v[140:141], v[80:81]
	v_pk_add_f32 v[142:143], v[142:143], v[82:83]
	v_pk_add_f32 v[120:121], v[120:121], v[80:81]
	v_pk_add_f32 v[122:123], v[122:123], v[82:83]
	v_pk_add_f32 v[104:105], v[104:105], v[80:81]
	v_pk_add_f32 v[106:107], v[106:107], v[82:83]
	v_pk_add_f32 v[76:77], v[76:77], v[80:81]
	v_pk_add_f32 v[78:79], v[78:79], v[82:83]
	v_pk_add_f32 v[56:57], v[56:57], v[80:81]
	v_pk_add_f32 v[58:59], v[58:59], v[82:83]
	v_pk_add_f32 v[40:41], v[40:41], v[80:81]
	v_pk_add_f32 v[42:43], v[42:43], v[82:83]
	v_pk_add_f32 v[24:25], v[24:25], v[80:81]
	v_pk_add_f32 v[26:27], v[26:27], v[82:83]
	v_pk_add_f32 v[8:9], v[8:9], v[80:81]
	v_pk_add_f32 v[10:11], v[10:11], v[82:83]
	v_pk_add_f32 v[132:133], v[132:133], v[88:89]
	v_pk_add_f32 v[134:135], v[134:135], v[90:91]
	v_pk_add_f32 v[116:117], v[116:117], v[88:89]
	v_pk_add_f32 v[118:119], v[118:119], v[90:91]
	v_pk_add_f32 v[100:101], v[100:101], v[88:89]
	v_pk_add_f32 v[102:103], v[102:103], v[90:91]
	v_pk_add_f32 v[68:69], v[68:69], v[88:89]
	v_pk_add_f32 v[70:71], v[70:71], v[90:91]
	v_pk_add_f32 v[52:53], v[52:53], v[88:89]
	v_pk_add_f32 v[54:55], v[54:55], v[90:91]
	v_pk_add_f32 v[36:37], v[36:37], v[88:89]
	v_pk_add_f32 v[38:39], v[38:39], v[90:91]
	v_pk_add_f32 v[20:21], v[20:21], v[88:89]
	v_pk_add_f32 v[22:23], v[22:23], v[90:91]
	v_pk_add_f32 v[4:5], v[4:5], v[88:89]
	v_pk_add_f32 v[6:7], v[6:7], v[90:91]
	v_pk_add_f32 v[128:129], v[128:129], v[92:93]
	v_pk_add_f32 v[130:131], v[130:131], v[94:95]
	v_pk_add_f32 v[112:113], v[112:113], v[92:93]
	v_pk_add_f32 v[114:115], v[114:115], v[94:95]
	v_pk_add_f32 v[96:97], v[96:97], v[92:93]
	v_pk_add_f32 v[98:99], v[98:99], v[94:95]
	v_pk_add_f32 v[64:65], v[64:65], v[92:93]
	v_pk_add_f32 v[66:67], v[66:67], v[94:95]
	v_pk_add_f32 v[48:49], v[48:49], v[92:93]
	v_pk_add_f32 v[50:51], v[50:51], v[94:95]
	v_pk_add_f32 v[32:33], v[32:33], v[92:93]
	v_pk_add_f32 v[34:35], v[34:35], v[94:95]
	v_pk_add_f32 v[16:17], v[16:17], v[92:93]
	v_pk_add_f32 v[18:19], v[18:19], v[94:95]
	v_pk_add_f32 v[0:1], v[0:1], v[92:93]
	v_pk_add_f32 v[2:3], v[2:3], v[94:95]
	s_add_u32 s94, s98, 0xc000
	s_addc_u32 s95, s99, 0
	global_load_dwordx4 v[240:243], v191, s[94:95] offset:0 nt
	global_load_dwordx4 v[244:247], v191, s[94:95] offset:64 nt
	s_add_u32 s94, s98, 0x12000
	s_addc_u32 s95, s99, 0
	global_load_dwordx4 v[248:251], v191, s[94:95] offset:0 nt
	global_load_dwordx4 v[252:255], v191, s[94:95] offset:64 nt
	s_add_u32 s94, s98, 0x30000
	s_addc_u32 s95, s99, 0
	global_load_dwordx4 v[136:139], v191, s[94:95] offset:0 nt
	global_load_dwordx4 v[148:151], v191, s[94:95] offset:64 nt
	s_add_u32 s94, s98, 0x36000
	s_addc_u32 s95, s99, 0
	global_load_dwordx4 v[152:155], v191, s[94:95] offset:0 nt
	global_load_dwordx4 v[156:159], v191, s[94:95] offset:64 nt
	s_waitcnt vmcnt(19)
	s_waitcnt vmcnt(11)
	v_cvt_f32_f16_e32 v72, v208
	v_cvt_f32_f16_sdwa v73, v208 dst_sel:DWORD dst_unused:UNUSED_PAD src0_sel:WORD_1
	v_cvt_f32_f16_e32 v74, v209
	v_cvt_f32_f16_sdwa v75, v209 dst_sel:DWORD dst_unused:UNUSED_PAD src0_sel:WORD_1
	v_cvt_f32_f16_e32 v80, v210
	v_cvt_f32_f16_sdwa v81, v210 dst_sel:DWORD dst_unused:UNUSED_PAD src0_sel:WORD_1
	v_cvt_f32_f16_e32 v82, v211
	v_cvt_f32_f16_sdwa v83, v211 dst_sel:DWORD dst_unused:UNUSED_PAD src0_sel:WORD_1
	v_sub_f32_e32 v72, v72, v238
	v_sub_f32_e32 v73, v73, v238
	v_sub_f32_e32 v74, v74, v238
	v_sub_f32_e32 v75, v75, v238
	v_sub_f32_e32 v80, v80, v238
	v_sub_f32_e32 v81, v81, v238
	v_sub_f32_e32 v82, v82, v238
	v_sub_f32_e32 v83, v83, v238
	v_pk_mul_f32 v[72:73], v[238:239], v[72:73] op_sel:[1,0]
	v_pk_mul_f32 v[74:75], v[238:239], v[74:75] op_sel:[1,0]
	v_pk_mul_f32 v[80:81], v[238:239], v[80:81] op_sel:[1,0]
	v_pk_mul_f32 v[82:83], v[238:239], v[82:83] op_sel:[1,0]
	v_pk_fma_f32 v[144:145], v[72:73], v[160:161], v[144:145]
	v_pk_fma_f32 v[146:147], v[74:75], v[162:163], v[146:147]
	v_pk_fma_f32 v[140:141], v[80:81], v[164:165], v[140:141]
	v_pk_fma_f32 v[142:143], v[82:83], v[166:167], v[142:143]
	v_cvt_pk_f16_f32 v144, v144, v145
	v_cvt_pk_f16_f32 v145, v146, v147
	v_cvt_pk_f16_f32 v146, v140, v141
	v_cvt_pk_f16_f32 v147, v142, v143
	ds_write_b128 v235, v[144:147]
	v_fma_mix_f32 v206, v144, 1.0, 0 op_sel_hi:[1,0,0]
	v_fma_mix_f32 v207, v144, v144, 0 op_sel_hi:[1,1,0]
	v_fma_mix_f32 v206, v144, 1.0, v206 op_sel:[1,0,0] op_sel_hi:[1,0,0]
	v_fma_mix_f32 v207, v144, v144, v207 op_sel:[1,1,0] op_sel_hi:[1,1,0]
	v_fma_mix_f32 v206, v145, 1.0, v206 op_sel_hi:[1,0,0]
	v_fma_mix_f32 v207, v145, v145, v207 op_sel_hi:[1,1,0]
	v_fma_mix_f32 v206, v145, 1.0, v206 op_sel:[1,0,0] op_sel_hi:[1,0,0]
	v_fma_mix_f32 v207, v145, v145, v207 op_sel:[1,1,0] op_sel_hi:[1,1,0]
	v_fma_mix_f32 v206, v146, 1.0, v206 op_sel_hi:[1,0,0]
	v_fma_mix_f32 v207, v146, v146, v207 op_sel_hi:[1,1,0]
	v_fma_mix_f32 v206, v146, 1.0, v206 op_sel:[1,0,0] op_sel_hi:[1,0,0]
	v_fma_mix_f32 v207, v146, v146, v207 op_sel:[1,1,0] op_sel_hi:[1,1,0]
	v_fma_mix_f32 v206, v147, 1.0, v206 op_sel_hi:[1,0,0]
	v_fma_mix_f32 v207, v147, v147, v207 op_sel_hi:[1,1,0]
	v_fma_mix_f32 v206, v147, 1.0, v206 op_sel:[1,0,0] op_sel_hi:[1,0,0]
	v_fma_mix_f32 v207, v147, v147, v207 op_sel:[1,1,0] op_sel_hi:[1,1,0]
	s_waitcnt vmcnt(10)
	v_cvt_f32_f16_e32 v72, v212
	v_cvt_f32_f16_sdwa v73, v212 dst_sel:DWORD dst_unused:UNUSED_PAD src0_sel:WORD_1
	v_cvt_f32_f16_e32 v74, v213
	v_cvt_f32_f16_sdwa v75, v213 dst_sel:DWORD dst_unused:UNUSED_PAD src0_sel:WORD_1
	v_cvt_f32_f16_e32 v80, v214
	v_cvt_f32_f16_sdwa v81, v214 dst_sel:DWORD dst_unused:UNUSED_PAD src0_sel:WORD_1
	v_cvt_f32_f16_e32 v82, v215
	v_cvt_f32_f16_sdwa v83, v215 dst_sel:DWORD dst_unused:UNUSED_PAD src0_sel:WORD_1
	v_sub_f32_e32 v72, v72, v238
	v_sub_f32_e32 v73, v73, v238
	v_sub_f32_e32 v74, v74, v238
	v_sub_f32_e32 v75, v75, v238
	v_sub_f32_e32 v80, v80, v238
	v_sub_f32_e32 v81, v81, v238
	v_sub_f32_e32 v82, v82, v238
	v_sub_f32_e32 v83, v83, v238
	v_pk_mul_f32 v[72:73], v[238:239], v[72:73] op_sel:[1,0]
	v_pk_mul_f32 v[74:75], v[238:239], v[74:75] op_sel:[1,0]
	v_pk_mul_f32 v[80:81], v[238:239], v[80:81] op_sel:[1,0]
	v_pk_mul_f32 v[82:83], v[238:239], v[82:83] op_sel:[1,0]
	v_pk_fma_f32 v[132:133], v[72:73], v[168:169], v[132:133]
	v_pk_fma_f32 v[134:135], v[74:75], v[170:171], v[134:135]
	v_pk_fma_f32 v[128:129], v[80:81], v[172:173], v[128:129]
	v_pk_fma_f32 v[130:131], v[82:83], v[174:175], v[130:131]
	v_cvt_pk_f16_f32 v132, v132, v133
	v_cvt_pk_f16_f32 v133, v134, v135
	v_cvt_pk_f16_f32 v134, v128, v129
	v_cvt_pk_f16_f32 v135, v130, v131
	ds_write_b128 v235, v[132:135] offset:64
	v_fma_mix_f32 v206, v132, 1.0, v206 op_sel_hi:[1,0,0]
	v_fma_mix_f32 v207, v132, v132, v207 op_sel_hi:[1,1,0]
	v_fma_mix_f32 v206, v132, 1.0, v206 op_sel:[1,0,0] op_sel_hi:[1,0,0]
	v_fma_mix_f32 v207, v132, v132, v207 op_sel:[1,1,0] op_sel_hi:[1,1,0]
	v_fma_mix_f32 v206, v133, 1.0, v206 op_sel_hi:[1,0,0]
	v_fma_mix_f32 v207, v133, v133, v207 op_sel_hi:[1,1,0]
	v_fma_mix_f32 v206, v133, 1.0, v206 op_sel:[1,0,0] op_sel_hi:[1,0,0]
	v_fma_mix_f32 v207, v133, v133, v207 op_sel:[1,1,0] op_sel_hi:[1,1,0]
	v_fma_mix_f32 v206, v134, 1.0, v206 op_sel_hi:[1,0,0]
	v_fma_mix_f32 v207, v134, v134, v207 op_sel_hi:[1,1,0]
	v_fma_mix_f32 v206, v134, 1.0, v206 op_sel:[1,0,0] op_sel_hi:[1,0,0]
	v_fma_mix_f32 v207, v134, v134, v207 op_sel:[1,1,0] op_sel_hi:[1,1,0]
	v_fma_mix_f32 v206, v135, 1.0, v206 op_sel_hi:[1,0,0]
	v_fma_mix_f32 v207, v135, v135, v207 op_sel_hi:[1,1,0]
	v_fma_mix_f32 v206, v135, 1.0, v206 op_sel:[1,0,0] op_sel_hi:[1,0,0]
	v_fma_mix_f32 v207, v135, v135, v207 op_sel:[1,1,0] op_sel_hi:[1,1,0]
	ds_read_b128 v[88:91], v236
	ds_read_b128 v[92:95], v236 offset:1152
	s_waitcnt vmcnt(9)
	v_cvt_f32_f16_e32 v72, v216
	v_cvt_f32_f16_sdwa v73, v216 dst_sel:DWORD dst_unused:UNUSED_PAD src0_sel:WORD_1
	v_cvt_f32_f16_e32 v74, v217
	v_cvt_f32_f16_sdwa v75, v217 dst_sel:DWORD dst_unused:UNUSED_PAD src0_sel:WORD_1
	v_cvt_f32_f16_e32 v80, v218
	v_cvt_f32_f16_sdwa v81, v218 dst_sel:DWORD dst_unused:UNUSED_PAD src0_sel:WORD_1
	v_cvt_f32_f16_e32 v82, v219
	v_cvt_f32_f16_sdwa v83, v219 dst_sel:DWORD dst_unused:UNUSED_PAD src0_sel:WORD_1
	v_sub_f32_e32 v72, v72, v192
	v_sub_f32_e32 v73, v73, v192
	v_sub_f32_e32 v74, v74, v192
	v_sub_f32_e32 v75, v75, v192
	v_sub_f32_e32 v80, v80, v192
	v_sub_f32_e32 v81, v81, v192
	v_sub_f32_e32 v82, v82, v192
	v_sub_f32_e32 v83, v83, v192
	v_pk_mul_f32 v[72:73], v[192:193], v[72:73] op_sel:[1,0]
	v_pk_mul_f32 v[74:75], v[192:193], v[74:75] op_sel:[1,0]
	v_pk_mul_f32 v[80:81], v[192:193], v[80:81] op_sel:[1,0]
	v_pk_mul_f32 v[82:83], v[192:193], v[82:83] op_sel:[1,0]
	v_pk_fma_f32 v[124:125], v[72:73], v[160:161], v[124:125]
	v_pk_fma_f32 v[126:127], v[74:75], v[162:163], v[126:127]
	v_pk_fma_f32 v[120:121], v[80:81], v[164:165], v[120:121]
	v_pk_fma_f32 v[122:123], v[82:83], v[166:167], v[122:123]
	v_cvt_pk_f16_f32 v124, v124, v125
	v_cvt_pk_f16_f32 v125, v126, v127
	v_cvt_pk_f16_f32 v126, v120, v121
	v_cvt_pk_f16_f32 v127, v122, v123
	s_waitcnt lgkmcnt(0)
	buffer_store_dwordx4 v[88:91], v224, s[24:27], 0 offen nt
	v_add_u32_e32 v82, 0x3000, v224
	buffer_store_dwordx4 v[92:95], v82, s[24:27], 0 offen nt
	ds_write_b128 v235, v[124:127]
	v_fma_mix_f32 v140, v124, 1.0, 0 op_sel_hi:[1,0,0]
	v_fma_mix_f32 v141, v124, v124, 0 op_sel_hi:[1,1,0]
	v_fma_mix_f32 v140, v124, 1.0, v140 op_sel:[1,0,0] op_sel_hi:[1,0,0]
	v_fma_mix_f32 v141, v124, v124, v141 op_sel:[1,1,0] op_sel_hi:[1,1,0]
	v_fma_mix_f32 v140, v125, 1.0, v140 op_sel_hi:[1,0,0]
	v_fma_mix_f32 v141, v125, v125, v141 op_sel_hi:[1,1,0]
	v_fma_mix_f32 v140, v125, 1.0, v140 op_sel:[1,0,0] op_sel_hi:[1,0,0]
	v_fma_mix_f32 v141, v125, v125, v141 op_sel:[1,1,0] op_sel_hi:[1,1,0]
	v_fma_mix_f32 v140, v126, 1.0, v140 op_sel_hi:[1,0,0]
	v_fma_mix_f32 v141, v126, v126, v141 op_sel_hi:[1,1,0]
	v_fma_mix_f32 v140, v126, 1.0, v140 op_sel:[1,0,0] op_sel_hi:[1,0,0]
	v_fma_mix_f32 v141, v126, v126, v141 op_sel:[1,1,0] op_sel_hi:[1,1,0]
	v_fma_mix_f32 v140, v127, 1.0, v140 op_sel_hi:[1,0,0]
	v_fma_mix_f32 v141, v127, v127, v141 op_sel_hi:[1,1,0]
	v_fma_mix_f32 v140, v127, 1.0, v140 op_sel:[1,0,0] op_sel_hi:[1,0,0]
	v_fma_mix_f32 v141, v127, v127, v141 op_sel:[1,1,0] op_sel_hi:[1,1,0]
	s_waitcnt vmcnt(10)
	v_cvt_f32_f16_e32 v72, v220
	v_cvt_f32_f16_sdwa v73, v220 dst_sel:DWORD dst_unused:UNUSED_PAD src0_sel:WORD_1
	v_cvt_f32_f16_e32 v74, v221
	v_cvt_f32_f16_sdwa v75, v221 dst_sel:DWORD dst_unused:UNUSED_PAD src0_sel:WORD_1
	v_cvt_f32_f16_e32 v80, v222
	v_cvt_f32_f16_sdwa v81, v222 dst_sel:DWORD dst_unused:UNUSED_PAD src0_sel:WORD_1
	v_cvt_f32_f16_e32 v82, v223
	v_cvt_f32_f16_sdwa v83, v223 dst_sel:DWORD dst_unused:UNUSED_PAD src0_sel:WORD_1
	v_sub_f32_e32 v72, v72, v192
	v_sub_f32_e32 v73, v73, v192
	v_sub_f32_e32 v74, v74, v192
	v_sub_f32_e32 v75, v75, v192
	v_sub_f32_e32 v80, v80, v192
	v_sub_f32_e32 v81, v81, v192
	v_sub_f32_e32 v82, v82, v192
	v_sub_f32_e32 v83, v83, v192
	v_pk_mul_f32 v[72:73], v[192:193], v[72:73] op_sel:[1,0]
	v_pk_mul_f32 v[74:75], v[192:193], v[74:75] op_sel:[1,0]
	v_pk_mul_f32 v[80:81], v[192:193], v[80:81] op_sel:[1,0]
	v_pk_mul_f32 v[82:83], v[192:193], v[82:83] op_sel:[1,0]
	v_pk_fma_f32 v[116:117], v[72:73], v[168:169], v[116:117]
	v_pk_fma_f32 v[118:119], v[74:75], v[170:171], v[118:119]
	v_pk_fma_f32 v[112:113], v[80:81], v[172:173], v[112:113]
	v_pk_fma_f32 v[114:115], v[82:83], v[174:175], v[114:115]
	v_cvt_pk_f16_f32 v116, v116, v117
	v_cvt_pk_f16_f32 v117, v118, v119
	v_cvt_pk_f16_f32 v118, v112, v113
	v_cvt_pk_f16_f32 v119, v114, v115
	ds_write_b128 v235, v[116:119] offset:64
	v_fma_mix_f32 v140, v116, 1.0, v140 op_sel_hi:[1,0,0]
	v_fma_mix_f32 v141, v116, v116, v141 op_sel_hi:[1,1,0]
	v_fma_mix_f32 v140, v116, 1.0, v140 op_sel:[1,0,0] op_sel_hi:[1,0,0]
	v_fma_mix_f32 v141, v116, v116, v141 op_sel:[1,1,0] op_sel_hi:[1,1,0]
	v_fma_mix_f32 v140, v117, 1.0, v140 op_sel_hi:[1,0,0]
	v_fma_mix_f32 v141, v117, v117, v141 op_sel_hi:[1,1,0]
	v_fma_mix_f32 v140, v117, 1.0, v140 op_sel:[1,0,0] op_sel_hi:[1,0,0]
	v_fma_mix_f32 v141, v117, v117, v141 op_sel:[1,1,0] op_sel_hi:[1,1,0]
	v_fma_mix_f32 v140, v118, 1.0, v140 op_sel_hi:[1,0,0]
	v_fma_mix_f32 v141, v118, v118, v141 op_sel_hi:[1,1,0]
	v_fma_mix_f32 v140, v118, 1.0, v140 op_sel:[1,0,0] op_sel_hi:[1,0,0]
	v_fma_mix_f32 v141, v118, v118, v141 op_sel:[1,1,0] op_sel_hi:[1,1,0]
	v_fma_mix_f32 v140, v119, 1.0, v140 op_sel_hi:[1,0,0]
	v_fma_mix_f32 v141, v119, v119, v141 op_sel_hi:[1,1,0]
	v_fma_mix_f32 v140, v119, 1.0, v140 op_sel:[1,0,0] op_sel_hi:[1,0,0]
	v_fma_mix_f32 v141, v119, v119, v141 op_sel:[1,1,0] op_sel_hi:[1,1,0]
	ds_read_b128 v[208:211], v236
	ds_read_b128 v[128:131], v236 offset:1152
	s_add_u32 s94, s98, 0x3c000
	s_addc_u32 s95, s99, 0
	global_load_dwordx4 v[212:215], v191, s[94:95] offset:0 nt
	global_load_dwordx4 v[144:147], v191, s[94:95] offset:64 nt
	s_add_u32 s94, s98, 0x42000
	s_addc_u32 s95, s99, 0
	global_load_dwordx4 v[132:135], v191, s[94:95] offset:0 nt
	global_load_dwordx4 v[88:91], v191, s[94:95] offset:64 nt
	s_waitcnt vmcnt(13)
	v_cvt_f32_f16_e32 v72, v240
	v_cvt_f32_f16_sdwa v73, v240 dst_sel:DWORD dst_unused:UNUSED_PAD src0_sel:WORD_1
	v_cvt_f32_f16_e32 v74, v241
	v_cvt_f32_f16_sdwa v75, v241 dst_sel:DWORD dst_unused:UNUSED_PAD src0_sel:WORD_1
	v_cvt_f32_f16_e32 v80, v242
	v_cvt_f32_f16_sdwa v81, v242 dst_sel:DWORD dst_unused:UNUSED_PAD src0_sel:WORD_1
	v_cvt_f32_f16_e32 v82, v243
	v_cvt_f32_f16_sdwa v83, v243 dst_sel:DWORD dst_unused:UNUSED_PAD src0_sel:WORD_1
	v_sub_f32_e32 v72, v72, v194
	v_sub_f32_e32 v73, v73, v194
	v_sub_f32_e32 v74, v74, v194
	v_sub_f32_e32 v75, v75, v194
	v_sub_f32_e32 v80, v80, v194
	v_sub_f32_e32 v81, v81, v194
	v_sub_f32_e32 v82, v82, v194
	v_sub_f32_e32 v83, v83, v194
	v_pk_mul_f32 v[72:73], v[194:195], v[72:73] op_sel:[1,0]
	v_pk_mul_f32 v[74:75], v[194:195], v[74:75] op_sel:[1,0]
	v_pk_mul_f32 v[80:81], v[194:195], v[80:81] op_sel:[1,0]
	v_pk_mul_f32 v[82:83], v[194:195], v[82:83] op_sel:[1,0]
	v_pk_fma_f32 v[108:109], v[72:73], v[160:161], v[108:109]
	v_pk_fma_f32 v[110:111], v[74:75], v[162:163], v[110:111]
	v_pk_fma_f32 v[104:105], v[80:81], v[164:165], v[104:105]
	v_pk_fma_f32 v[106:107], v[82:83], v[166:167], v[106:107]
	v_cvt_pk_f16_f32 v108, v108, v109
	v_cvt_pk_f16_f32 v109, v110, v111
	v_cvt_pk_f16_f32 v110, v104, v105
	v_cvt_pk_f16_f32 v111, v106, v107
	s_waitcnt lgkmcnt(0)
	v_add_u32_e32 v83, 0x6000, v224
	buffer_store_dwordx4 v[208:211], v83, s[24:27], 0 offen nt
	v_add_u32_e32 v82, 0x9000, v224
	buffer_store_dwordx4 v[128:131], v82, s[24:27], 0 offen nt
	ds_write_b128 v235, v[108:111]
	v_fma_mix_f32 v142, v108, 1.0, 0 op_sel_hi:[1,0,0]
	v_fma_mix_f32 v143, v108, v108, 0 op_sel_hi:[1,1,0]
	v_fma_mix_f32 v142, v108, 1.0, v142 op_sel:[1,0,0] op_sel_hi:[1,0,0]
	v_fma_mix_f32 v143, v108, v108, v143 op_sel:[1,1,0] op_sel_hi:[1,1,0]
	v_fma_mix_f32 v142, v109, 1.0, v142 op_sel_hi:[1,0,0]
	v_fma_mix_f32 v143, v109, v109, v143 op_sel_hi:[1,1,0]
	v_fma_mix_f32 v142, v109, 1.0, v142 op_sel:[1,0,0] op_sel_hi:[1,0,0]
	v_fma_mix_f32 v143, v109, v109, v143 op_sel:[1,1,0] op_sel_hi:[1,1,0]
	v_fma_mix_f32 v142, v110, 1.0, v142 op_sel_hi:[1,0,0]
	v_fma_mix_f32 v143, v110, v110, v143 op_sel_hi:[1,1,0]
	v_fma_mix_f32 v142, v110, 1.0, v142 op_sel:[1,0,0] op_sel_hi:[1,0,0]
	v_fma_mix_f32 v143, v110, v110, v143 op_sel:[1,1,0] op_sel_hi:[1,1,0]
	v_fma_mix_f32 v142, v111, 1.0, v142 op_sel_hi:[1,0,0]
	v_fma_mix_f32 v143, v111, v111, v143 op_sel_hi:[1,1,0]
	v_fma_mix_f32 v142, v111, 1.0, v142 op_sel:[1,0,0] op_sel_hi:[1,0,0]
	v_fma_mix_f32 v143, v111, v111, v143 op_sel:[1,1,0] op_sel_hi:[1,1,0]
	s_waitcnt vmcnt(14)
	v_cvt_f32_f16_e32 v72, v244
	v_cvt_f32_f16_sdwa v73, v244 dst_sel:DWORD dst_unused:UNUSED_PAD src0_sel:WORD_1
	v_cvt_f32_f16_e32 v74, v245
	v_cvt_f32_f16_sdwa v75, v245 dst_sel:DWORD dst_unused:UNUSED_PAD src0_sel:WORD_1
	v_cvt_f32_f16_e32 v80, v246
	v_cvt_f32_f16_sdwa v81, v246 dst_sel:DWORD dst_unused:UNUSED_PAD src0_sel:WORD_1
	v_cvt_f32_f16_e32 v82, v247
	v_cvt_f32_f16_sdwa v83, v247 dst_sel:DWORD dst_unused:UNUSED_PAD src0_sel:WORD_1
	v_sub_f32_e32 v72, v72, v194
	v_sub_f32_e32 v73, v73, v194
	v_sub_f32_e32 v74, v74, v194
	v_sub_f32_e32 v75, v75, v194
	v_sub_f32_e32 v80, v80, v194
	v_sub_f32_e32 v81, v81, v194
	v_sub_f32_e32 v82, v82, v194
	v_sub_f32_e32 v83, v83, v194
	v_pk_mul_f32 v[72:73], v[194:195], v[72:73] op_sel:[1,0]
	v_pk_mul_f32 v[74:75], v[194:195], v[74:75] op_sel:[1,0]
	v_pk_mul_f32 v[80:81], v[194:195], v[80:81] op_sel:[1,0]
	v_pk_mul_f32 v[82:83], v[194:195], v[82:83] op_sel:[1,0]
	v_pk_fma_f32 v[100:101], v[72:73], v[168:169], v[100:101]
	v_pk_fma_f32 v[102:103], v[74:75], v[170:171], v[102:103]
	v_pk_fma_f32 v[96:97], v[80:81], v[172:173], v[96:97]
	v_pk_fma_f32 v[98:99], v[82:83], v[174:175], v[98:99]
	v_cvt_pk_f16_f32 v100, v100, v101
	v_cvt_pk_f16_f32 v101, v102, v103
	v_cvt_pk_f16_f32 v102, v96, v97
	v_cvt_pk_f16_f32 v103, v98, v99
	ds_write_b128 v235, v[100:103] offset:64
	v_fma_mix_f32 v142, v100, 1.0, v142 op_sel_hi:[1,0,0]
	v_fma_mix_f32 v143, v100, v100, v143 op_sel_hi:[1,1,0]
	v_fma_mix_f32 v142, v100, 1.0, v142 op_sel:[1,0,0] op_sel_hi:[1,0,0]
	v_fma_mix_f32 v143, v100, v100, v143 op_sel:[1,1,0] op_sel_hi:[1,1,0]
	v_fma_mix_f32 v142, v101, 1.0, v142 op_sel_hi:[1,0,0]
	v_fma_mix_f32 v143, v101, v101, v143 op_sel_hi:[1,1,0]
	v_fma_mix_f32 v142, v101, 1.0, v142 op_sel:[1,0,0] op_sel_hi:[1,0,0]
	v_fma_mix_f32 v143, v101, v101, v143 op_sel:[1,1,0] op_sel_hi:[1,1,0]
	v_fma_mix_f32 v142, v102, 1.0, v142 op_sel_hi:[1,0,0]
	v_fma_mix_f32 v143, v102, v102, v143 op_sel_hi:[1,1,0]
	v_fma_mix_f32 v142, v102, 1.0, v142 op_sel:[1,0,0] op_sel_hi:[1,0,0]
	v_fma_mix_f32 v143, v102, v102, v143 op_sel:[1,1,0] op_sel_hi:[1,1,0]
	v_fma_mix_f32 v142, v103, 1.0, v142 op_sel_hi:[1,0,0]
	v_fma_mix_f32 v143, v103, v103, v143 op_sel_hi:[1,1,0]
	v_fma_mix_f32 v142, v103, 1.0, v142 op_sel:[1,0,0] op_sel_hi:[1,0,0]
	v_fma_mix_f32 v143, v103, v103, v143 op_sel:[1,1,0] op_sel_hi:[1,1,0]
	ds_read_b128 v[92:95], v236
	ds_read_b128 v[120:123], v236 offset:1152
	s_waitcnt vmcnt(13)
	v_cvt_f32_f16_e32 v72, v248
	v_cvt_f32_f16_sdwa v73, v248 dst_sel:DWORD dst_unused:UNUSED_PAD src0_sel:WORD_1
	v_cvt_f32_f16_e32 v74, v249
	v_cvt_f32_f16_sdwa v75, v249 dst_sel:DWORD dst_unused:UNUSED_PAD src0_sel:WORD_1
	v_cvt_f32_f16_e32 v80, v250
	v_cvt_f32_f16_sdwa v81, v250 dst_sel:DWORD dst_unused:UNUSED_PAD src0_sel:WORD_1
	v_cvt_f32_f16_e32 v82, v251
	v_cvt_f32_f16_sdwa v83, v251 dst_sel:DWORD dst_unused:UNUSED_PAD src0_sel:WORD_1
	v_sub_f32_e32 v72, v72, v196
	v_sub_f32_e32 v73, v73, v196
	v_sub_f32_e32 v74, v74, v196
	v_sub_f32_e32 v75, v75, v196
	v_sub_f32_e32 v80, v80, v196
	v_sub_f32_e32 v81, v81, v196
	v_sub_f32_e32 v82, v82, v196
	v_sub_f32_e32 v83, v83, v196
	v_pk_mul_f32 v[72:73], v[196:197], v[72:73] op_sel:[1,0]
	v_pk_mul_f32 v[74:75], v[196:197], v[74:75] op_sel:[1,0]
	v_pk_mul_f32 v[80:81], v[196:197], v[80:81] op_sel:[1,0]
	v_pk_mul_f32 v[82:83], v[196:197], v[82:83] op_sel:[1,0]
	v_pk_fma_f32 v[84:85], v[72:73], v[160:161], v[84:85]
	v_pk_fma_f32 v[86:87], v[74:75], v[162:163], v[86:87]
	v_pk_fma_f32 v[76:77], v[80:81], v[164:165], v[76:77]
	v_pk_fma_f32 v[78:79], v[82:83], v[166:167], v[78:79]
	v_cvt_pk_f16_f32 v84, v84, v85
	v_cvt_pk_f16_f32 v85, v86, v87
	v_cvt_pk_f16_f32 v86, v76, v77
	v_cvt_pk_f16_f32 v87, v78, v79
	s_waitcnt lgkmcnt(0)
	v_add_u32_e32 v83, 0xc000, v224
	buffer_store_dwordx4 v[92:95], v83, s[24:27], 0 offen nt
	v_add_u32_e32 v82, 0xf000, v224
	buffer_store_dwordx4 v[120:123], v82, s[24:27], 0 offen nt
	ds_write_b128 v235, v[84:87]
	v_fma_mix_f32 v216, v84, 1.0, 0 op_sel_hi:[1,0,0]
	v_fma_mix_f32 v217, v84, v84, 0 op_sel_hi:[1,1,0]
	v_fma_mix_f32 v216, v84, 1.0, v216 op_sel:[1,0,0] op_sel_hi:[1,0,0]
	v_fma_mix_f32 v217, v84, v84, v217 op_sel:[1,1,0] op_sel_hi:[1,1,0]
	v_fma_mix_f32 v216, v85, 1.0, v216 op_sel_hi:[1,0,0]
	v_fma_mix_f32 v217, v85, v85, v217 op_sel_hi:[1,1,0]
	v_fma_mix_f32 v216, v85, 1.0, v216 op_sel:[1,0,0] op_sel_hi:[1,0,0]
	v_fma_mix_f32 v217, v85, v85, v217 op_sel:[1,1,0] op_sel_hi:[1,1,0]
	v_fma_mix_f32 v216, v86, 1.0, v216 op_sel_hi:[1,0,0]
	v_fma_mix_f32 v217, v86, v86, v217 op_sel_hi:[1,1,0]
	v_fma_mix_f32 v216, v86, 1.0, v216 op_sel:[1,0,0] op_sel_hi:[1,0,0]
	v_fma_mix_f32 v217, v86, v86, v217 op_sel:[1,1,0] op_sel_hi:[1,1,0]
	v_fma_mix_f32 v216, v87, 1.0, v216 op_sel_hi:[1,0,0]
	v_fma_mix_f32 v217, v87, v87, v217 op_sel_hi:[1,1,0]
	v_fma_mix_f32 v216, v87, 1.0, v216 op_sel:[1,0,0] op_sel_hi:[1,0,0]
	v_fma_mix_f32 v217, v87, v87, v217 op_sel:[1,1,0] op_sel_hi:[1,1,0]
	s_waitcnt vmcnt(14)
	v_cvt_f32_f16_e32 v72, v252
	v_cvt_f32_f16_sdwa v73, v252 dst_sel:DWORD dst_unused:UNUSED_PAD src0_sel:WORD_1
	v_cvt_f32_f16_e32 v74, v253
	v_cvt_f32_f16_sdwa v75, v253 dst_sel:DWORD dst_unused:UNUSED_PAD src0_sel:WORD_1
	v_cvt_f32_f16_e32 v80, v254
	v_cvt_f32_f16_sdwa v81, v254 dst_sel:DWORD dst_unused:UNUSED_PAD src0_sel:WORD_1
	v_cvt_f32_f16_e32 v82, v255
	v_cvt_f32_f16_sdwa v83, v255 dst_sel:DWORD dst_unused:UNUSED_PAD src0_sel:WORD_1
	v_sub_f32_e32 v72, v72, v196
	v_sub_f32_e32 v73, v73, v196
	v_sub_f32_e32 v74, v74, v196
	v_sub_f32_e32 v75, v75, v196
	v_sub_f32_e32 v80, v80, v196
	v_sub_f32_e32 v81, v81, v196
	v_sub_f32_e32 v82, v82, v196
	v_sub_f32_e32 v83, v83, v196
	v_pk_mul_f32 v[72:73], v[196:197], v[72:73] op_sel:[1,0]
	v_pk_mul_f32 v[74:75], v[196:197], v[74:75] op_sel:[1,0]
	v_pk_mul_f32 v[80:81], v[196:197], v[80:81] op_sel:[1,0]
	v_pk_mul_f32 v[82:83], v[196:197], v[82:83] op_sel:[1,0]
	v_pk_fma_f32 v[68:69], v[72:73], v[168:169], v[68:69]
	v_pk_fma_f32 v[70:71], v[74:75], v[170:171], v[70:71]
	v_pk_fma_f32 v[64:65], v[80:81], v[172:173], v[64:65]
	v_pk_fma_f32 v[66:67], v[82:83], v[174:175], v[66:67]
	v_cvt_pk_f16_f32 v68, v68, v69
	v_cvt_pk_f16_f32 v69, v70, v71
	v_cvt_pk_f16_f32 v70, v64, v65
	v_cvt_pk_f16_f32 v71, v66, v67
	ds_write_b128 v235, v[68:71] offset:64
	v_fma_mix_f32 v216, v68, 1.0, v216 op_sel_hi:[1,0,0]
	v_fma_mix_f32 v217, v68, v68, v217 op_sel_hi:[1,1,0]
	v_fma_mix_f32 v216, v68, 1.0, v216 op_sel:[1,0,0] op_sel_hi:[1,0,0]
	v_fma_mix_f32 v217, v68, v68, v217 op_sel:[1,1,0] op_sel_hi:[1,1,0]
	v_fma_mix_f32 v216, v69, 1.0, v216 op_sel_hi:[1,0,0]
	v_fma_mix_f32 v217, v69, v69, v217 op_sel_hi:[1,1,0]
	v_fma_mix_f32 v216, v69, 1.0, v216 op_sel:[1,0,0] op_sel_hi:[1,0,0]
	v_fma_mix_f32 v217, v69, v69, v217 op_sel:[1,1,0] op_sel_hi:[1,1,0]
	v_fma_mix_f32 v216, v70, 1.0, v216 op_sel_hi:[1,0,0]
	v_fma_mix_f32 v217, v70, v70, v217 op_sel_hi:[1,1,0]
	v_fma_mix_f32 v216, v70, 1.0, v216 op_sel:[1,0,0] op_sel_hi:[1,0,0]
	v_fma_mix_f32 v217, v70, v70, v217 op_sel:[1,1,0] op_sel_hi:[1,1,0]
	v_fma_mix_f32 v216, v71, 1.0, v216 op_sel_hi:[1,0,0]
	v_fma_mix_f32 v217, v71, v71, v217 op_sel_hi:[1,1,0]
	v_fma_mix_f32 v216, v71, 1.0, v216 op_sel:[1,0,0] op_sel_hi:[1,0,0]
	v_fma_mix_f32 v217, v71, v71, v217 op_sel:[1,1,0] op_sel_hi:[1,1,0]
	ds_read_b128 v[112:115], v236
	ds_read_b128 v[220:223], v236 offset:1152
	s_waitcnt vmcnt(13)
	v_cvt_f32_f16_e32 v72, v136
	v_cvt_f32_f16_sdwa v73, v136 dst_sel:DWORD dst_unused:UNUSED_PAD src0_sel:WORD_1
	v_cvt_f32_f16_e32 v74, v137
	v_cvt_f32_f16_sdwa v75, v137 dst_sel:DWORD dst_unused:UNUSED_PAD src0_sel:WORD_1
	v_cvt_f32_f16_e32 v80, v138
	v_cvt_f32_f16_sdwa v81, v138 dst_sel:DWORD dst_unused:UNUSED_PAD src0_sel:WORD_1
	v_cvt_f32_f16_e32 v82, v139
	v_cvt_f32_f16_sdwa v83, v139 dst_sel:DWORD dst_unused:UNUSED_PAD src0_sel:WORD_1
	v_sub_f32_e32 v72, v72, v198
	v_sub_f32_e32 v73, v73, v198
	v_sub_f32_e32 v74, v74, v198
	v_sub_f32_e32 v75, v75, v198
	v_sub_f32_e32 v80, v80, v198
	v_sub_f32_e32 v81, v81, v198
	v_sub_f32_e32 v82, v82, v198
	v_sub_f32_e32 v83, v83, v198
	v_pk_mul_f32 v[72:73], v[198:199], v[72:73] op_sel:[1,0]
	v_pk_mul_f32 v[74:75], v[198:199], v[74:75] op_sel:[1,0]
	v_pk_mul_f32 v[80:81], v[198:199], v[80:81] op_sel:[1,0]
	v_pk_mul_f32 v[82:83], v[198:199], v[82:83] op_sel:[1,0]
	v_pk_fma_f32 v[60:61], v[72:73], v[160:161], v[60:61]
	v_pk_fma_f32 v[62:63], v[74:75], v[162:163], v[62:63]
	v_pk_fma_f32 v[56:57], v[80:81], v[164:165], v[56:57]
	v_pk_fma_f32 v[58:59], v[82:83], v[166:167], v[58:59]
	v_cvt_pk_f16_f32 v60, v60, v61
	v_cvt_pk_f16_f32 v61, v62, v63
	v_cvt_pk_f16_f32 v62, v56, v57
	v_cvt_pk_f16_f32 v63, v58, v59
	s_waitcnt lgkmcnt(0)
	v_add_u32_e32 v83, 0x12000, v224
	buffer_store_dwordx4 v[112:115], v83, s[24:27], 0 offen nt
	v_add_u32_e32 v82, 0x15000, v224
	buffer_store_dwordx4 v[220:223], v82, s[24:27], 0 offen nt
	ds_write_b128 v235, v[60:63]
	v_fma_mix_f32 v218, v60, 1.0, 0 op_sel_hi:[1,0,0]
	v_fma_mix_f32 v219, v60, v60, 0 op_sel_hi:[1,1,0]
	v_fma_mix_f32 v218, v60, 1.0, v218 op_sel:[1,0,0] op_sel_hi:[1,0,0]
	v_fma_mix_f32 v219, v60, v60, v219 op_sel:[1,1,0] op_sel_hi:[1,1,0]
	v_fma_mix_f32 v218, v61, 1.0, v218 op_sel_hi:[1,0,0]
	v_fma_mix_f32 v219, v61, v61, v219 op_sel_hi:[1,1,0]
	v_fma_mix_f32 v218, v61, 1.0, v218 op_sel:[1,0,0] op_sel_hi:[1,0,0]
	v_fma_mix_f32 v219, v61, v61, v219 op_sel:[1,1,0] op_sel_hi:[1,1,0]
	v_fma_mix_f32 v218, v62, 1.0, v218 op_sel_hi:[1,0,0]
	v_fma_mix_f32 v219, v62, v62, v219 op_sel_hi:[1,1,0]
	v_fma_mix_f32 v218, v62, 1.0, v218 op_sel:[1,0,0] op_sel_hi:[1,0,0]
	v_fma_mix_f32 v219, v62, v62, v219 op_sel:[1,1,0] op_sel_hi:[1,1,0]
	v_fma_mix_f32 v218, v63, 1.0, v218 op_sel_hi:[1,0,0]
	v_fma_mix_f32 v219, v63, v63, v219 op_sel_hi:[1,1,0]
	v_fma_mix_f32 v218, v63, 1.0, v218 op_sel:[1,0,0] op_sel_hi:[1,0,0]
	v_fma_mix_f32 v219, v63, v63, v219 op_sel:[1,1,0] op_sel_hi:[1,1,0]
	s_waitcnt vmcnt(14)
	v_cvt_f32_f16_e32 v72, v148
	v_cvt_f32_f16_sdwa v73, v148 dst_sel:DWORD dst_unused:UNUSED_PAD src0_sel:WORD_1
	v_cvt_f32_f16_e32 v74, v149
	v_cvt_f32_f16_sdwa v75, v149 dst_sel:DWORD dst_unused:UNUSED_PAD src0_sel:WORD_1
	v_cvt_f32_f16_e32 v80, v150
	v_cvt_f32_f16_sdwa v81, v150 dst_sel:DWORD dst_unused:UNUSED_PAD src0_sel:WORD_1
	v_cvt_f32_f16_e32 v82, v151
	v_cvt_f32_f16_sdwa v83, v151 dst_sel:DWORD dst_unused:UNUSED_PAD src0_sel:WORD_1
	v_sub_f32_e32 v72, v72, v198
	v_sub_f32_e32 v73, v73, v198
	v_sub_f32_e32 v74, v74, v198
	v_sub_f32_e32 v75, v75, v198
	v_sub_f32_e32 v80, v80, v198
	v_sub_f32_e32 v81, v81, v198
	v_sub_f32_e32 v82, v82, v198
	v_sub_f32_e32 v83, v83, v198
	v_pk_mul_f32 v[72:73], v[198:199], v[72:73] op_sel:[1,0]
	v_pk_mul_f32 v[74:75], v[198:199], v[74:75] op_sel:[1,0]
	v_pk_mul_f32 v[80:81], v[198:199], v[80:81] op_sel:[1,0]
	v_pk_mul_f32 v[82:83], v[198:199], v[82:83] op_sel:[1,0]
	v_pk_fma_f32 v[52:53], v[72:73], v[168:169], v[52:53]
	v_pk_fma_f32 v[54:55], v[74:75], v[170:171], v[54:55]
	v_pk_fma_f32 v[48:49], v[80:81], v[172:173], v[48:49]
	v_pk_fma_f32 v[50:51], v[82:83], v[174:175], v[50:51]
	v_cvt_pk_f16_f32 v52, v52, v53
	v_cvt_pk_f16_f32 v53, v54, v55
	v_cvt_pk_f16_f32 v54, v48, v49
	v_cvt_pk_f16_f32 v55, v50, v51
	ds_write_b128 v235, v[52:55] offset:64
	v_fma_mix_f32 v218, v52, 1.0, v218 op_sel_hi:[1,0,0]
	v_fma_mix_f32 v219, v52, v52, v219 op_sel_hi:[1,1,0]
	v_fma_mix_f32 v218, v52, 1.0, v218 op_sel:[1,0,0] op_sel_hi:[1,0,0]
	v_fma_mix_f32 v219, v52, v52, v219 op_sel:[1,1,0] op_sel_hi:[1,1,0]
	v_fma_mix_f32 v218, v53, 1.0, v218 op_sel_hi:[1,0,0]
	v_fma_mix_f32 v219, v53, v53, v219 op_sel_hi:[1,1,0]
	v_fma_mix_f32 v218, v53, 1.0, v218 op_sel:[1,0,0] op_sel_hi:[1,0,0]
	v_fma_mix_f32 v219, v53, v53, v219 op_sel:[1,1,0] op_sel_hi:[1,1,0]
	v_fma_mix_f32 v218, v54, 1.0, v218 op_sel_hi:[1,0,0]
	v_fma_mix_f32 v219, v54, v54, v219 op_sel_hi:[1,1,0]
	v_fma_mix_f32 v218, v54, 1.0, v218 op_sel:[1,0,0] op_sel_hi:[1,0,0]
	v_fma_mix_f32 v219, v54, v54, v219 op_sel:[1,1,0] op_sel_hi:[1,1,0]
	v_fma_mix_f32 v218, v55, 1.0, v218 op_sel_hi:[1,0,0]
	v_fma_mix_f32 v219, v55, v55, v219 op_sel_hi:[1,1,0]
	v_fma_mix_f32 v218, v55, 1.0, v218 op_sel:[1,0,0] op_sel_hi:[1,0,0]
	v_fma_mix_f32 v219, v55, v55, v219 op_sel:[1,1,0] op_sel_hi:[1,1,0]
	ds_read_b128 v[124:127], v236
	ds_read_b128 v[116:119], v236 offset:1152
	s_waitcnt vmcnt(13)
	v_cvt_f32_f16_e32 v72, v152
	v_cvt_f32_f16_sdwa v73, v152 dst_sel:DWORD dst_unused:UNUSED_PAD src0_sel:WORD_1
	v_cvt_f32_f16_e32 v74, v153
	v_cvt_f32_f16_sdwa v75, v153 dst_sel:DWORD dst_unused:UNUSED_PAD src0_sel:WORD_1
	v_cvt_f32_f16_e32 v80, v154
	v_cvt_f32_f16_sdwa v81, v154 dst_sel:DWORD dst_unused:UNUSED_PAD src0_sel:WORD_1
	v_cvt_f32_f16_e32 v82, v155
	v_cvt_f32_f16_sdwa v83, v155 dst_sel:DWORD dst_unused:UNUSED_PAD src0_sel:WORD_1
	v_sub_f32_e32 v72, v72, v200
	v_sub_f32_e32 v73, v73, v200
	v_sub_f32_e32 v74, v74, v200
	v_sub_f32_e32 v75, v75, v200
	v_sub_f32_e32 v80, v80, v200
	v_sub_f32_e32 v81, v81, v200
	v_sub_f32_e32 v82, v82, v200
	v_sub_f32_e32 v83, v83, v200
	v_pk_mul_f32 v[72:73], v[200:201], v[72:73] op_sel:[1,0]
	v_pk_mul_f32 v[74:75], v[200:201], v[74:75] op_sel:[1,0]
	v_pk_mul_f32 v[80:81], v[200:201], v[80:81] op_sel:[1,0]
	v_pk_mul_f32 v[82:83], v[200:201], v[82:83] op_sel:[1,0]
	v_pk_fma_f32 v[44:45], v[72:73], v[160:161], v[44:45]
	v_pk_fma_f32 v[46:47], v[74:75], v[162:163], v[46:47]
	v_pk_fma_f32 v[40:41], v[80:81], v[164:165], v[40:41]
	v_pk_fma_f32 v[42:43], v[82:83], v[166:167], v[42:43]
	v_cvt_pk_f16_f32 v44, v44, v45
	v_cvt_pk_f16_f32 v45, v46, v47
	v_cvt_pk_f16_f32 v46, v40, v41
	v_cvt_pk_f16_f32 v47, v42, v43
	s_waitcnt lgkmcnt(0)
	v_add_u32_e32 v83, 0x30000, v224
	buffer_store_dwordx4 v[124:127], v83, s[24:27], 0 offen nt
	v_add_u32_e32 v82, 0x33000, v224
	buffer_store_dwordx4 v[116:119], v82, s[24:27], 0 offen nt
	ds_write_b128 v235, v[44:47]
	v_fma_mix_f32 v208, v44, 1.0, 0 op_sel_hi:[1,0,0]
	v_fma_mix_f32 v209, v44, v44, 0 op_sel_hi:[1,1,0]
	v_fma_mix_f32 v208, v44, 1.0, v208 op_sel:[1,0,0] op_sel_hi:[1,0,0]
	v_fma_mix_f32 v209, v44, v44, v209 op_sel:[1,1,0] op_sel_hi:[1,1,0]
	v_fma_mix_f32 v208, v45, 1.0, v208 op_sel_hi:[1,0,0]
	v_fma_mix_f32 v209, v45, v45, v209 op_sel_hi:[1,1,0]
	v_fma_mix_f32 v208, v45, 1.0, v208 op_sel:[1,0,0] op_sel_hi:[1,0,0]
	v_fma_mix_f32 v209, v45, v45, v209 op_sel:[1,1,0] op_sel_hi:[1,1,0]
	v_fma_mix_f32 v208, v46, 1.0, v208 op_sel_hi:[1,0,0]
	v_fma_mix_f32 v209, v46, v46, v209 op_sel_hi:[1,1,0]
	v_fma_mix_f32 v208, v46, 1.0, v208 op_sel:[1,0,0] op_sel_hi:[1,0,0]
	v_fma_mix_f32 v209, v46, v46, v209 op_sel:[1,1,0] op_sel_hi:[1,1,0]
	v_fma_mix_f32 v208, v47, 1.0, v208 op_sel_hi:[1,0,0]
	v_fma_mix_f32 v209, v47, v47, v209 op_sel_hi:[1,1,0]
	v_fma_mix_f32 v208, v47, 1.0, v208 op_sel:[1,0,0] op_sel_hi:[1,0,0]
	v_fma_mix_f32 v209, v47, v47, v209 op_sel:[1,1,0] op_sel_hi:[1,1,0]
	s_waitcnt vmcnt(14)
	v_cvt_f32_f16_e32 v72, v156
	v_cvt_f32_f16_sdwa v73, v156 dst_sel:DWORD dst_unused:UNUSED_PAD src0_sel:WORD_1
	v_cvt_f32_f16_e32 v74, v157
	v_cvt_f32_f16_sdwa v75, v157 dst_sel:DWORD dst_unused:UNUSED_PAD src0_sel:WORD_1
	v_cvt_f32_f16_e32 v80, v158
	v_cvt_f32_f16_sdwa v81, v158 dst_sel:DWORD dst_unused:UNUSED_PAD src0_sel:WORD_1
	v_cvt_f32_f16_e32 v82, v159
	v_cvt_f32_f16_sdwa v83, v159 dst_sel:DWORD dst_unused:UNUSED_PAD src0_sel:WORD_1
	v_sub_f32_e32 v72, v72, v200
	v_sub_f32_e32 v73, v73, v200
	v_sub_f32_e32 v74, v74, v200
	v_sub_f32_e32 v75, v75, v200
	v_sub_f32_e32 v80, v80, v200
	v_sub_f32_e32 v81, v81, v200
	v_sub_f32_e32 v82, v82, v200
	v_sub_f32_e32 v83, v83, v200
	v_pk_mul_f32 v[72:73], v[200:201], v[72:73] op_sel:[1,0]
	v_pk_mul_f32 v[74:75], v[200:201], v[74:75] op_sel:[1,0]
	v_pk_mul_f32 v[80:81], v[200:201], v[80:81] op_sel:[1,0]
	v_pk_mul_f32 v[82:83], v[200:201], v[82:83] op_sel:[1,0]
	v_pk_fma_f32 v[36:37], v[72:73], v[168:169], v[36:37]
	v_pk_fma_f32 v[38:39], v[74:75], v[170:171], v[38:39]
	v_pk_fma_f32 v[32:33], v[80:81], v[172:173], v[32:33]
	v_pk_fma_f32 v[34:35], v[82:83], v[174:175], v[34:35]
	v_cvt_pk_f16_f32 v36, v36, v37
	v_cvt_pk_f16_f32 v37, v38, v39
	v_cvt_pk_f16_f32 v38, v32, v33
	v_cvt_pk_f16_f32 v39, v34, v35
	ds_write_b128 v235, v[36:39] offset:64
	v_fma_mix_f32 v208, v36, 1.0, v208 op_sel_hi:[1,0,0]
	v_fma_mix_f32 v209, v36, v36, v209 op_sel_hi:[1,1,0]
	v_fma_mix_f32 v208, v36, 1.0, v208 op_sel:[1,0,0] op_sel_hi:[1,0,0]
	v_fma_mix_f32 v209, v36, v36, v209 op_sel:[1,1,0] op_sel_hi:[1,1,0]
	v_fma_mix_f32 v208, v37, 1.0, v208 op_sel_hi:[1,0,0]
	v_fma_mix_f32 v209, v37, v37, v209 op_sel_hi:[1,1,0]
	v_fma_mix_f32 v208, v37, 1.0, v208 op_sel:[1,0,0] op_sel_hi:[1,0,0]
	v_fma_mix_f32 v209, v37, v37, v209 op_sel:[1,1,0] op_sel_hi:[1,1,0]
	v_fma_mix_f32 v208, v38, 1.0, v208 op_sel_hi:[1,0,0]
	v_fma_mix_f32 v209, v38, v38, v209 op_sel_hi:[1,1,0]
	v_fma_mix_f32 v208, v38, 1.0, v208 op_sel:[1,0,0] op_sel_hi:[1,0,0]
	v_fma_mix_f32 v209, v38, v38, v209 op_sel:[1,1,0] op_sel_hi:[1,1,0]
	v_fma_mix_f32 v208, v39, 1.0, v208 op_sel_hi:[1,0,0]
	v_fma_mix_f32 v209, v39, v39, v209 op_sel_hi:[1,1,0]
	v_fma_mix_f32 v208, v39, 1.0, v208 op_sel:[1,0,0] op_sel_hi:[1,0,0]
	v_fma_mix_f32 v209, v39, v39, v209 op_sel:[1,1,0] op_sel_hi:[1,1,0]
	ds_read_b128 v[128:131], v236
	ds_read_b128 v[104:107], v236 offset:1152
	s_waitcnt vmcnt(11)
	v_cvt_f32_f16_e32 v72, v212
	v_cvt_f32_f16_sdwa v73, v212 dst_sel:DWORD dst_unused:UNUSED_PAD src0_sel:WORD_1
	v_cvt_f32_f16_e32 v74, v213
	v_cvt_f32_f16_sdwa v75, v213 dst_sel:DWORD dst_unused:UNUSED_PAD src0_sel:WORD_1
	v_cvt_f32_f16_e32 v80, v214
	v_cvt_f32_f16_sdwa v81, v214 dst_sel:DWORD dst_unused:UNUSED_PAD src0_sel:WORD_1
	v_cvt_f32_f16_e32 v82, v215
	v_cvt_f32_f16_sdwa v83, v215 dst_sel:DWORD dst_unused:UNUSED_PAD src0_sel:WORD_1
	v_sub_f32_e32 v72, v72, v202
	v_sub_f32_e32 v73, v73, v202
	v_sub_f32_e32 v74, v74, v202
	v_sub_f32_e32 v75, v75, v202
	v_sub_f32_e32 v80, v80, v202
	v_sub_f32_e32 v81, v81, v202
	v_sub_f32_e32 v82, v82, v202
	v_sub_f32_e32 v83, v83, v202
	v_pk_mul_f32 v[72:73], v[202:203], v[72:73] op_sel:[1,0]
	v_pk_mul_f32 v[74:75], v[202:203], v[74:75] op_sel:[1,0]
	v_pk_mul_f32 v[80:81], v[202:203], v[80:81] op_sel:[1,0]
	v_pk_mul_f32 v[82:83], v[202:203], v[82:83] op_sel:[1,0]
	v_pk_fma_f32 v[28:29], v[72:73], v[160:161], v[28:29]
	v_pk_fma_f32 v[30:31], v[74:75], v[162:163], v[30:31]
	v_pk_fma_f32 v[24:25], v[80:81], v[164:165], v[24:25]
	v_pk_fma_f32 v[26:27], v[82:83], v[166:167], v[26:27]
	v_cvt_pk_f16_f32 v28, v28, v29
	v_cvt_pk_f16_f32 v29, v30, v31
	v_cvt_pk_f16_f32 v30, v24, v25
	v_cvt_pk_f16_f32 v31, v26, v27
	s_waitcnt lgkmcnt(0)
	v_add_u32_e32 v83, 0x36000, v224
	buffer_store_dwordx4 v[128:131], v83, s[24:27], 0 offen nt
	v_add_u32_e32 v82, 0x39000, v224
	buffer_store_dwordx4 v[104:107], v82, s[24:27], 0 offen nt
	ds_write_b128 v235, v[28:31]
	v_fma_mix_f32 v210, v28, 1.0, 0 op_sel_hi:[1,0,0]
	v_fma_mix_f32 v211, v28, v28, 0 op_sel_hi:[1,1,0]
	v_fma_mix_f32 v210, v28, 1.0, v210 op_sel:[1,0,0] op_sel_hi:[1,0,0]
	v_fma_mix_f32 v211, v28, v28, v211 op_sel:[1,1,0] op_sel_hi:[1,1,0]
	v_fma_mix_f32 v210, v29, 1.0, v210 op_sel_hi:[1,0,0]
	v_fma_mix_f32 v211, v29, v29, v211 op_sel_hi:[1,1,0]
	v_fma_mix_f32 v210, v29, 1.0, v210 op_sel:[1,0,0] op_sel_hi:[1,0,0]
	v_fma_mix_f32 v211, v29, v29, v211 op_sel:[1,1,0] op_sel_hi:[1,1,0]
	v_fma_mix_f32 v210, v30, 1.0, v210 op_sel_hi:[1,0,0]
	v_fma_mix_f32 v211, v30, v30, v211 op_sel_hi:[1,1,0]
	v_fma_mix_f32 v210, v30, 1.0, v210 op_sel:[1,0,0] op_sel_hi:[1,0,0]
	v_fma_mix_f32 v211, v30, v30, v211 op_sel:[1,1,0] op_sel_hi:[1,1,0]
	v_fma_mix_f32 v210, v31, 1.0, v210 op_sel_hi:[1,0,0]
	v_fma_mix_f32 v211, v31, v31, v211 op_sel_hi:[1,1,0]
	v_fma_mix_f32 v210, v31, 1.0, v210 op_sel:[1,0,0] op_sel_hi:[1,0,0]
	v_fma_mix_f32 v211, v31, v31, v211 op_sel:[1,1,0] op_sel_hi:[1,1,0]
	s_waitcnt vmcnt(12)
	v_cvt_f32_f16_e32 v72, v144
	v_cvt_f32_f16_sdwa v73, v144 dst_sel:DWORD dst_unused:UNUSED_PAD src0_sel:WORD_1
	v_cvt_f32_f16_e32 v74, v145
	v_cvt_f32_f16_sdwa v75, v145 dst_sel:DWORD dst_unused:UNUSED_PAD src0_sel:WORD_1
	v_cvt_f32_f16_e32 v80, v146
	v_cvt_f32_f16_sdwa v81, v146 dst_sel:DWORD dst_unused:UNUSED_PAD src0_sel:WORD_1
	v_cvt_f32_f16_e32 v82, v147
	v_cvt_f32_f16_sdwa v83, v147 dst_sel:DWORD dst_unused:UNUSED_PAD src0_sel:WORD_1
	v_sub_f32_e32 v72, v72, v202
	v_sub_f32_e32 v73, v73, v202
	v_sub_f32_e32 v74, v74, v202
	v_sub_f32_e32 v75, v75, v202
	v_sub_f32_e32 v80, v80, v202
	v_sub_f32_e32 v81, v81, v202
	v_sub_f32_e32 v82, v82, v202
	v_sub_f32_e32 v83, v83, v202
	v_pk_mul_f32 v[72:73], v[202:203], v[72:73] op_sel:[1,0]
	v_pk_mul_f32 v[74:75], v[202:203], v[74:75] op_sel:[1,0]
	v_pk_mul_f32 v[80:81], v[202:203], v[80:81] op_sel:[1,0]
	v_pk_mul_f32 v[82:83], v[202:203], v[82:83] op_sel:[1,0]
	v_pk_fma_f32 v[20:21], v[72:73], v[168:169], v[20:21]
	v_pk_fma_f32 v[22:23], v[74:75], v[170:171], v[22:23]
	v_pk_fma_f32 v[16:17], v[80:81], v[172:173], v[16:17]
	v_pk_fma_f32 v[18:19], v[82:83], v[174:175], v[18:19]
	v_cvt_pk_f16_f32 v20, v20, v21
	v_cvt_pk_f16_f32 v21, v22, v23
	v_cvt_pk_f16_f32 v22, v16, v17
	v_cvt_pk_f16_f32 v23, v18, v19
	ds_write_b128 v235, v[20:23] offset:64
	v_fma_mix_f32 v210, v20, 1.0, v210 op_sel_hi:[1,0,0]
	v_fma_mix_f32 v211, v20, v20, v211 op_sel_hi:[1,1,0]
	v_fma_mix_f32 v210, v20, 1.0, v210 op_sel:[1,0,0] op_sel_hi:[1,0,0]
	v_fma_mix_f32 v211, v20, v20, v211 op_sel:[1,1,0] op_sel_hi:[1,1,0]
	v_fma_mix_f32 v210, v21, 1.0, v210 op_sel_hi:[1,0,0]
	v_fma_mix_f32 v211, v21, v21, v211 op_sel_hi:[1,1,0]
	v_fma_mix_f32 v210, v21, 1.0, v210 op_sel:[1,0,0] op_sel_hi:[1,0,0]
	v_fma_mix_f32 v211, v21, v21, v211 op_sel:[1,1,0] op_sel_hi:[1,1,0]
	v_fma_mix_f32 v210, v22, 1.0, v210 op_sel_hi:[1,0,0]
	v_fma_mix_f32 v211, v22, v22, v211 op_sel_hi:[1,1,0]
	v_fma_mix_f32 v210, v22, 1.0, v210 op_sel:[1,0,0] op_sel_hi:[1,0,0]
	v_fma_mix_f32 v211, v22, v22, v211 op_sel:[1,1,0] op_sel_hi:[1,1,0]
	v_fma_mix_f32 v210, v23, 1.0, v210 op_sel_hi:[1,0,0]
	v_fma_mix_f32 v211, v23, v23, v211 op_sel_hi:[1,1,0]
	v_fma_mix_f32 v210, v23, 1.0, v210 op_sel:[1,0,0] op_sel_hi:[1,0,0]
	v_fma_mix_f32 v211, v23, v23, v211 op_sel:[1,1,0] op_sel_hi:[1,1,0]
	ds_read_b128 v[240:243], v236
	ds_read_b128 v[96:99], v236 offset:1152
	s_waitcnt vmcnt(11)
	v_cvt_f32_f16_e32 v72, v132
	v_cvt_f32_f16_sdwa v73, v132 dst_sel:DWORD dst_unused:UNUSED_PAD src0_sel:WORD_1
	v_cvt_f32_f16_e32 v74, v133
	v_cvt_f32_f16_sdwa v75, v133 dst_sel:DWORD dst_unused:UNUSED_PAD src0_sel:WORD_1
	v_cvt_f32_f16_e32 v80, v134
	v_cvt_f32_f16_sdwa v81, v134 dst_sel:DWORD dst_unused:UNUSED_PAD src0_sel:WORD_1
	v_cvt_f32_f16_e32 v82, v135
	v_cvt_f32_f16_sdwa v83, v135 dst_sel:DWORD dst_unused:UNUSED_PAD src0_sel:WORD_1
	v_sub_f32_e32 v72, v72, v204
	v_sub_f32_e32 v73, v73, v204
	v_sub_f32_e32 v74, v74, v204
	v_sub_f32_e32 v75, v75, v204
	v_sub_f32_e32 v80, v80, v204
	v_sub_f32_e32 v81, v81, v204
	v_sub_f32_e32 v82, v82, v204
	v_sub_f32_e32 v83, v83, v204
	v_pk_mul_f32 v[72:73], v[204:205], v[72:73] op_sel:[1,0]
	v_pk_mul_f32 v[74:75], v[204:205], v[74:75] op_sel:[1,0]
	v_pk_mul_f32 v[80:81], v[204:205], v[80:81] op_sel:[1,0]
	v_pk_mul_f32 v[82:83], v[204:205], v[82:83] op_sel:[1,0]
	v_pk_fma_f32 v[12:13], v[72:73], v[160:161], v[12:13]
	v_pk_fma_f32 v[14:15], v[74:75], v[162:163], v[14:15]
	v_pk_fma_f32 v[8:9], v[80:81], v[164:165], v[8:9]
	v_pk_fma_f32 v[10:11], v[82:83], v[166:167], v[10:11]
	v_cvt_pk_f16_f32 v12, v12, v13
	v_cvt_pk_f16_f32 v13, v14, v15
	v_cvt_pk_f16_f32 v14, v8, v9
	v_cvt_pk_f16_f32 v15, v10, v11
	s_waitcnt lgkmcnt(0)
	v_add_u32_e32 v83, 0x3c000, v224
	buffer_store_dwordx4 v[240:243], v83, s[24:27], 0 offen nt
	v_add_u32_e32 v82, 0x3f000, v224
	buffer_store_dwordx4 v[96:99], v82, s[24:27], 0 offen nt
	ds_write_b128 v235, v[12:15]
	v_fma_mix_f32 v244, v12, 1.0, 0 op_sel_hi:[1,0,0]
	v_fma_mix_f32 v245, v12, v12, 0 op_sel_hi:[1,1,0]
	v_fma_mix_f32 v244, v12, 1.0, v244 op_sel:[1,0,0] op_sel_hi:[1,0,0]
	v_fma_mix_f32 v245, v12, v12, v245 op_sel:[1,1,0] op_sel_hi:[1,1,0]
	v_fma_mix_f32 v244, v13, 1.0, v244 op_sel_hi:[1,0,0]
	v_fma_mix_f32 v245, v13, v13, v245 op_sel_hi:[1,1,0]
	v_fma_mix_f32 v244, v13, 1.0, v244 op_sel:[1,0,0] op_sel_hi:[1,0,0]
	v_fma_mix_f32 v245, v13, v13, v245 op_sel:[1,1,0] op_sel_hi:[1,1,0]
	v_fma_mix_f32 v244, v14, 1.0, v244 op_sel_hi:[1,0,0]
	v_fma_mix_f32 v245, v14, v14, v245 op_sel_hi:[1,1,0]
	v_fma_mix_f32 v244, v14, 1.0, v244 op_sel:[1,0,0] op_sel_hi:[1,0,0]
	v_fma_mix_f32 v245, v14, v14, v245 op_sel:[1,1,0] op_sel_hi:[1,1,0]
	v_fma_mix_f32 v244, v15, 1.0, v244 op_sel_hi:[1,0,0]
	v_fma_mix_f32 v245, v15, v15, v245 op_sel_hi:[1,1,0]
	v_fma_mix_f32 v244, v15, 1.0, v244 op_sel:[1,0,0] op_sel_hi:[1,0,0]
	v_fma_mix_f32 v245, v15, v15, v245 op_sel:[1,1,0] op_sel_hi:[1,1,0]
	s_waitcnt vmcnt(12)
	v_cvt_f32_f16_e32 v72, v88
	v_cvt_f32_f16_sdwa v73, v88 dst_sel:DWORD dst_unused:UNUSED_PAD src0_sel:WORD_1
	v_cvt_f32_f16_e32 v74, v89
	v_cvt_f32_f16_sdwa v75, v89 dst_sel:DWORD dst_unused:UNUSED_PAD src0_sel:WORD_1
	v_cvt_f32_f16_e32 v80, v90
	v_cvt_f32_f16_sdwa v81, v90 dst_sel:DWORD dst_unused:UNUSED_PAD src0_sel:WORD_1
	v_cvt_f32_f16_e32 v82, v91
	v_cvt_f32_f16_sdwa v83, v91 dst_sel:DWORD dst_unused:UNUSED_PAD src0_sel:WORD_1
	v_sub_f32_e32 v72, v72, v204
	v_sub_f32_e32 v73, v73, v204
	v_sub_f32_e32 v74, v74, v204
	v_sub_f32_e32 v75, v75, v204
	v_sub_f32_e32 v80, v80, v204
	v_sub_f32_e32 v81, v81, v204
	v_sub_f32_e32 v82, v82, v204
	v_sub_f32_e32 v83, v83, v204
	v_pk_mul_f32 v[72:73], v[204:205], v[72:73] op_sel:[1,0]
	v_pk_mul_f32 v[74:75], v[204:205], v[74:75] op_sel:[1,0]
	v_pk_mul_f32 v[80:81], v[204:205], v[80:81] op_sel:[1,0]
	v_pk_mul_f32 v[82:83], v[204:205], v[82:83] op_sel:[1,0]
	v_pk_fma_f32 v[4:5], v[72:73], v[168:169], v[4:5]
	v_pk_fma_f32 v[6:7], v[74:75], v[170:171], v[6:7]
	v_pk_fma_f32 v[0:1], v[80:81], v[172:173], v[0:1]
	v_pk_fma_f32 v[2:3], v[82:83], v[174:175], v[2:3]
	v_cvt_pk_f16_f32 v4, v4, v5
	v_cvt_pk_f16_f32 v5, v6, v7
	v_cvt_pk_f16_f32 v6, v0, v1
	v_cvt_pk_f16_f32 v7, v2, v3
	ds_write_b128 v235, v[4:7] offset:64
	v_fma_mix_f32 v244, v4, 1.0, v244 op_sel_hi:[1,0,0]
	v_fma_mix_f32 v245, v4, v4, v245 op_sel_hi:[1,1,0]
	v_fma_mix_f32 v244, v4, 1.0, v244 op_sel:[1,0,0] op_sel_hi:[1,0,0]
	v_fma_mix_f32 v245, v4, v4, v245 op_sel:[1,1,0] op_sel_hi:[1,1,0]
	v_fma_mix_f32 v244, v5, 1.0, v244 op_sel_hi:[1,0,0]
	v_fma_mix_f32 v245, v5, v5, v245 op_sel_hi:[1,1,0]
	v_fma_mix_f32 v244, v5, 1.0, v244 op_sel:[1,0,0] op_sel_hi:[1,0,0]
	v_fma_mix_f32 v245, v5, v5, v245 op_sel:[1,1,0] op_sel_hi:[1,1,0]
	v_fma_mix_f32 v244, v6, 1.0, v244 op_sel_hi:[1,0,0]
	v_fma_mix_f32 v245, v6, v6, v245 op_sel_hi:[1,1,0]
	v_fma_mix_f32 v244, v6, 1.0, v244 op_sel:[1,0,0] op_sel_hi:[1,0,0]
	v_fma_mix_f32 v245, v6, v6, v245 op_sel:[1,1,0] op_sel_hi:[1,1,0]
	v_fma_mix_f32 v244, v7, 1.0, v244 op_sel_hi:[1,0,0]
	v_fma_mix_f32 v245, v7, v7, v245 op_sel_hi:[1,1,0]
	v_fma_mix_f32 v244, v7, 1.0, v244 op_sel:[1,0,0] op_sel_hi:[1,0,0]
	v_fma_mix_f32 v245, v7, v7, v245 op_sel:[1,1,0] op_sel_hi:[1,1,0]
	ds_read_b128 v[108:111], v236
	ds_read_b128 v[100:103], v236 offset:1152
	s_waitcnt lgkmcnt(0)
	v_add_u32_e32 v83, 0x42000, v224
	buffer_store_dwordx4 v[108:111], v83, s[24:27], 0 offen nt
	v_add_u32_e32 v82, 0x45000, v224
	buffer_store_dwordx4 v[100:103], v82, s[24:27], 0 offen nt
	v_xor_b32_e32 v225, 16, v234
	v_lshlrev_b32_e32 v225, 2, v225
	v_xor_b32_e32 v246, 32, v234
	v_lshlrev_b32_e32 v246, 2, v246
	ds_bpermute_b32 v92, v225, v206
	ds_bpermute_b32 v93, v225, v207
	ds_bpermute_b32 v94, v225, v140
	ds_bpermute_b32 v95, v225, v141
	ds_bpermute_b32 v120, v225, v142
	ds_bpermute_b32 v121, v225, v143
	ds_bpermute_b32 v122, v225, v216
	ds_bpermute_b32 v123, v225, v217
	s_waitcnt lgkmcnt(0)
	v_pk_add_f32 v[206:207], v[206:207], v[92:93]
	v_pk_add_f32 v[140:141], v[140:141], v[94:95]
	v_pk_add_f32 v[142:143], v[142:143], v[120:121]
	v_pk_add_f32 v[216:217], v[216:217], v[122:123]
	ds_bpermute_b32 v92, v225, v218
	ds_bpermute_b32 v93, v225, v219
	ds_bpermute_b32 v94, v225, v208
	ds_bpermute_b32 v95, v225, v209
	ds_bpermute_b32 v120, v225, v210
	ds_bpermute_b32 v121, v225, v211
	ds_bpermute_b32 v122, v225, v244
	ds_bpermute_b32 v123, v225, v245
	s_waitcnt lgkmcnt(0)
	v_pk_add_f32 v[218:219], v[218:219], v[92:93]
	v_pk_add_f32 v[208:209], v[208:209], v[94:95]
	v_pk_add_f32 v[210:211], v[210:211], v[120:121]
	v_pk_add_f32 v[244:245], v[244:245], v[122:123]
	ds_bpermute_b32 v92, v246, v206
	ds_bpermute_b32 v93, v246, v207
	ds_bpermute_b32 v94, v246, v140
	ds_bpermute_b32 v95, v246, v141
	ds_bpermute_b32 v120, v246, v142
	ds_bpermute_b32 v121, v246, v143
	ds_bpermute_b32 v122, v246, v216
	ds_bpermute_b32 v123, v246, v217
	s_waitcnt lgkmcnt(0)
	v_pk_add_f32 v[206:207], v[206:207], v[92:93]
	v_pk_add_f32 v[140:141], v[140:141], v[94:95]
	v_pk_add_f32 v[142:143], v[142:143], v[120:121]
	v_pk_add_f32 v[216:217], v[216:217], v[122:123]
	ds_bpermute_b32 v92, v246, v218
	ds_bpermute_b32 v93, v246, v219
	ds_bpermute_b32 v94, v246, v208
	ds_bpermute_b32 v95, v246, v209
	ds_bpermute_b32 v120, v246, v210
	ds_bpermute_b32 v121, v246, v211
	ds_bpermute_b32 v122, v246, v244
	ds_bpermute_b32 v123, v246, v245
	s_waitcnt lgkmcnt(0)
	v_pk_add_f32 v[218:219], v[218:219], v[92:93]
	v_pk_add_f32 v[208:209], v[208:209], v[94:95]
	v_pk_add_f32 v[210:211], v[210:211], v[120:121]
	v_pk_add_f32 v[244:245], v[244:245], v[122:123]
	s_mov_b64 exec, 0xffff
	global_store_dwordx2 v190, v[206:207], s[100:101] offset:0
	global_store_dwordx2 v190, v[140:141], s[100:101] offset:128
	global_store_dwordx2 v190, v[142:143], s[100:101] offset:256
	global_store_dwordx2 v190, v[216:217], s[100:101] offset:384
	global_store_dwordx2 v190, v[218:219], s[100:101] offset:1024
	global_store_dwordx2 v190, v[208:209], s[100:101] offset:1152
	global_store_dwordx2 v190, v[210:211], s[100:101] offset:1280
	global_store_dwordx2 v190, v[244:245], s[100:101] offset:1408
	s_mov_b64 exec, -1
	s_mov_b32 s83, s81
	s_mov_b32 s84, s82
	s_mov_b64 s[40:41], s[0:1]
	s_mov_b64 s[38:39], s[8:9]
	s_mov_b64 vcc, s[6:7]
	s_cbranch_vccz .LBB10_12
	s_waitcnt vmcnt(0)
	s_cmpk_gt_u32 s44, 0xff
	s_cbranch_scc1 .LBB10_31
	s_barrier

.LBB10_32:
	s_endpgm
	s_endpgm
	s_endpgm
	s_endpgm
	s_endpgm
	s_endpgm
	s_endpgm
	s_endpgm
	s_endpgm
	s_endpgm
	s_endpgm
	s_endpgm
	s_endpgm
	s_endpgm
	s_endpgm
	s_endpgm
	s_endpgm
	s_endpgm
	s_endpgm
	s_endpgm
	s_endpgm
	s_endpgm
	.section	.rodata,"a",@progbits
	.p2align	6, 0x0
